# v6 + lane-permuted (quad-contiguous) GEMM epilogue stores, software-pipelined: wait+store of store k issued at the position of store k+1 so the ds_bpermute latency overlaps the next store's VALU work
# speedup vs baseline: 1.0090x; 1.0019x over previous
.LBB0_174:
	v_mbcnt_lo_u32_b32 v244, -1, 0
	v_mbcnt_hi_u32_b32 v244, -1, v244
	v_lshrrev_b32_e32 v245, 2, v244
	v_and_b32_e32 v244, 3, v244
	v_lshl_add_u32 v244, v244, 4, v245
	v_lshlrev_b32_e32 v244, 2, v244
	s_ashr_i32 s15, s60, 3
	s_add_i32 s62, s15, s75
	s_lshl_b32 s15, s60, 8
	s_and_b32 s15, s15, 0x700
	s_cmp_eq_u32 s62, 0
	v_lshl_add_u32 v174, s28, 8, v1
	s_cselect_b64 s[26:27], -1, 0
	v_or_b32_e32 v82, s15, v209
	s_and_b64 s[26:27], s[50:51], s[26:27]
	v_or_b32_e32 v180, 16, v174
	v_or_b32_e32 v178, 32, v174
	v_or_b32_e32 v176, 48, v174
	s_mov_b64 s[64:65], -1
	s_and_b64 vcc, exec, s[26:27]
	v_lshlrev_b32_e32 v114, 1, v82
	v_ashrrev_i32_e32 v175, 31, v174
	v_ashrrev_i32_e32 v181, 31, v180
	v_ashrrev_i32_e32 v179, 31, v178
	v_ashrrev_i32_e32 v177, 31, v176
	s_cbranch_vccnz .LBB0_177
	v_lshl_add_u32 v158, s14, 10, v210
	ds_read2_b32 v[88:89], v158 offset1:16
	s_ashr_i32 s63, s62, 31
	s_lshl_b64 s[26:27], s[62:63], 25
	s_add_u32 s26, s84, s26
	s_addc_u32 s27, s85, s27
	v_lshl_add_u64 v[90:91], s[26:27], 0, v[114:115]
	v_lshlrev_b64 v[82:83], 12, v[174:175]
	s_waitcnt lgkmcnt(0)
	v_pk_mul_f32 v[84:85], v[144:145], v[88:89] op_sel_hi:[1,0]
	v_lshl_add_u64 v[82:83], v[90:91], 0, v[82:83]
	v_pk_mul_f32 v[86:87], v[146:147], v[88:89] op_sel_hi:[1,0]
	v_cvt_pk_bf16_f32 v84, v84, v85
	v_pk_mul_f32 v[92:93], v[142:143], v[88:89] op_sel_hi:[1,0]
	v_cvt_pk_bf16_f32 v85, v86, v87
	v_pk_mul_f32 v[94:95], v[140:141], v[88:89] op_sel_hi:[1,0]
	v_cvt_pk_bf16_f32 v87, v92, v93
	v_pk_mul_f32 v[92:93], v[134:135], v[88:89] op_sel_hi:[1,0]
	v_cvt_pk_bf16_f32 v86, v94, v95
	ds_bpermute_b32 v232, v244, v84
	ds_bpermute_b32 v233, v244, v85
	ds_bpermute_b32 v234, v244, v86
	ds_bpermute_b32 v235, v244, v87
	ds_bpermute_b32 v236, v244, v82
	ds_bpermute_b32 v237, v244, v83
	v_pk_mul_f32 v[94:95], v[132:133], v[88:89] op_sel_hi:[1,0]
	s_mov_b32 s15, 0x80000
	v_pk_mul_f32 v[84:85], v[136:137], v[88:89] op_sel_hi:[1,0]
	v_pk_mul_f32 v[86:87], v[138:139], v[88:89] op_sel_hi:[1,0]
	v_cvt_pk_bf16_f32 v84, v84, v85
	v_mov_b32_e32 v88, v89
	v_cvt_pk_bf16_f32 v85, v86, v87
	v_cvt_pk_bf16_f32 v86, v94, v95
	v_cvt_pk_bf16_f32 v87, v92, v93
	s_waitcnt lgkmcnt(0)
	global_store_dwordx4 v[236:237], v[232:235], off
	ds_bpermute_b32 v238, v244, v84
	ds_bpermute_b32 v239, v244, v85
	ds_bpermute_b32 v240, v244, v86
	ds_bpermute_b32 v241, v244, v87
	ds_bpermute_b32 v242, v244, v82
	ds_bpermute_b32 v243, v244, v83
	v_pk_mul_f32 v[94:95], v[126:127], v[88:89] op_sel_hi:[1,0]
	v_pk_mul_f32 v[96:97], v[124:125], v[88:89] op_sel_hi:[1,0]
	v_lshlrev_b64 v[84:85], 12, v[180:181]
	v_lshl_add_u64 v[92:93], v[90:91], 0, v[84:85]
	v_pk_mul_f32 v[86:87], v[130:131], v[88:89] op_sel_hi:[1,0]
	v_pk_mul_f32 v[84:85], v[128:129], v[88:89] op_sel_hi:[1,0]
	s_mov_b64 s[16:17], 0x80000
	v_cvt_pk_bf16_f32 v84, v84, v85
	v_cvt_pk_bf16_f32 v85, v86, v87
	v_cvt_pk_bf16_f32 v86, v96, v97
	v_cvt_pk_bf16_f32 v87, v94, v95
	s_waitcnt lgkmcnt(0)
	global_store_dwordx4 v[242:243], v[238:241], off offset:64
	ds_bpermute_b32 v232, v244, v84
	ds_bpermute_b32 v233, v244, v85
	ds_bpermute_b32 v234, v244, v86
	ds_bpermute_b32 v235, v244, v87
	ds_bpermute_b32 v236, v244, v92
	ds_bpermute_b32 v237, v244, v93
	v_pk_mul_f32 v[94:95], v[118:119], v[88:89] op_sel_hi:[1,0]
	s_nop 0
	v_pk_mul_f32 v[86:87], v[122:123], v[88:89] op_sel_hi:[1,0]
	v_pk_mul_f32 v[84:85], v[120:121], v[88:89] op_sel_hi:[1,0]
	v_pk_mul_f32 v[88:89], v[116:117], v[88:89] op_sel_hi:[1,0]
	v_cvt_pk_bf16_f32 v84, v84, v85
	v_cvt_pk_bf16_f32 v85, v86, v87
	v_cvt_pk_bf16_f32 v87, v94, v95
	s_nop 0
	v_cvt_pk_bf16_f32 v86, v88, v89
	ds_read2_b32 v[88:89], v158 offset0:32 offset1:48
	s_waitcnt lgkmcnt(0)
	global_store_dwordx4 v[236:237], v[232:235], off
	ds_bpermute_b32 v238, v244, v84
	ds_bpermute_b32 v239, v244, v85
	ds_bpermute_b32 v240, v244, v86
	ds_bpermute_b32 v241, v244, v87
	ds_bpermute_b32 v242, v244, v92
	ds_bpermute_b32 v243, v244, v93
	s_waitcnt lgkmcnt(0)
	v_pk_mul_f32 v[94:95], v[108:109], v[88:89] op_sel_hi:[1,0]
	v_lshlrev_b64 v[84:85], 12, v[178:179]
	v_lshl_add_u64 v[92:93], v[90:91], 0, v[84:85]
	v_pk_mul_f32 v[84:85], v[110:111], v[88:89] op_sel_hi:[1,0]
	v_pk_mul_f32 v[86:87], v[112:113], v[88:89] op_sel_hi:[1,0]
	v_cvt_pk_bf16_f32 v84, v84, v85
	v_pk_mul_f32 v[96:97], v[106:107], v[88:89] op_sel_hi:[1,0]
	v_cvt_pk_bf16_f32 v85, v86, v87
	v_cvt_pk_bf16_f32 v87, v94, v95
	v_pk_mul_f32 v[94:95], v[100:101], v[88:89] op_sel_hi:[1,0]
	v_cvt_pk_bf16_f32 v86, v96, v97
	s_waitcnt lgkmcnt(0)
	global_store_dwordx4 v[242:243], v[238:241], off offset:64
	ds_bpermute_b32 v232, v244, v84
	ds_bpermute_b32 v233, v244, v85
	ds_bpermute_b32 v234, v244, v86
	ds_bpermute_b32 v235, v244, v87
	ds_bpermute_b32 v236, v244, v92
	ds_bpermute_b32 v237, v244, v93
	v_pk_mul_f32 v[96:97], v[98:99], v[88:89] op_sel_hi:[1,0]
	s_nop 0
	v_pk_mul_f32 v[84:85], v[102:103], v[88:89] op_sel_hi:[1,0]
	v_pk_mul_f32 v[86:87], v[104:105], v[88:89] op_sel_hi:[1,0]
	v_cvt_pk_bf16_f32 v84, v84, v85
	v_mov_b32_e32 v88, v89
	v_cvt_pk_bf16_f32 v85, v86, v87
	v_cvt_pk_bf16_f32 v86, v96, v97
	v_cvt_pk_bf16_f32 v87, v94, v95
	s_waitcnt lgkmcnt(0)
	global_store_dwordx4 v[236:237], v[232:235], off
	ds_bpermute_b32 v238, v244, v84
	ds_bpermute_b32 v239, v244, v85
	ds_bpermute_b32 v240, v244, v86
	ds_bpermute_b32 v241, v244, v87
	ds_bpermute_b32 v242, v244, v92
	ds_bpermute_b32 v243, v244, v93
	v_pk_mul_f32 v[94:95], v[74:75], v[88:89] op_sel_hi:[1,0]
	v_pk_mul_f32 v[92:93], v[76:77], v[88:89] op_sel_hi:[1,0]
	v_lshlrev_b64 v[84:85], 12, v[176:177]
	v_lshl_add_u64 v[90:91], v[90:91], 0, v[84:85]
	v_pk_mul_f32 v[86:87], v[80:81], v[88:89] op_sel_hi:[1,0]
	v_pk_mul_f32 v[84:85], v[78:79], v[88:89] op_sel_hi:[1,0]
	s_nop 0
	v_cvt_pk_bf16_f32 v84, v84, v85
	v_cvt_pk_bf16_f32 v85, v86, v87
	v_cvt_pk_bf16_f32 v86, v94, v95
	ds_read2_b32 v[94:95], v158 offset0:128 offset1:144
	v_cvt_pk_bf16_f32 v87, v92, v93
	s_waitcnt lgkmcnt(0)
	global_store_dwordx4 v[242:243], v[238:241], off offset:64
	ds_bpermute_b32 v232, v244, v84
	ds_bpermute_b32 v233, v244, v85
	ds_bpermute_b32 v234, v244, v86
	ds_bpermute_b32 v235, v244, v87
	ds_bpermute_b32 v236, v244, v90
	ds_bpermute_b32 v237, v244, v91
	v_pk_mul_f32 v[92:93], v[68:69], v[88:89] op_sel_hi:[1,0]
	s_nop 0
	v_pk_mul_f32 v[86:87], v[72:73], v[88:89] op_sel_hi:[1,0]
	v_pk_mul_f32 v[84:85], v[70:71], v[88:89] op_sel_hi:[1,0]
	v_pk_mul_f32 v[88:89], v[66:67], v[88:89] op_sel_hi:[1,0]
	v_cvt_pk_bf16_f32 v84, v84, v85
	v_cvt_pk_bf16_f32 v85, v86, v87
	v_cvt_pk_bf16_f32 v87, v92, v93
	s_waitcnt lgkmcnt(0)
	v_pk_mul_f32 v[92:93], v[58:59], v[94:95] op_sel_hi:[1,0]
	v_cvt_pk_bf16_f32 v86, v88, v89
	s_waitcnt lgkmcnt(0)
	global_store_dwordx4 v[236:237], v[232:235], off
	ds_bpermute_b32 v238, v244, v84
	ds_bpermute_b32 v239, v244, v85
	ds_bpermute_b32 v240, v244, v86
	ds_bpermute_b32 v241, v244, v87
	ds_bpermute_b32 v242, v244, v90
	ds_bpermute_b32 v243, v244, v91
	v_pk_mul_f32 v[90:91], v[60:61], v[94:95] op_sel_hi:[1,0]
	v_lshl_add_u64 v[88:89], v[82:83], 0, s[16:17]
	v_pk_mul_f32 v[86:87], v[64:65], v[94:95] op_sel_hi:[1,0]
	v_pk_mul_f32 v[84:85], v[62:63], v[94:95] op_sel_hi:[1,0]
	s_mov_b64 s[16:17], 0x90000
	v_cvt_pk_bf16_f32 v84, v84, v85
	v_cvt_pk_bf16_f32 v85, v86, v87
	v_cvt_pk_bf16_f32 v87, v90, v91
	v_add_co_u32_e32 v90, vcc, s15, v82
	v_cvt_pk_bf16_f32 v86, v92, v93
	v_pk_mul_f32 v[92:93], v[50:51], v[94:95] op_sel_hi:[1,0]
	s_nop 0
	v_addc_co_u32_e32 v91, vcc, 0, v83, vcc
	s_waitcnt lgkmcnt(0)
	global_store_dwordx4 v[242:243], v[238:241], off offset:64
	ds_bpermute_b32 v232, v244, v84
	ds_bpermute_b32 v233, v244, v85
	ds_bpermute_b32 v234, v244, v86
	ds_bpermute_b32 v235, v244, v87
	ds_bpermute_b32 v236, v244, v90
	ds_bpermute_b32 v237, v244, v91
	v_pk_mul_f32 v[90:91], v[52:53], v[94:95] op_sel_hi:[1,0]
	s_mov_b32 s15, 0x90000
	v_pk_mul_f32 v[86:87], v[56:57], v[94:95] op_sel_hi:[1,0]
	v_pk_mul_f32 v[84:85], v[54:55], v[94:95] op_sel_hi:[1,0]
	s_nop 0
	v_cvt_pk_bf16_f32 v84, v84, v85
	v_cvt_pk_bf16_f32 v85, v86, v87
	v_cvt_pk_bf16_f32 v86, v92, v93
	v_cvt_pk_bf16_f32 v87, v90, v91
	v_mov_b32_e32 v90, v95
	s_waitcnt lgkmcnt(0)
	global_store_dwordx4 v[236:237], v[232:235], off
	ds_bpermute_b32 v238, v244, v84
	ds_bpermute_b32 v239, v244, v85
	ds_bpermute_b32 v240, v244, v86
	ds_bpermute_b32 v241, v244, v87
	ds_bpermute_b32 v242, v244, v88
	ds_bpermute_b32 v243, v244, v89
	v_pk_mul_f32 v[94:95], v[42:43], v[90:91] op_sel_hi:[1,0]
	v_pk_mul_f32 v[92:93], v[44:45], v[90:91] op_sel_hi:[1,0]
	v_pk_mul_f32 v[86:87], v[48:49], v[90:91] op_sel_hi:[1,0]
	v_pk_mul_f32 v[84:85], v[46:47], v[90:91] op_sel_hi:[1,0]
	v_lshl_add_u64 v[88:89], v[82:83], 0, s[16:17]
	v_cvt_pk_bf16_f32 v84, v84, v85
	v_cvt_pk_bf16_f32 v85, v86, v87
	v_cvt_pk_bf16_f32 v86, v94, v95
	ds_read2_b32 v[94:95], v158 offset0:160 offset1:176
	v_cvt_pk_bf16_f32 v87, v92, v93
	v_add_co_u32_e32 v92, vcc, s15, v82
	s_mov_b32 s15, 0xa0000
	s_nop 0
	v_addc_co_u32_e32 v93, vcc, 0, v83, vcc
	s_waitcnt lgkmcnt(0)
	global_store_dwordx4 v[242:243], v[238:241], off offset:64
	ds_bpermute_b32 v232, v244, v84
	ds_bpermute_b32 v233, v244, v85
	ds_bpermute_b32 v234, v244, v86
	ds_bpermute_b32 v235, v244, v87
	ds_bpermute_b32 v236, v244, v92
	ds_bpermute_b32 v237, v244, v93
	v_pk_mul_f32 v[92:93], v[36:37], v[90:91] op_sel_hi:[1,0]
	s_mov_b64 s[16:17], 0xa0000
	v_pk_mul_f32 v[86:87], v[40:41], v[90:91] op_sel_hi:[1,0]
	v_pk_mul_f32 v[84:85], v[38:39], v[90:91] op_sel_hi:[1,0]
	v_pk_mul_f32 v[90:91], v[34:35], v[90:91] op_sel_hi:[1,0]
	v_cvt_pk_bf16_f32 v84, v84, v85
	v_cvt_pk_bf16_f32 v85, v86, v87
	v_cvt_pk_bf16_f32 v87, v92, v93
	s_waitcnt lgkmcnt(0)
	v_pk_mul_f32 v[92:93], v[26:27], v[94:95] op_sel_hi:[1,0]
	v_cvt_pk_bf16_f32 v86, v90, v91
	s_waitcnt lgkmcnt(0)
	global_store_dwordx4 v[236:237], v[232:235], off
	ds_bpermute_b32 v238, v244, v84
	ds_bpermute_b32 v239, v244, v85
	ds_bpermute_b32 v240, v244, v86
	ds_bpermute_b32 v241, v244, v87
	ds_bpermute_b32 v242, v244, v88
	ds_bpermute_b32 v243, v244, v89
	v_pk_mul_f32 v[90:91], v[28:29], v[94:95] op_sel_hi:[1,0]
	v_lshl_add_u64 v[88:89], v[82:83], 0, s[16:17]
	v_pk_mul_f32 v[86:87], v[32:33], v[94:95] op_sel_hi:[1,0]
	v_pk_mul_f32 v[84:85], v[30:31], v[94:95] op_sel_hi:[1,0]
	s_mov_b64 s[16:17], 0xb0000
	v_cvt_pk_bf16_f32 v84, v84, v85
	v_cvt_pk_bf16_f32 v85, v86, v87
	v_cvt_pk_bf16_f32 v87, v90, v91
	v_add_co_u32_e32 v90, vcc, s15, v82
	v_cvt_pk_bf16_f32 v86, v92, v93
	s_mov_b32 s15, 0xb0000
	s_nop 0
	v_addc_co_u32_e32 v91, vcc, 0, v83, vcc
	s_waitcnt lgkmcnt(0)
	global_store_dwordx4 v[242:243], v[238:241], off offset:64
	ds_bpermute_b32 v232, v244, v84
	ds_bpermute_b32 v233, v244, v85
	ds_bpermute_b32 v234, v244, v86
	ds_bpermute_b32 v235, v244, v87
	ds_bpermute_b32 v236, v244, v90
	ds_bpermute_b32 v237, v244, v91
	v_pk_mul_f32 v[90:91], v[20:21], v[94:95] op_sel_hi:[1,0]
	v_pk_mul_f32 v[92:93], v[18:19], v[94:95] op_sel_hi:[1,0]
	v_pk_mul_f32 v[86:87], v[24:25], v[94:95] op_sel_hi:[1,0]
	v_pk_mul_f32 v[84:85], v[22:23], v[94:95] op_sel_hi:[1,0]
	s_nop 0
	v_cvt_pk_bf16_f32 v84, v84, v85
	v_cvt_pk_bf16_f32 v85, v86, v87
	v_cvt_pk_bf16_f32 v87, v90, v91
	v_mov_b32_e32 v90, v95
	v_cvt_pk_bf16_f32 v86, v92, v93
	s_waitcnt lgkmcnt(0)
	global_store_dwordx4 v[236:237], v[232:235], off
	ds_bpermute_b32 v238, v244, v84
	ds_bpermute_b32 v239, v244, v85
	ds_bpermute_b32 v240, v244, v86
	ds_bpermute_b32 v241, v244, v87
	ds_bpermute_b32 v242, v244, v88
	ds_bpermute_b32 v243, v244, v89
	v_lshl_add_u64 v[88:89], v[82:83], 0, s[16:17]
	v_add_co_u32_e32 v82, vcc, s15, v82
	v_pk_mul_f32 v[84:85], v[14:15], v[90:91] op_sel_hi:[1,0]
	v_pk_mul_f32 v[86:87], v[16:17], v[90:91] op_sel_hi:[1,0]
	v_cvt_pk_bf16_f32 v84, v84, v85
	v_addc_co_u32_e32 v83, vcc, 0, v83, vcc
	v_cvt_pk_bf16_f32 v85, v86, v87
	v_pk_mul_f32 v[92:93], v[12:13], v[90:91] op_sel_hi:[1,0]
	v_pk_mul_f32 v[94:95], v[10:11], v[90:91] op_sel_hi:[1,0]
	v_cvt_pk_bf16_f32 v87, v92, v93
	s_nop 0
	v_cvt_pk_bf16_f32 v86, v94, v95
	s_waitcnt lgkmcnt(0)
	global_store_dwordx4 v[242:243], v[238:241], off offset:64
	ds_bpermute_b32 v232, v244, v84
	ds_bpermute_b32 v233, v244, v85
	ds_bpermute_b32 v234, v244, v86
	ds_bpermute_b32 v235, v244, v87
	ds_bpermute_b32 v236, v244, v82
	ds_bpermute_b32 v237, v244, v83
	v_pk_mul_f32 v[82:83], v[6:7], v[90:91] op_sel_hi:[1,0]
	s_nop 0
	v_pk_mul_f32 v[84:85], v[8:9], v[90:91] op_sel_hi:[1,0]
	v_pk_mul_f32 v[86:87], v[4:5], v[90:91] op_sel_hi:[1,0]
	v_pk_mul_f32 v[90:91], v[2:3], v[90:91] op_sel_hi:[1,0]
	v_cvt_pk_bf16_f32 v82, v82, v83
	v_cvt_pk_bf16_f32 v83, v84, v85
	v_cvt_pk_bf16_f32 v85, v86, v87
	s_nop 0
	v_cvt_pk_bf16_f32 v84, v90, v91
	s_waitcnt lgkmcnt(0)
	global_store_dwordx4 v[236:237], v[232:235], off
	ds_bpermute_b32 v238, v244, v82
	ds_bpermute_b32 v239, v244, v83
	ds_bpermute_b32 v240, v244, v84
	ds_bpermute_b32 v241, v244, v85
	ds_bpermute_b32 v242, v244, v88
	ds_bpermute_b32 v243, v244, v89
	s_waitcnt lgkmcnt(0)
	global_store_dwordx4 v[242:243], v[238:241], off offset:64
	s_cbranch_execz .LBB0_178

.LBB0_178:
	s_lshl_b32 s14, s14, 10
	v_add_u32_e32 v213, s14, v211
	ds_read_b32 v82, v213
	s_waitcnt lgkmcnt(0)
	v_pk_mul_f32 v[84:85], v[146:147], v[82:83] op_sel_hi:[1,0]
	v_pk_mul_f32 v[86:87], v[144:145], v[82:83] op_sel_hi:[1,0]
	v_pk_mul_f32 v[84:85], v[84:85], v[84:85]
	v_pk_mul_f32 v[88:89], v[140:141], v[82:83] op_sel_hi:[1,0]
	v_pk_fma_f32 v[84:85], v[86:87], v[86:87], v[84:85]
	v_pk_mul_f32 v[86:87], v[142:143], v[82:83] op_sel_hi:[1,0]
	s_nop 0
	v_pk_mul_f32 v[86:87], v[86:87], v[86:87]
	s_nop 0
	v_pk_fma_f32 v[86:87], v[88:89], v[88:89], v[86:87]
	v_pk_mul_f32 v[88:89], v[136:137], v[82:83] op_sel_hi:[1,0]
	v_pk_add_f32 v[84:85], v[84:85], v[86:87]
	v_pk_mul_f32 v[86:87], v[138:139], v[82:83] op_sel_hi:[1,0]
	s_nop 0
	v_pk_mul_f32 v[86:87], v[86:87], v[86:87]
	s_nop 0
	v_pk_fma_f32 v[86:87], v[88:89], v[88:89], v[86:87]
	s_nop 0
	v_pk_add_f32 v[84:85], v[86:87], v[84:85]
	v_pk_mul_f32 v[86:87], v[134:135], v[82:83] op_sel_hi:[1,0]
	v_pk_mul_f32 v[82:83], v[132:133], v[82:83] op_sel_hi:[1,0]
	v_pk_mul_f32 v[86:87], v[86:87], v[86:87]
	s_nop 0
	v_pk_fma_f32 v[82:83], v[82:83], v[82:83], v[86:87]
	s_nop 0
	v_pk_add_f32 v[82:83], v[82:83], v[84:85]
	s_nop 0
	v_add_f32_e32 v82, v82, v83
	ds_swizzle_b32 v83, v82 offset:swizzle(SWAP,16)
	s_waitcnt lgkmcnt(0)
	v_add_f32_e32 v82, v82, v83
	v_mov_b32_e32 v83, v82
	s_nop 1
	v_permlane32_swap_b32_e32 v82, v83
	s_and_saveexec_b64 s[62:63], s[38:39]
	v_add_f32_e32 v82, v82, v83
	ds_write_b32 v183, v82
	s_or_b64 exec, exec, s[62:63]
	ds_read_b32 v82, v213 offset:64
	s_waitcnt lgkmcnt(0)
	v_pk_mul_f32 v[84:85], v[130:131], v[82:83] op_sel_hi:[1,0]
	v_pk_mul_f32 v[86:87], v[128:129], v[82:83] op_sel_hi:[1,0]
	v_pk_mul_f32 v[84:85], v[84:85], v[84:85]
	v_pk_mul_f32 v[88:89], v[124:125], v[82:83] op_sel_hi:[1,0]
	v_pk_fma_f32 v[84:85], v[86:87], v[86:87], v[84:85]
	v_pk_mul_f32 v[86:87], v[126:127], v[82:83] op_sel_hi:[1,0]
	s_nop 0
	v_pk_mul_f32 v[86:87], v[86:87], v[86:87]
	s_nop 0
	v_pk_fma_f32 v[86:87], v[88:89], v[88:89], v[86:87]
	v_pk_mul_f32 v[88:89], v[120:121], v[82:83] op_sel_hi:[1,0]
	v_pk_add_f32 v[84:85], v[84:85], v[86:87]
	v_pk_mul_f32 v[86:87], v[122:123], v[82:83] op_sel_hi:[1,0]
	s_nop 0
	v_pk_mul_f32 v[86:87], v[86:87], v[86:87]
	s_nop 0
	v_pk_fma_f32 v[86:87], v[88:89], v[88:89], v[86:87]
	s_nop 0
	v_pk_add_f32 v[84:85], v[86:87], v[84:85]
	v_pk_mul_f32 v[86:87], v[118:119], v[82:83] op_sel_hi:[1,0]
	v_pk_mul_f32 v[82:83], v[116:117], v[82:83] op_sel_hi:[1,0]
	v_pk_mul_f32 v[86:87], v[86:87], v[86:87]
	s_nop 0
	v_pk_fma_f32 v[82:83], v[82:83], v[82:83], v[86:87]
	s_nop 0
	v_pk_add_f32 v[82:83], v[82:83], v[84:85]
	s_nop 0
	v_add_f32_e32 v82, v82, v83
	ds_swizzle_b32 v83, v82 offset:swizzle(SWAP,16)
	s_waitcnt lgkmcnt(0)
	v_add_f32_e32 v82, v82, v83
	v_mov_b32_e32 v83, v82
	s_nop 1
	v_permlane32_swap_b32_e32 v82, v83
	s_and_saveexec_b64 s[62:63], s[38:39]
	v_add_f32_e32 v82, v82, v83
	ds_write_b32 v195, v82
	s_or_b64 exec, exec, s[62:63]
	ds_read_b32 v82, v213 offset:128
	s_waitcnt lgkmcnt(0)
	v_pk_mul_f32 v[84:85], v[112:113], v[82:83] op_sel_hi:[1,0]
	v_pk_mul_f32 v[86:87], v[110:111], v[82:83] op_sel_hi:[1,0]
	v_pk_mul_f32 v[84:85], v[84:85], v[84:85]
	v_pk_mul_f32 v[88:89], v[106:107], v[82:83] op_sel_hi:[1,0]
	v_pk_fma_f32 v[84:85], v[86:87], v[86:87], v[84:85]
	v_pk_mul_f32 v[86:87], v[108:109], v[82:83] op_sel_hi:[1,0]
	s_nop 0
	v_pk_mul_f32 v[86:87], v[86:87], v[86:87]
	s_nop 0
	v_pk_fma_f32 v[86:87], v[88:89], v[88:89], v[86:87]
	v_pk_mul_f32 v[88:89], v[102:103], v[82:83] op_sel_hi:[1,0]
	v_pk_add_f32 v[84:85], v[84:85], v[86:87]
	v_pk_mul_f32 v[86:87], v[104:105], v[82:83] op_sel_hi:[1,0]
	s_nop 0
	v_pk_mul_f32 v[86:87], v[86:87], v[86:87]
	s_nop 0
	v_pk_fma_f32 v[86:87], v[88:89], v[88:89], v[86:87]
	s_nop 0
	v_pk_add_f32 v[84:85], v[86:87], v[84:85]
	v_pk_mul_f32 v[86:87], v[100:101], v[82:83] op_sel_hi:[1,0]
	v_pk_mul_f32 v[82:83], v[98:99], v[82:83] op_sel_hi:[1,0]
	v_pk_mul_f32 v[86:87], v[86:87], v[86:87]
	s_nop 0
	v_pk_fma_f32 v[82:83], v[82:83], v[82:83], v[86:87]
	s_nop 0
	v_pk_add_f32 v[82:83], v[82:83], v[84:85]
	s_nop 0
	v_add_f32_e32 v82, v82, v83
	ds_swizzle_b32 v83, v82 offset:swizzle(SWAP,16)
	s_waitcnt lgkmcnt(0)
	v_add_f32_e32 v82, v82, v83
	v_mov_b32_e32 v83, v82
	s_nop 1
	v_permlane32_swap_b32_e32 v82, v83
	s_and_saveexec_b64 s[62:63], s[38:39]
	v_add_f32_e32 v82, v82, v83
	ds_write_b32 v197, v82
	s_or_b64 exec, exec, s[62:63]
	ds_read_b32 v82, v213 offset:192
	s_waitcnt lgkmcnt(0)
	v_pk_mul_f32 v[84:85], v[80:81], v[82:83] op_sel_hi:[1,0]
	v_pk_mul_f32 v[86:87], v[78:79], v[82:83] op_sel_hi:[1,0]
	v_pk_mul_f32 v[84:85], v[84:85], v[84:85]
	v_pk_mul_f32 v[88:89], v[74:75], v[82:83] op_sel_hi:[1,0]
	v_pk_fma_f32 v[84:85], v[86:87], v[86:87], v[84:85]
	v_pk_mul_f32 v[86:87], v[76:77], v[82:83] op_sel_hi:[1,0]
	s_nop 0
	v_pk_mul_f32 v[86:87], v[86:87], v[86:87]
	s_nop 0
	v_pk_fma_f32 v[86:87], v[88:89], v[88:89], v[86:87]
	v_pk_mul_f32 v[88:89], v[70:71], v[82:83] op_sel_hi:[1,0]
	v_pk_add_f32 v[84:85], v[84:85], v[86:87]
	v_pk_mul_f32 v[86:87], v[72:73], v[82:83] op_sel_hi:[1,0]
	s_nop 0
	v_pk_mul_f32 v[86:87], v[86:87], v[86:87]
	s_nop 0
	v_pk_fma_f32 v[86:87], v[88:89], v[88:89], v[86:87]
	s_nop 0
	v_pk_add_f32 v[84:85], v[86:87], v[84:85]
	v_pk_mul_f32 v[86:87], v[68:69], v[82:83] op_sel_hi:[1,0]
	v_pk_mul_f32 v[82:83], v[66:67], v[82:83] op_sel_hi:[1,0]
	v_pk_mul_f32 v[86:87], v[86:87], v[86:87]
	s_nop 0
	v_pk_fma_f32 v[82:83], v[82:83], v[82:83], v[86:87]
	s_nop 0
	v_pk_add_f32 v[82:83], v[82:83], v[84:85]
	s_nop 0
	v_add_f32_e32 v82, v82, v83
	ds_swizzle_b32 v83, v82 offset:swizzle(SWAP,16)
	s_waitcnt lgkmcnt(0)
	v_add_f32_e32 v82, v82, v83
	v_mov_b32_e32 v83, v82
	s_nop 1
	v_permlane32_swap_b32_e32 v82, v83
	s_and_saveexec_b64 s[62:63], s[38:39]
	v_add_f32_e32 v82, v82, v83
	ds_write_b32 v199, v82
	s_or_b64 exec, exec, s[62:63]
	ds_read_b32 v82, v213 offset:512
	s_waitcnt lgkmcnt(0)
	v_pk_mul_f32 v[84:85], v[64:65], v[82:83] op_sel_hi:[1,0]
	v_pk_mul_f32 v[86:87], v[62:63], v[82:83] op_sel_hi:[1,0]
	v_pk_mul_f32 v[84:85], v[84:85], v[84:85]
	v_pk_mul_f32 v[88:89], v[58:59], v[82:83] op_sel_hi:[1,0]
	v_pk_fma_f32 v[84:85], v[86:87], v[86:87], v[84:85]
	v_pk_mul_f32 v[86:87], v[60:61], v[82:83] op_sel_hi:[1,0]
	s_nop 0
	v_pk_mul_f32 v[86:87], v[86:87], v[86:87]
	s_nop 0
	v_pk_fma_f32 v[86:87], v[88:89], v[88:89], v[86:87]
	v_pk_mul_f32 v[88:89], v[54:55], v[82:83] op_sel_hi:[1,0]
	v_pk_add_f32 v[84:85], v[84:85], v[86:87]
	v_pk_mul_f32 v[86:87], v[56:57], v[82:83] op_sel_hi:[1,0]
	s_nop 0
	v_pk_mul_f32 v[86:87], v[86:87], v[86:87]
	s_nop 0
	v_pk_fma_f32 v[86:87], v[88:89], v[88:89], v[86:87]
	s_nop 0
	v_pk_add_f32 v[84:85], v[86:87], v[84:85]
	v_pk_mul_f32 v[86:87], v[52:53], v[82:83] op_sel_hi:[1,0]
	v_pk_mul_f32 v[82:83], v[50:51], v[82:83] op_sel_hi:[1,0]
	v_pk_mul_f32 v[86:87], v[86:87], v[86:87]
	s_nop 0
	v_pk_fma_f32 v[82:83], v[82:83], v[82:83], v[86:87]
	s_nop 0
	v_pk_add_f32 v[82:83], v[82:83], v[84:85]
	s_nop 0
	v_add_f32_e32 v82, v82, v83
	ds_swizzle_b32 v83, v82 offset:swizzle(SWAP,16)
	s_waitcnt lgkmcnt(0)
	v_add_f32_e32 v82, v82, v83
	v_mov_b32_e32 v83, v82
	s_nop 1
	v_permlane32_swap_b32_e32 v82, v83
	s_and_saveexec_b64 s[62:63], s[38:39]
	v_add_f32_e32 v82, v82, v83
	ds_write_b32 v201, v82
	s_or_b64 exec, exec, s[62:63]
	ds_read_b32 v82, v213 offset:576
	s_waitcnt lgkmcnt(0)
	v_pk_mul_f32 v[84:85], v[48:49], v[82:83] op_sel_hi:[1,0]
	v_pk_mul_f32 v[86:87], v[46:47], v[82:83] op_sel_hi:[1,0]
	v_pk_mul_f32 v[84:85], v[84:85], v[84:85]
	v_pk_mul_f32 v[88:89], v[42:43], v[82:83] op_sel_hi:[1,0]
	v_pk_fma_f32 v[84:85], v[86:87], v[86:87], v[84:85]
	v_pk_mul_f32 v[86:87], v[44:45], v[82:83] op_sel_hi:[1,0]
	s_nop 0
	v_pk_mul_f32 v[86:87], v[86:87], v[86:87]
	s_nop 0
	v_pk_fma_f32 v[86:87], v[88:89], v[88:89], v[86:87]
	v_pk_mul_f32 v[88:89], v[38:39], v[82:83] op_sel_hi:[1,0]
	v_pk_add_f32 v[84:85], v[84:85], v[86:87]
	v_pk_mul_f32 v[86:87], v[40:41], v[82:83] op_sel_hi:[1,0]
	s_nop 0
	v_pk_mul_f32 v[86:87], v[86:87], v[86:87]
	s_nop 0
	v_pk_fma_f32 v[86:87], v[88:89], v[88:89], v[86:87]
	s_nop 0
	v_pk_add_f32 v[84:85], v[86:87], v[84:85]
	v_pk_mul_f32 v[86:87], v[36:37], v[82:83] op_sel_hi:[1,0]
	v_pk_mul_f32 v[82:83], v[34:35], v[82:83] op_sel_hi:[1,0]
	v_pk_mul_f32 v[86:87], v[86:87], v[86:87]
	s_nop 0
	v_pk_fma_f32 v[82:83], v[82:83], v[82:83], v[86:87]
	s_nop 0
	v_pk_add_f32 v[82:83], v[82:83], v[84:85]
	s_nop 0
	v_add_f32_e32 v82, v82, v83
	ds_swizzle_b32 v83, v82 offset:swizzle(SWAP,16)
	s_waitcnt lgkmcnt(0)
	v_add_f32_e32 v82, v82, v83
	v_mov_b32_e32 v83, v82
	s_nop 1
	v_permlane32_swap_b32_e32 v82, v83
	s_and_saveexec_b64 s[62:63], s[38:39]
	v_add_f32_e32 v82, v82, v83
	ds_write_b32 v203, v82
	s_or_b64 exec, exec, s[62:63]
	ds_read_b32 v82, v213 offset:640
	s_waitcnt lgkmcnt(0)
	v_pk_mul_f32 v[84:85], v[32:33], v[82:83] op_sel_hi:[1,0]
	v_pk_mul_f32 v[86:87], v[30:31], v[82:83] op_sel_hi:[1,0]
	v_pk_mul_f32 v[84:85], v[84:85], v[84:85]
	v_pk_mul_f32 v[88:89], v[26:27], v[82:83] op_sel_hi:[1,0]
	v_pk_fma_f32 v[84:85], v[86:87], v[86:87], v[84:85]
	v_pk_mul_f32 v[86:87], v[28:29], v[82:83] op_sel_hi:[1,0]
	s_nop 0
	v_pk_mul_f32 v[86:87], v[86:87], v[86:87]
	s_nop 0
	v_pk_fma_f32 v[86:87], v[88:89], v[88:89], v[86:87]
	v_pk_mul_f32 v[88:89], v[22:23], v[82:83] op_sel_hi:[1,0]
	v_pk_add_f32 v[84:85], v[84:85], v[86:87]
	v_pk_mul_f32 v[86:87], v[24:25], v[82:83] op_sel_hi:[1,0]
	s_nop 0
	v_pk_mul_f32 v[86:87], v[86:87], v[86:87]
	s_nop 0
	v_pk_fma_f32 v[86:87], v[88:89], v[88:89], v[86:87]
	s_nop 0
	v_pk_add_f32 v[84:85], v[86:87], v[84:85]
	v_pk_mul_f32 v[86:87], v[20:21], v[82:83] op_sel_hi:[1,0]
	v_pk_mul_f32 v[82:83], v[18:19], v[82:83] op_sel_hi:[1,0]
	v_pk_mul_f32 v[86:87], v[86:87], v[86:87]
	s_nop 0
	v_pk_fma_f32 v[82:83], v[82:83], v[82:83], v[86:87]
	s_nop 0
	v_pk_add_f32 v[82:83], v[82:83], v[84:85]
	s_nop 0
	v_add_f32_e32 v82, v82, v83
	ds_swizzle_b32 v83, v82 offset:swizzle(SWAP,16)
	s_waitcnt lgkmcnt(0)
	v_add_f32_e32 v82, v82, v83
	v_mov_b32_e32 v83, v82
	s_nop 1
	v_permlane32_swap_b32_e32 v82, v83
	s_and_saveexec_b64 s[62:63], s[38:39]
	v_add_f32_e32 v82, v82, v83
	ds_write_b32 v205, v82
	s_or_b64 exec, exec, s[62:63]
	ds_read_b32 v82, v213 offset:704
	s_waitcnt lgkmcnt(0)
	v_pk_mul_f32 v[84:85], v[16:17], v[82:83] op_sel_hi:[1,0]
	v_pk_mul_f32 v[86:87], v[14:15], v[82:83] op_sel_hi:[1,0]
	v_pk_mul_f32 v[84:85], v[84:85], v[84:85]
	v_pk_mul_f32 v[88:89], v[10:11], v[82:83] op_sel_hi:[1,0]
	v_pk_fma_f32 v[84:85], v[86:87], v[86:87], v[84:85]
	v_pk_mul_f32 v[86:87], v[12:13], v[82:83] op_sel_hi:[1,0]
	s_nop 0
	v_pk_mul_f32 v[86:87], v[86:87], v[86:87]
	s_nop 0
	v_pk_fma_f32 v[86:87], v[88:89], v[88:89], v[86:87]
	v_pk_mul_f32 v[88:89], v[6:7], v[82:83] op_sel_hi:[1,0]
	v_pk_add_f32 v[84:85], v[84:85], v[86:87]
	v_pk_mul_f32 v[86:87], v[8:9], v[82:83] op_sel_hi:[1,0]
	s_nop 0
	v_pk_mul_f32 v[86:87], v[86:87], v[86:87]
	s_nop 0
	v_pk_fma_f32 v[86:87], v[88:89], v[88:89], v[86:87]
	s_nop 0
	v_pk_add_f32 v[84:85], v[86:87], v[84:85]
	v_pk_mul_f32 v[86:87], v[4:5], v[82:83] op_sel_hi:[1,0]
	v_pk_mul_f32 v[82:83], v[2:3], v[82:83] op_sel_hi:[1,0]
	v_pk_mul_f32 v[86:87], v[86:87], v[86:87]
	s_nop 0
	v_pk_fma_f32 v[82:83], v[82:83], v[82:83], v[86:87]
	s_nop 0
	v_pk_add_f32 v[82:83], v[82:83], v[84:85]
	s_nop 0
	v_add_f32_e32 v82, v82, v83
	ds_swizzle_b32 v83, v82 offset:swizzle(SWAP,16)
	s_waitcnt lgkmcnt(0)
	v_add_f32_e32 v82, v82, v83
	v_mov_b32_e32 v83, v82
	s_nop 1
	v_permlane32_swap_b32_e32 v82, v83
	s_and_saveexec_b64 s[62:63], s[38:39]
	v_add_f32_e32 v82, v82, v83
	ds_write_b32 v207, v82
	s_or_b64 exec, exec, s[62:63]
	s_waitcnt lgkmcnt(0)
	s_barrier
	global_load_dwordx4 v[94:97], v[168:169], off offset:16
	global_load_dwordx4 v[90:93], v[168:169], off
	global_load_dwordx4 v[82:85], v[168:169], off offset:144
	global_load_dwordx4 v[86:89], v[168:169], off offset:128
	ds_read_b32 v158, v183
	ds_read_b32 v159, v194
	s_lshl_b32 s14, s60, 1
	s_and_b32 s14, s14, 14
	s_lshl_b32 s15, s28, 1
	s_or_b32 s14, s88, s14
	s_waitcnt lgkmcnt(0)
	v_add_f32_e32 v158, v158, v159
	v_fmamk_f32 v158, v158, 0x3c000000, v185
	v_rsq_f32_e32 v160, v158
	ds_read2_b32 v[158:159], v213 offset1:16
	s_and_b32 s15, s15, 0x7fffff0
	s_or_b32 s14, s15, s14
	s_lshl_b32 s15, s28, 2
	s_and_b32 s15, s15, 28
	s_waitcnt lgkmcnt(0)
	v_mul_f32_e32 v158, v158, v160
	v_lshlrev_b64 v[160:161], 12, v[174:175]
	v_lshl_add_u64 v[160:161], s[46:47], 0, v[160:161]
	v_pk_mul_f32 v[144:145], v[144:145], v[158:159] op_sel_hi:[1,0]
	v_pk_mul_f32 v[146:147], v[146:147], v[158:159] op_sel_hi:[1,0]
	v_pk_mul_f32 v[218:219], v[140:141], v[158:159] op_sel_hi:[1,0]
	v_lshl_add_u64 v[160:161], v[160:161], 0, v[114:115]
	v_pk_mul_f32 v[140:141], v[142:143], v[158:159] op_sel_hi:[1,0]
	s_lshl_b32 s14, s14, 5
	s_add_i32 s15, s15, s8
	s_add_i32 s28, s15, s14
	s_ashr_i32 s29, s28, 31
	s_lshl_b64 s[14:15], s[28:29], 9
	s_waitcnt vmcnt(0)
	v_pk_mul_f32 v[142:143], v[94:95], v[218:219]
	v_pk_mul_f32 v[214:215], v[92:93], v[146:147]
	v_pk_mul_f32 v[216:217], v[90:91], v[144:145]
	v_pk_fma_f32 v[218:219], v[90:91], v[144:145], 0 op_sel_hi:[1,1,0]
	v_cvt_pk_bf16_f32 v144, v216, v217
	v_cvt_pk_bf16_f32 v145, v214, v215
	v_pk_mul_f32 v[140:141], v[96:97], v[140:141]
	v_pk_fma_f32 v[220:221], v[92:93], v[146:147], 0 op_sel_hi:[1,1,0]
	v_cvt_pk_bf16_f32 v146, v142, v143
	v_cvt_pk_bf16_f32 v147, v140, v141
	ds_bpermute_b32 v232, v244, v144
	ds_bpermute_b32 v233, v244, v145
	ds_bpermute_b32 v234, v244, v146
	ds_bpermute_b32 v235, v244, v147
	ds_bpermute_b32 v236, v244, v160
	ds_bpermute_b32 v237, v244, v161
	s_nop 1
	v_pk_mul_f32 v[144:145], v[136:137], v[158:159] op_sel_hi:[1,0]
	v_pk_mul_f32 v[136:137], v[138:139], v[158:159] op_sel_hi:[1,0]
	v_pk_mul_f32 v[138:139], v[86:87], v[144:145]
	v_pk_mul_f32 v[144:145], v[132:133], v[158:159] op_sel_hi:[1,0]
	v_pk_mul_f32 v[132:133], v[134:135], v[158:159] op_sel_hi:[1,0]
	v_pk_mul_f32 v[136:137], v[88:89], v[136:137]
	v_pk_mul_f32 v[132:133], v[84:85], v[132:133]
	v_pk_mul_f32 v[134:135], v[82:83], v[144:145]
	v_cvt_pk_bf16_f32 v144, v138, v139
	v_cvt_pk_bf16_f32 v145, v136, v137
	v_cvt_pk_bf16_f32 v147, v132, v133
	s_nop 0
	v_cvt_pk_bf16_f32 v146, v134, v135
	s_waitcnt lgkmcnt(0)
	global_store_dwordx4 v[236:237], v[232:235], off
	ds_bpermute_b32 v238, v244, v144
	ds_bpermute_b32 v239, v244, v145
	ds_bpermute_b32 v240, v244, v146
	ds_bpermute_b32 v241, v244, v147
	ds_bpermute_b32 v242, v244, v160
	ds_bpermute_b32 v243, v244, v161
	ds_read_b32 v144, v195
	ds_read_b32 v145, v196
	v_lshlrev_b64 v[146:147], 12, v[180:181]
	v_lshl_add_u64 v[146:147], s[46:47], 0, v[146:147]
	v_lshl_add_u64 v[146:147], v[146:147], 0, v[114:115]
	s_waitcnt lgkmcnt(0)
	v_add_f32_e32 v144, v144, v145
	v_fmamk_f32 v144, v144, 0x3c000000, v185
	v_rsq_f32_e32 v144, v144
	s_nop 0
	v_mul_f32_e32 v144, v159, v144
	v_pk_mul_f32 v[128:129], v[128:129], v[144:145] op_sel_hi:[1,0]
	v_pk_mul_f32 v[130:131], v[130:131], v[144:145] op_sel_hi:[1,0]
	v_pk_mul_f32 v[160:161], v[90:91], v[128:129]
	v_pk_mul_f32 v[158:159], v[92:93], v[130:131]
	v_pk_mul_f32 v[180:181], v[124:125], v[144:145] op_sel_hi:[1,0]
	v_pk_mul_f32 v[124:125], v[126:127], v[144:145] op_sel_hi:[1,0]
	v_pk_fma_f32 v[214:215], v[90:91], v[128:129], v[218:219]
	v_cvt_pk_bf16_f32 v128, v160, v161
	v_cvt_pk_bf16_f32 v129, v158, v159
	v_pk_mul_f32 v[124:125], v[96:97], v[124:125]
	v_pk_mul_f32 v[126:127], v[94:95], v[180:181]
	v_pk_fma_f32 v[180:181], v[92:93], v[130:131], v[220:221]
	v_cvt_pk_bf16_f32 v130, v126, v127
	v_cvt_pk_bf16_f32 v131, v124, v125
	s_waitcnt lgkmcnt(0)
	global_store_dwordx4 v[242:243], v[238:241], off offset:64
	ds_bpermute_b32 v232, v244, v128
	ds_bpermute_b32 v233, v244, v129
	ds_bpermute_b32 v234, v244, v130
	ds_bpermute_b32 v235, v244, v131
	ds_bpermute_b32 v236, v244, v146
	ds_bpermute_b32 v237, v244, v147
	s_nop 1
	v_pk_mul_f32 v[128:129], v[120:121], v[144:145] op_sel_hi:[1,0]
	v_pk_mul_f32 v[120:121], v[122:123], v[144:145] op_sel_hi:[1,0]
	v_pk_mul_f32 v[122:123], v[86:87], v[128:129]
	v_pk_mul_f32 v[128:129], v[116:117], v[144:145] op_sel_hi:[1,0]
	v_pk_mul_f32 v[116:117], v[118:119], v[144:145] op_sel_hi:[1,0]
	v_pk_mul_f32 v[120:121], v[88:89], v[120:121]
	v_pk_mul_f32 v[116:117], v[84:85], v[116:117]
	v_pk_mul_f32 v[118:119], v[82:83], v[128:129]
	v_cvt_pk_bf16_f32 v128, v122, v123
	v_cvt_pk_bf16_f32 v129, v120, v121
	v_cvt_pk_bf16_f32 v131, v116, v117
	s_nop 0
	v_cvt_pk_bf16_f32 v130, v118, v119
	s_waitcnt lgkmcnt(0)
	global_store_dwordx4 v[236:237], v[232:235], off
	ds_bpermute_b32 v238, v244, v128
	ds_bpermute_b32 v239, v244, v129
	ds_bpermute_b32 v240, v244, v130
	ds_bpermute_b32 v241, v244, v131
	ds_bpermute_b32 v242, v244, v146
	ds_bpermute_b32 v243, v244, v147
	ds_read_b32 v128, v197
	ds_read_b32 v129, v198
	s_waitcnt lgkmcnt(0)
	v_add_f32_e32 v128, v128, v129
	v_fmamk_f32 v128, v128, 0x3c000000, v185
	v_rsq_f32_e32 v130, v128
	ds_read2_b32 v[128:129], v213 offset0:32 offset1:48
	s_waitcnt lgkmcnt(0)
	v_mul_f32_e32 v128, v128, v130
	v_lshlrev_b64 v[130:131], 12, v[178:179]
	v_pk_mul_f32 v[110:111], v[110:111], v[128:129] op_sel_hi:[1,0]
	v_lshl_add_u64 v[130:131], s[46:47], 0, v[130:131]
	v_pk_mul_f32 v[112:113], v[112:113], v[128:129] op_sel_hi:[1,0]
	v_pk_mul_f32 v[144:145], v[90:91], v[110:111]
	v_lshl_add_u64 v[130:131], v[130:131], 0, v[114:115]
	v_pk_mul_f32 v[146:147], v[92:93], v[112:113]
	v_pk_mul_f32 v[158:159], v[106:107], v[128:129] op_sel_hi:[1,0]
	v_pk_mul_f32 v[106:107], v[108:109], v[128:129] op_sel_hi:[1,0]
	v_cvt_pk_bf16_f32 v144, v144, v145
	v_cvt_pk_bf16_f32 v145, v146, v147
	v_pk_mul_f32 v[108:109], v[94:95], v[158:159]
	v_pk_mul_f32 v[106:107], v[96:97], v[106:107]
	v_cvt_pk_bf16_f32 v146, v108, v109
	v_pk_fma_f32 v[110:111], v[90:91], v[110:111], v[214:215]
	v_cvt_pk_bf16_f32 v147, v106, v107
	s_waitcnt lgkmcnt(0)
	global_store_dwordx4 v[242:243], v[238:241], off offset:64
	ds_bpermute_b32 v232, v244, v144
	ds_bpermute_b32 v233, v244, v145
	ds_bpermute_b32 v234, v244, v146
	ds_bpermute_b32 v235, v244, v147
	ds_bpermute_b32 v236, v244, v130
	ds_bpermute_b32 v237, v244, v131
	v_pk_fma_f32 v[112:113], v[92:93], v[112:113], v[180:181]
	s_nop 0
	v_pk_mul_f32 v[144:145], v[102:103], v[128:129] op_sel_hi:[1,0]
	v_pk_mul_f32 v[102:103], v[104:105], v[128:129] op_sel_hi:[1,0]
	v_pk_mul_f32 v[104:105], v[86:87], v[144:145]
	v_pk_mul_f32 v[144:145], v[98:99], v[128:129] op_sel_hi:[1,0]
	v_pk_mul_f32 v[98:99], v[100:101], v[128:129] op_sel_hi:[1,0]
	v_pk_mul_f32 v[102:103], v[88:89], v[102:103]
	v_pk_mul_f32 v[98:99], v[84:85], v[98:99]
	v_pk_mul_f32 v[100:101], v[82:83], v[144:145]
	v_cvt_pk_bf16_f32 v144, v104, v105
	v_cvt_pk_bf16_f32 v145, v102, v103
	v_cvt_pk_bf16_f32 v147, v98, v99
	s_nop 0
	v_cvt_pk_bf16_f32 v146, v100, v101
	s_waitcnt lgkmcnt(0)
	global_store_dwordx4 v[236:237], v[232:235], off
	ds_bpermute_b32 v238, v244, v144
	ds_bpermute_b32 v239, v244, v145
	ds_bpermute_b32 v240, v244, v146
	ds_bpermute_b32 v241, v244, v147
	ds_bpermute_b32 v242, v244, v130
	ds_bpermute_b32 v243, v244, v131
	ds_read_b32 v128, v199
	ds_read_b32 v130, v200
	s_waitcnt lgkmcnt(0)
	v_add_f32_e32 v128, v128, v130
	v_fmamk_f32 v128, v128, 0x3c000000, v185
	v_rsq_f32_e32 v128, v128
	v_lshlrev_b64 v[130:131], 12, v[176:177]
	v_lshl_add_u64 v[130:131], s[46:47], 0, v[130:131]
	v_lshl_add_u64 v[130:131], v[130:131], 0, v[114:115]
	v_mul_f32_e32 v128, v129, v128
	v_pk_mul_f32 v[144:145], v[78:79], v[128:129] op_sel_hi:[1,0]
	v_pk_mul_f32 v[80:81], v[80:81], v[128:129] op_sel_hi:[1,0]
	v_pk_mul_f32 v[74:75], v[74:75], v[128:129] op_sel_hi:[1,0]
	v_pk_mul_f32 v[76:77], v[76:77], v[128:129] op_sel_hi:[1,0]
	v_pk_mul_f32 v[146:147], v[92:93], v[80:81]
	v_pk_mul_f32 v[158:159], v[90:91], v[144:145]
	v_pk_mul_f32 v[76:77], v[96:97], v[76:77]
	v_pk_mul_f32 v[78:79], v[94:95], v[74:75]
	v_pk_fma_f32 v[160:161], v[92:93], v[80:81], v[112:113]
	v_pk_fma_f32 v[80:81], v[90:91], v[144:145], v[110:111]
	v_cvt_pk_bf16_f32 v110, v158, v159
	v_cvt_pk_bf16_f32 v111, v146, v147
	v_cvt_pk_bf16_f32 v112, v78, v79
	v_cvt_pk_bf16_f32 v113, v76, v77
	v_pk_mul_f32 v[70:71], v[70:71], v[128:129] op_sel_hi:[1,0]
	v_pk_mul_f32 v[72:73], v[72:73], v[128:129] op_sel_hi:[1,0]
	v_pk_mul_f32 v[66:67], v[66:67], v[128:129] op_sel_hi:[1,0]
	v_pk_mul_f32 v[68:69], v[68:69], v[128:129] op_sel_hi:[1,0]
	s_waitcnt lgkmcnt(0)
	global_store_dwordx4 v[242:243], v[238:241], off offset:64
	ds_bpermute_b32 v232, v244, v110
	ds_bpermute_b32 v233, v244, v111
	ds_bpermute_b32 v234, v244, v112
	ds_bpermute_b32 v235, v244, v113
	ds_bpermute_b32 v236, v244, v130
	ds_bpermute_b32 v237, v244, v131
	v_pk_mul_f32 v[72:73], v[88:89], v[72:73]
	v_pk_mul_f32 v[74:75], v[86:87], v[70:71]
	v_pk_mul_f32 v[68:69], v[84:85], v[68:69]
	v_pk_mul_f32 v[70:71], v[82:83], v[66:67]
	v_cvt_pk_bf16_f32 v110, v74, v75
	v_cvt_pk_bf16_f32 v111, v72, v73
	v_cvt_pk_bf16_f32 v113, v68, v69
	v_lshl_add_u64 v[66:67], v[166:167], 0, s[14:15]
	v_cvt_pk_bf16_f32 v112, v70, v71
	s_waitcnt lgkmcnt(0)
	global_store_dwordx4 v[236:237], v[232:235], off
	ds_bpermute_b32 v238, v244, v110
	ds_bpermute_b32 v239, v244, v111
	ds_bpermute_b32 v240, v244, v112
	ds_bpermute_b32 v241, v244, v113
	ds_bpermute_b32 v242, v244, v130
	ds_bpermute_b32 v243, v244, v131
	ds_swizzle_b32 v110, v80 offset:swizzle(SWAP,1)
	ds_swizzle_b32 v111, v81 offset:swizzle(SWAP,1)
	ds_swizzle_b32 v112, v160 offset:swizzle(SWAP,1)
	ds_swizzle_b32 v113, v161 offset:swizzle(SWAP,1)
	s_waitcnt lgkmcnt(2)
	v_pk_add_f32 v[80:81], v[80:81], v[110:111]
	ds_swizzle_b32 v110, v80 offset:swizzle(SWAP,2)
	s_waitcnt lgkmcnt(1)
	v_pk_add_f32 v[112:113], v[160:161], v[112:113]
	ds_swizzle_b32 v111, v81 offset:swizzle(SWAP,2)
	ds_swizzle_b32 v128, v112 offset:swizzle(SWAP,2)
	ds_swizzle_b32 v129, v113 offset:swizzle(SWAP,2)
	s_waitcnt lgkmcnt(2)
	v_pk_add_f32 v[80:81], v[80:81], v[110:111]
	ds_swizzle_b32 v110, v80 offset:swizzle(SWAP,4)
	s_waitcnt lgkmcnt(1)
	v_pk_add_f32 v[112:113], v[112:113], v[128:129]
	ds_swizzle_b32 v111, v81 offset:swizzle(SWAP,4)
	ds_swizzle_b32 v128, v112 offset:swizzle(SWAP,4)
	ds_swizzle_b32 v129, v113 offset:swizzle(SWAP,4)
	s_waitcnt lgkmcnt(2)
	v_pk_add_f32 v[80:81], v[80:81], v[110:111]
	ds_swizzle_b32 v110, v80 offset:swizzle(SWAP,8)
	s_waitcnt lgkmcnt(1)
	v_pk_add_f32 v[112:113], v[112:113], v[128:129]
	ds_swizzle_b32 v111, v81 offset:swizzle(SWAP,8)
	ds_swizzle_b32 v128, v112 offset:swizzle(SWAP,8)
	ds_swizzle_b32 v129, v113 offset:swizzle(SWAP,8)
	s_waitcnt lgkmcnt(0)
	global_store_dwordx4 v[242:243], v[238:241], off offset:64
	s_and_saveexec_b64 s[60:61], s[40:41]
	s_cbranch_execz .LBB0_196
	s_waitcnt lgkmcnt(0)
	v_pk_add_f32 v[112:113], v[112:113], v[128:129]
	v_pk_add_f32 v[110:111], v[80:81], v[110:111]
	global_store_dwordx4 v[66:67], v[110:113], off

.LBB0_202:
	s_or_b64 exec, exec, s[60:61]
	ds_read_b32 v66, v201
	ds_read_b32 v67, v202
	ds_read2_b32 v[68:69], v213 offset0:128 offset1:144
	s_mov_b64 s[14:15], 0x80000
	s_waitcnt lgkmcnt(1)
	v_add_f32_e32 v66, v66, v67
	v_fmamk_f32 v66, v66, 0x3c000000, v185
	v_rsq_f32_e32 v66, v66
	s_waitcnt lgkmcnt(0)
	v_mul_f32_e32 v68, v68, v66
	v_lshlrev_b64 v[66:67], 12, v[174:175]
	v_lshl_add_u64 v[66:67], s[46:47], 0, v[66:67]
	v_lshl_add_u64 v[66:67], v[66:67], 0, v[114:115]
	v_pk_mul_f32 v[64:65], v[64:65], v[68:69] op_sel_hi:[1,0]
	v_lshl_add_u64 v[70:71], v[66:67], 0, s[14:15]
	v_pk_mul_f32 v[62:63], v[62:63], v[68:69] op_sel_hi:[1,0]
	v_pk_mul_f32 v[72:73], v[92:93], v[64:65]
	v_pk_mul_f32 v[76:77], v[58:59], v[68:69] op_sel_hi:[1,0]
	s_mov_b32 s14, 0x80000
	v_pk_mul_f32 v[74:75], v[90:91], v[62:63]
	v_pk_mul_f32 v[58:59], v[60:61], v[68:69] op_sel_hi:[1,0]
	v_pk_mul_f32 v[60:61], v[94:95], v[76:77]
	v_pk_fma_f32 v[76:77], v[90:91], v[62:63], 0 op_sel_hi:[1,1,0]
	v_cvt_pk_bf16_f32 v63, v72, v73
	v_add_co_u32_e32 v72, vcc, s14, v66
	v_cvt_pk_bf16_f32 v62, v74, v75
	v_pk_mul_f32 v[58:59], v[96:97], v[58:59]
	s_nop 0
	v_addc_co_u32_e32 v73, vcc, 0, v67, vcc
	v_pk_fma_f32 v[78:79], v[92:93], v[64:65], 0 op_sel_hi:[1,1,0]
	v_cvt_pk_bf16_f32 v64, v60, v61
	v_cvt_pk_bf16_f32 v65, v58, v59
	ds_bpermute_b32 v232, v244, v62
	ds_bpermute_b32 v233, v244, v63
	ds_bpermute_b32 v234, v244, v64
	ds_bpermute_b32 v235, v244, v65
	ds_bpermute_b32 v236, v244, v72
	ds_bpermute_b32 v237, v244, v73
	s_mov_b64 s[14:15], 0x90000
	s_nop 0
	v_pk_mul_f32 v[62:63], v[54:55], v[68:69] op_sel_hi:[1,0]
	v_pk_mul_f32 v[54:55], v[56:57], v[68:69] op_sel_hi:[1,0]
	v_pk_mul_f32 v[56:57], v[86:87], v[62:63]
	v_pk_mul_f32 v[62:63], v[50:51], v[68:69] op_sel_hi:[1,0]
	v_pk_mul_f32 v[50:51], v[52:53], v[68:69] op_sel_hi:[1,0]
	v_pk_mul_f32 v[54:55], v[88:89], v[54:55]
	v_pk_mul_f32 v[50:51], v[84:85], v[50:51]
	v_pk_mul_f32 v[52:53], v[82:83], v[62:63]
	v_cvt_pk_bf16_f32 v62, v56, v57
	v_cvt_pk_bf16_f32 v63, v54, v55
	v_cvt_pk_bf16_f32 v65, v50, v51
	s_nop 0
	v_cvt_pk_bf16_f32 v64, v52, v53
	s_waitcnt lgkmcnt(0)
	global_store_dwordx4 v[236:237], v[232:235], off
	ds_bpermute_b32 v238, v244, v62
	ds_bpermute_b32 v239, v244, v63
	ds_bpermute_b32 v240, v244, v64
	ds_bpermute_b32 v241, v244, v65
	ds_bpermute_b32 v242, v244, v70
	ds_bpermute_b32 v243, v244, v71
	ds_read_b32 v62, v203
	ds_read_b32 v63, v204
	v_lshl_add_u64 v[64:65], v[66:67], 0, s[14:15]
	s_mov_b32 s14, 0x90000
	s_waitcnt lgkmcnt(0)
	v_add_f32_e32 v62, v62, v63
	v_fmamk_f32 v62, v62, 0x3c000000, v185
	v_rsq_f32_e32 v62, v62
	s_nop 0
	v_mul_f32_e32 v62, v69, v62
	v_pk_mul_f32 v[48:49], v[48:49], v[62:63] op_sel_hi:[1,0]
	v_pk_mul_f32 v[46:47], v[46:47], v[62:63] op_sel_hi:[1,0]
	v_pk_mul_f32 v[68:69], v[92:93], v[48:49]
	v_pk_mul_f32 v[70:71], v[90:91], v[46:47]
	v_pk_fma_f32 v[74:75], v[90:91], v[46:47], v[76:77]
	v_cvt_pk_bf16_f32 v47, v68, v69
	v_add_co_u32_e32 v68, vcc, s14, v66
	v_pk_mul_f32 v[72:73], v[42:43], v[62:63] op_sel_hi:[1,0]
	v_pk_mul_f32 v[42:43], v[44:45], v[62:63] op_sel_hi:[1,0]
	v_cvt_pk_bf16_f32 v46, v70, v71
	v_addc_co_u32_e32 v69, vcc, 0, v67, vcc
	v_pk_mul_f32 v[42:43], v[96:97], v[42:43]
	v_pk_mul_f32 v[44:45], v[94:95], v[72:73]
	v_pk_fma_f32 v[72:73], v[92:93], v[48:49], v[78:79]
	v_cvt_pk_bf16_f32 v48, v44, v45
	v_cvt_pk_bf16_f32 v49, v42, v43
	s_waitcnt lgkmcnt(0)
	global_store_dwordx4 v[242:243], v[238:241], off offset:64
	ds_bpermute_b32 v232, v244, v46
	ds_bpermute_b32 v233, v244, v47
	ds_bpermute_b32 v234, v244, v48
	ds_bpermute_b32 v235, v244, v49
	ds_bpermute_b32 v236, v244, v68
	ds_bpermute_b32 v237, v244, v69
	s_mov_b64 s[14:15], 0xa0000
	s_nop 0
	v_pk_mul_f32 v[46:47], v[38:39], v[62:63] op_sel_hi:[1,0]
	v_pk_mul_f32 v[38:39], v[40:41], v[62:63] op_sel_hi:[1,0]
	v_pk_mul_f32 v[40:41], v[86:87], v[46:47]
	v_pk_mul_f32 v[46:47], v[34:35], v[62:63] op_sel_hi:[1,0]
	v_pk_mul_f32 v[34:35], v[36:37], v[62:63] op_sel_hi:[1,0]
	v_pk_mul_f32 v[38:39], v[88:89], v[38:39]
	v_pk_mul_f32 v[34:35], v[84:85], v[34:35]
	v_pk_mul_f32 v[36:37], v[82:83], v[46:47]
	v_cvt_pk_bf16_f32 v46, v40, v41
	v_cvt_pk_bf16_f32 v47, v38, v39
	v_cvt_pk_bf16_f32 v49, v34, v35
	s_nop 0
	v_cvt_pk_bf16_f32 v48, v36, v37
	s_waitcnt lgkmcnt(0)
	global_store_dwordx4 v[236:237], v[232:235], off
	ds_bpermute_b32 v238, v244, v46
	ds_bpermute_b32 v239, v244, v47
	ds_bpermute_b32 v240, v244, v48
	ds_bpermute_b32 v241, v244, v49
	ds_bpermute_b32 v242, v244, v64
	ds_bpermute_b32 v243, v244, v65
	ds_read_b32 v46, v205
	ds_read_b32 v47, v206
	s_waitcnt lgkmcnt(0)
	v_add_f32_e32 v46, v46, v47
	v_fmamk_f32 v46, v46, 0x3c000000, v185
	v_rsq_f32_e32 v48, v46
	ds_read2_b32 v[46:47], v213 offset0:160 offset1:176
	s_waitcnt lgkmcnt(0)
	v_mul_f32_e32 v46, v46, v48
	v_lshl_add_u64 v[48:49], v[66:67], 0, s[14:15]
	v_pk_mul_f32 v[30:31], v[30:31], v[46:47] op_sel_hi:[1,0]
	v_pk_mul_f32 v[68:69], v[26:27], v[46:47] op_sel_hi:[1,0]
	s_mov_b32 s14, 0xa0000
	v_pk_mul_f32 v[32:33], v[32:33], v[46:47] op_sel_hi:[1,0]
	v_pk_mul_f32 v[62:63], v[90:91], v[30:31]
	v_pk_mul_f32 v[26:27], v[28:29], v[46:47] op_sel_hi:[1,0]
	v_pk_mul_f32 v[28:29], v[94:95], v[68:69]
	v_add_co_u32_e32 v68, vcc, s14, v66
	v_pk_mul_f32 v[64:65], v[92:93], v[32:33]
	v_cvt_pk_bf16_f32 v62, v62, v63
	s_nop 0
	v_addc_co_u32_e32 v69, vcc, 0, v67, vcc
	v_cvt_pk_bf16_f32 v63, v64, v65
	v_pk_mul_f32 v[26:27], v[96:97], v[26:27]
	v_cvt_pk_bf16_f32 v64, v28, v29
	s_mov_b64 s[14:15], 0xb0000
	v_cvt_pk_bf16_f32 v65, v26, v27
	s_waitcnt lgkmcnt(0)
	global_store_dwordx4 v[242:243], v[238:241], off offset:64
	ds_bpermute_b32 v232, v244, v62
	ds_bpermute_b32 v233, v244, v63
	ds_bpermute_b32 v234, v244, v64
	ds_bpermute_b32 v235, v244, v65
	ds_bpermute_b32 v236, v244, v68
	ds_bpermute_b32 v237, v244, v69
	v_pk_fma_f32 v[30:31], v[90:91], v[30:31], v[74:75]
	v_pk_fma_f32 v[32:33], v[92:93], v[32:33], v[72:73]
	v_pk_mul_f32 v[62:63], v[22:23], v[46:47] op_sel_hi:[1,0]
	v_pk_mul_f32 v[22:23], v[24:25], v[46:47] op_sel_hi:[1,0]
	v_pk_mul_f32 v[24:25], v[86:87], v[62:63]
	v_pk_mul_f32 v[62:63], v[18:19], v[46:47] op_sel_hi:[1,0]
	v_pk_mul_f32 v[18:19], v[20:21], v[46:47] op_sel_hi:[1,0]
	v_pk_mul_f32 v[22:23], v[88:89], v[22:23]
	v_pk_mul_f32 v[18:19], v[84:85], v[18:19]
	v_pk_mul_f32 v[20:21], v[82:83], v[62:63]
	v_cvt_pk_bf16_f32 v62, v24, v25
	v_cvt_pk_bf16_f32 v63, v22, v23
	v_cvt_pk_bf16_f32 v65, v18, v19
	s_nop 0
	v_cvt_pk_bf16_f32 v64, v20, v21
	s_waitcnt lgkmcnt(0)
	global_store_dwordx4 v[236:237], v[232:235], off
	ds_bpermute_b32 v238, v244, v62
	ds_bpermute_b32 v239, v244, v63
	ds_bpermute_b32 v240, v244, v64
	ds_bpermute_b32 v241, v244, v65
	ds_bpermute_b32 v242, v244, v48
	ds_bpermute_b32 v243, v244, v49
	ds_read_b32 v46, v207
	ds_read_b32 v48, v208
	s_waitcnt lgkmcnt(0)
	v_add_f32_e32 v46, v46, v48
	v_fmamk_f32 v46, v46, 0x3c000000, v185
	v_rsq_f32_e32 v46, v46
	v_lshl_add_u64 v[48:49], v[66:67], 0, s[14:15]
	s_mov_b32 s14, 0xb0000
	v_mul_f32_e32 v46, v47, v46
	v_pk_mul_f32 v[10:11], v[10:11], v[46:47] op_sel_hi:[1,0]
	v_pk_mul_f32 v[62:63], v[14:15], v[46:47] op_sel_hi:[1,0]
	v_pk_mul_f32 v[16:17], v[16:17], v[46:47] op_sel_hi:[1,0]
	v_pk_mul_f32 v[12:13], v[12:13], v[46:47] op_sel_hi:[1,0]
	v_pk_mul_f32 v[14:15], v[94:95], v[10:11]
	v_add_co_u32_e32 v10, vcc, s14, v66
	v_pk_mul_f32 v[64:65], v[92:93], v[16:17]
	v_pk_mul_f32 v[68:69], v[90:91], v[62:63]
	v_pk_mul_f32 v[12:13], v[96:97], v[12:13]
	v_pk_fma_f32 v[70:71], v[92:93], v[16:17], v[32:33]
	v_pk_fma_f32 v[16:17], v[90:91], v[62:63], v[30:31]
	v_cvt_pk_bf16_f32 v30, v68, v69
	v_cvt_pk_bf16_f32 v31, v64, v65
	v_cvt_pk_bf16_f32 v32, v14, v15
	v_cvt_pk_bf16_f32 v33, v12, v13
	v_addc_co_u32_e32 v11, vcc, 0, v67, vcc
	v_pk_mul_f32 v[6:7], v[6:7], v[46:47] op_sel_hi:[1,0]
	v_pk_mul_f32 v[8:9], v[8:9], v[46:47] op_sel_hi:[1,0]
	v_pk_mul_f32 v[2:3], v[2:3], v[46:47] op_sel_hi:[1,0]
	v_pk_mul_f32 v[4:5], v[4:5], v[46:47] op_sel_hi:[1,0]
	s_waitcnt lgkmcnt(0)
	global_store_dwordx4 v[242:243], v[238:241], off offset:64
	ds_bpermute_b32 v232, v244, v30
	ds_bpermute_b32 v233, v244, v31
	ds_bpermute_b32 v234, v244, v32
	ds_bpermute_b32 v235, v244, v33
	ds_bpermute_b32 v236, v244, v10
	ds_bpermute_b32 v237, v244, v11
	v_pk_mul_f32 v[8:9], v[88:89], v[8:9]
	v_pk_mul_f32 v[10:11], v[86:87], v[6:7]
	v_pk_mul_f32 v[4:5], v[84:85], v[4:5]
	v_pk_mul_f32 v[6:7], v[82:83], v[2:3]
	v_cvt_pk_bf16_f32 v30, v10, v11
	v_cvt_pk_bf16_f32 v31, v8, v9
	v_cvt_pk_bf16_f32 v33, v4, v5
	s_add_i32 s14, s28, 2
	v_cvt_pk_bf16_f32 v32, v6, v7
	s_waitcnt lgkmcnt(0)
	global_store_dwordx4 v[236:237], v[232:235], off
	ds_bpermute_b32 v238, v244, v30
	ds_bpermute_b32 v239, v244, v31
	ds_bpermute_b32 v240, v244, v32
	ds_bpermute_b32 v241, v244, v33
	ds_bpermute_b32 v242, v244, v48
	ds_bpermute_b32 v243, v244, v49
	ds_swizzle_b32 v30, v16 offset:swizzle(SWAP,1)
	ds_swizzle_b32 v31, v17 offset:swizzle(SWAP,1)
	ds_swizzle_b32 v32, v70 offset:swizzle(SWAP,1)
	ds_swizzle_b32 v33, v71 offset:swizzle(SWAP,1)
	s_ashr_i32 s15, s14, 31
	s_lshl_b64 s[14:15], s[14:15], 9
	s_waitcnt lgkmcnt(2)
	v_pk_add_f32 v[16:17], v[16:17], v[30:31]
	ds_swizzle_b32 v30, v16 offset:swizzle(SWAP,2)
	s_waitcnt lgkmcnt(1)
	v_pk_add_f32 v[32:33], v[70:71], v[32:33]
	ds_swizzle_b32 v31, v17 offset:swizzle(SWAP,2)
	ds_swizzle_b32 v46, v32 offset:swizzle(SWAP,2)
	ds_swizzle_b32 v47, v33 offset:swizzle(SWAP,2)
	v_lshl_add_u64 v[2:3], v[166:167], 0, s[14:15]
	s_waitcnt lgkmcnt(2)
	v_pk_add_f32 v[16:17], v[16:17], v[30:31]
	ds_swizzle_b32 v30, v16 offset:swizzle(SWAP,4)
	s_waitcnt lgkmcnt(1)
	v_pk_add_f32 v[32:33], v[32:33], v[46:47]
	ds_swizzle_b32 v31, v17 offset:swizzle(SWAP,4)
	ds_swizzle_b32 v46, v32 offset:swizzle(SWAP,4)
	ds_swizzle_b32 v47, v33 offset:swizzle(SWAP,4)
	s_waitcnt lgkmcnt(2)
	v_pk_add_f32 v[16:17], v[16:17], v[30:31]
	ds_swizzle_b32 v30, v16 offset:swizzle(SWAP,8)
	s_waitcnt lgkmcnt(1)
	v_pk_add_f32 v[32:33], v[32:33], v[46:47]
	ds_swizzle_b32 v31, v17 offset:swizzle(SWAP,8)
	ds_swizzle_b32 v46, v32 offset:swizzle(SWAP,8)
	ds_swizzle_b32 v47, v33 offset:swizzle(SWAP,8)
	s_waitcnt lgkmcnt(0)
	global_store_dwordx4 v[242:243], v[238:241], off offset:64
	s_and_saveexec_b64 s[28:29], s[40:41]
	s_cbranch_execz .LBB0_204
	s_waitcnt lgkmcnt(0)
	v_pk_add_f32 v[32:33], v[32:33], v[46:47]
	v_pk_add_f32 v[30:31], v[16:17], v[30:31]
	global_store_dwordx4 v[2:3], v[30:33], off

.LBB0_352:
	s_ashr_i32 s59, s58, 31
	s_lshl_b64 s[14:15], s[58:59], 25
	s_add_u32 s14, s37, s14
	s_addc_u32 s15, s64, s15
	v_lshlrev_b32_e32 v114, 1, v177
	v_ashrrev_i32_e32 v153, 31, v152
	v_lshl_add_u64 v[132:133], s[14:15], 0, v[114:115]
	v_lshlrev_b64 v[136:137], 12, v[152:153]
	v_mov_b32_e32 v155, v154
	v_lshl_add_u64 v[136:137], v[132:133], 0, v[136:137]
	v_cvt_pk_bf16_f32 v166, v166, v167
	v_cvt_pk_bf16_f32 v167, v134, v135
	v_cvt_pk_bf16_f32 v168, v168, v169
	v_cvt_pk_bf16_f32 v169, v138, v139
	v_mov_b32_e32 v158, v154
	v_mov_b32_e32 v159, v154
	v_cndmask_b32_e64 v114, 0, 1, s[56:57]
	ds_bpermute_b32 v232, v244, v166
	ds_bpermute_b32 v233, v244, v167
	ds_bpermute_b32 v234, v244, v168
	ds_bpermute_b32 v235, v244, v169
	ds_bpermute_b32 v236, v244, v136
	ds_bpermute_b32 v237, v244, v137
	v_pk_mul_f32 v[138:139], v[122:123], v[158:159]
	v_pk_mul_f32 v[134:135], v[120:121], v[154:155]
	v_pk_mul_f32 v[166:167], v[118:119], v[158:159]
	v_cmp_ne_u32_e64 s[40:41], 1, v114
	s_andn2_b64 vcc, exec, s[56:57]
	v_pk_mul_f32 v[168:169], v[116:117], v[154:155]
	s_waitcnt lgkmcnt(0)
	global_store_dwordx4 v[236:237], v[232:235], off
	s_cbranch_vccnz .LBB0_354
	v_max_f32_e32 v114, v134, v134
	v_max_f32_e32 v134, 0xc2a00000, v114
	v_max_f32_e32 v114, v168, v168
	v_max_f32_e32 v158, 0xc2a00000, v114
	v_mul_f32_e32 v114, 0xbfb8aa3b, v134
	v_exp_f32_e32 v114, v114
	v_mul_f32_e32 v155, 0xbfb8aa3b, v158
	v_exp_f32_e32 v155, v155
	v_max_f32_e32 v135, v135, v135
	v_add_f32_e32 v114, 1.0, v114
	v_rcp_f32_e32 v160, v114
	v_add_f32_e32 v114, 1.0, v155
	v_max_f32_e32 v135, 0xc2a00000, v135
	v_max_f32_e32 v155, v169, v169
	v_max_f32_e32 v159, 0xc2a00000, v155
	v_mul_f32_e32 v155, 0xbfb8aa3b, v135
	v_exp_f32_e32 v155, v155
	v_mul_f32_e32 v161, 0xbfb8aa3b, v159
	v_exp_f32_e32 v169, v161
	v_max_f32_e32 v138, v138, v138
	v_rcp_f32_e32 v168, v114
	v_add_f32_e32 v114, 1.0, v155
	v_max_f32_e32 v138, 0xc2a00000, v138
	v_max_f32_e32 v155, v166, v166
	v_max_f32_e32 v166, 0xc2a00000, v155
	v_mul_f32_e32 v155, 0xbfb8aa3b, v138
	v_exp_f32_e32 v155, v155
	v_rcp_f32_e32 v161, v114
	v_add_f32_e32 v114, 1.0, v169
	v_mul_f32_e32 v169, 0xbfb8aa3b, v166
	v_exp_f32_e32 v171, v169
	v_max_f32_e32 v139, v139, v139
	v_rcp_f32_e32 v169, v114
	v_add_f32_e32 v114, 1.0, v155
	v_max_f32_e32 v139, 0xc2a00000, v139
	v_max_f32_e32 v155, v167, v167
	v_max_f32_e32 v167, 0xc2a00000, v155
	v_mul_f32_e32 v155, 0xbfb8aa3b, v139
	v_rcp_f32_e32 v170, v114
	v_add_f32_e32 v114, 1.0, v171
	v_exp_f32_e32 v155, v155
	v_mul_f32_e32 v171, 0xbfb8aa3b, v167
	v_exp_f32_e32 v179, v171
	v_rcp_f32_e32 v178, v114
	v_add_f32_e32 v114, 1.0, v155
	v_rcp_f32_e32 v171, v114
	v_add_f32_e32 v114, 1.0, v179
	v_rcp_f32_e32 v179, v114
	v_pk_mul_f32 v[134:135], v[134:135], v[160:161]
	v_pk_mul_f32 v[138:139], v[138:139], v[170:171]
	v_pk_mul_f32 v[168:169], v[158:159], v[168:169]
	v_pk_mul_f32 v[166:167], v[166:167], v[178:179]

.LBB0_356:
	v_or_b32_e32 v136, 16, v152
	v_ashrrev_i32_e32 v137, 31, v136
	v_lshlrev_b64 v[136:137], 12, v[136:137]
	v_mov_b32_e32 v135, v134
	v_lshl_add_u64 v[136:137], v[132:133], 0, v[136:137]
	v_cvt_pk_bf16_f32 v168, v168, v169
	v_cvt_pk_bf16_f32 v169, v138, v139
	v_cvt_pk_bf16_f32 v170, v170, v171
	v_cvt_pk_bf16_f32 v171, v166, v167
	v_mov_b32_e32 v158, v134
	v_mov_b32_e32 v159, v134
	ds_bpermute_b32 v232, v244, v168
	ds_bpermute_b32 v233, v244, v169
	ds_bpermute_b32 v234, v244, v170
	ds_bpermute_b32 v235, v244, v171
	ds_bpermute_b32 v236, v244, v136
	ds_bpermute_b32 v237, v244, v137
	v_pk_mul_f32 v[138:139], v[104:105], v[158:159]
	v_pk_mul_f32 v[166:167], v[100:101], v[158:159]
	v_pk_mul_f32 v[168:169], v[102:103], v[134:135]
	s_and_b64 vcc, exec, s[40:41]
	v_pk_mul_f32 v[170:171], v[98:99], v[134:135]
	s_waitcnt lgkmcnt(0)
	global_store_dwordx4 v[236:237], v[232:235], off
	s_cbranch_vccnz .LBB0_358
	v_max_f32_e32 v114, v168, v168
	v_max_f32_e32 v134, 0xc2a00000, v114
	v_max_f32_e32 v114, v170, v170
	v_max_f32_e32 v158, 0xc2a00000, v114
	v_mul_f32_e32 v114, 0xbfb8aa3b, v134
	v_exp_f32_e32 v114, v114
	v_mul_f32_e32 v135, 0xbfb8aa3b, v158
	v_exp_f32_e32 v135, v135
	v_max_f32_e32 v155, v171, v171
	v_add_f32_e32 v114, 1.0, v114
	v_rcp_f32_e32 v160, v114
	v_add_f32_e32 v114, 1.0, v135
	v_max_f32_e32 v135, v169, v169
	v_max_f32_e32 v135, 0xc2a00000, v135
	v_max_f32_e32 v159, 0xc2a00000, v155
	v_mul_f32_e32 v155, 0xbfb8aa3b, v135
	v_exp_f32_e32 v155, v155
	v_mul_f32_e32 v161, 0xbfb8aa3b, v159
	v_exp_f32_e32 v168, v161
	v_max_f32_e32 v138, v138, v138
	v_rcp_f32_e32 v170, v114
	v_add_f32_e32 v114, 1.0, v155
	v_max_f32_e32 v138, 0xc2a00000, v138
	v_max_f32_e32 v155, v166, v166
	v_max_f32_e32 v166, 0xc2a00000, v155
	v_mul_f32_e32 v155, 0xbfb8aa3b, v138
	v_exp_f32_e32 v155, v155
	v_rcp_f32_e32 v161, v114
	v_add_f32_e32 v114, 1.0, v168
	v_mul_f32_e32 v168, 0xbfb8aa3b, v166
	v_exp_f32_e32 v168, v168
	v_max_f32_e32 v139, v139, v139
	v_rcp_f32_e32 v171, v114
	v_add_f32_e32 v114, 1.0, v155
	v_max_f32_e32 v139, 0xc2a00000, v139
	v_max_f32_e32 v155, v167, v167
	v_max_f32_e32 v167, 0xc2a00000, v155
	v_mul_f32_e32 v155, 0xbfb8aa3b, v139
	v_rcp_f32_e32 v178, v114
	v_add_f32_e32 v114, 1.0, v168
	v_exp_f32_e32 v155, v155
	v_mul_f32_e32 v168, 0xbfb8aa3b, v167
	v_exp_f32_e32 v168, v168
	v_rcp_f32_e32 v180, v114
	v_add_f32_e32 v114, 1.0, v155
	v_rcp_f32_e32 v179, v114
	v_add_f32_e32 v114, 1.0, v168
	v_rcp_f32_e32 v181, v114
	v_pk_mul_f32 v[168:169], v[134:135], v[160:161]
	v_pk_mul_f32 v[138:139], v[138:139], v[178:179]
	v_pk_mul_f32 v[170:171], v[158:159], v[170:171]
	v_pk_mul_f32 v[166:167], v[166:167], v[180:181]
.LBB0_358:
	ds_read_b32 v134, v176 offset:128
	v_cvt_pk_bf16_f32 v168, v168, v169
	v_cvt_pk_bf16_f32 v169, v138, v139
	v_cvt_pk_bf16_f32 v170, v170, v171
	v_cvt_pk_bf16_f32 v171, v166, v167
	ds_bpermute_b32 v238, v244, v168
	ds_bpermute_b32 v239, v244, v169
	ds_bpermute_b32 v240, v244, v170
	ds_bpermute_b32 v241, v244, v171
	ds_bpermute_b32 v242, v244, v136
	ds_bpermute_b32 v243, v244, v137
	s_waitcnt lgkmcnt(0)
	v_pk_mul_f32 v[138:139], v[96:97], v[134:135] op_sel_hi:[1,0]
	v_pk_mul_f32 v[166:167], v[92:93], v[134:135] op_sel_hi:[1,0]
	v_pk_mul_f32 v[168:169], v[94:95], v[134:135] op_sel_hi:[1,0]
	s_and_b64 vcc, exec, s[40:41]
	v_pk_mul_f32 v[170:171], v[90:91], v[134:135] op_sel_hi:[1,0]
	s_waitcnt lgkmcnt(0)
	global_store_dwordx4 v[242:243], v[238:241], off offset:64
	s_cbranch_vccnz .LBB0_360
	v_max_f32_e32 v114, v168, v168
	v_max_f32_e32 v136, 0xc2a00000, v114
	v_max_f32_e32 v114, v170, v170
	v_max_f32_e32 v158, 0xc2a00000, v114
	v_mul_f32_e32 v114, 0xbfb8aa3b, v136
	v_exp_f32_e32 v114, v114
	v_mul_f32_e32 v135, 0xbfb8aa3b, v158
	v_exp_f32_e32 v135, v135
	v_add_f32_e32 v114, 1.0, v114
	v_rcp_f32_e32 v160, v114
	v_add_f32_e32 v114, 1.0, v135
	v_max_f32_e32 v135, v169, v169
	v_max_f32_e32 v137, 0xc2a00000, v135
	v_max_f32_e32 v135, v171, v171
	v_max_f32_e32 v159, 0xc2a00000, v135
	v_mul_f32_e32 v135, 0xbfb8aa3b, v137
	v_exp_f32_e32 v135, v135
	v_mul_f32_e32 v155, 0xbfb8aa3b, v159
	v_rcp_f32_e32 v170, v114
	v_exp_f32_e32 v155, v155
	v_add_f32_e32 v114, 1.0, v135
	v_max_f32_e32 v135, v138, v138
	v_max_f32_e32 v138, 0xc2a00000, v135
	v_max_f32_e32 v135, v166, v166
	v_max_f32_e32 v166, 0xc2a00000, v135
	v_mul_f32_e32 v135, 0xbfb8aa3b, v138
	v_exp_f32_e32 v135, v135
	v_rcp_f32_e32 v161, v114
	v_add_f32_e32 v114, 1.0, v155
	v_mul_f32_e32 v155, 0xbfb8aa3b, v166
	v_exp_f32_e32 v155, v155
	v_rcp_f32_e32 v171, v114
	v_add_f32_e32 v114, 1.0, v135
	v_max_f32_e32 v135, v139, v139
	v_max_f32_e32 v139, 0xc2a00000, v135
	v_max_f32_e32 v135, v167, v167
	v_max_f32_e32 v167, 0xc2a00000, v135
	v_mul_f32_e32 v135, 0xbfb8aa3b, v139
	v_rcp_f32_e32 v178, v114
	v_add_f32_e32 v114, 1.0, v155
	v_exp_f32_e32 v135, v135
	v_mul_f32_e32 v155, 0xbfb8aa3b, v167
	v_exp_f32_e32 v155, v155
	v_rcp_f32_e32 v180, v114
	v_add_f32_e32 v114, 1.0, v135
	v_rcp_f32_e32 v179, v114
	v_add_f32_e32 v114, 1.0, v155
	v_rcp_f32_e32 v181, v114
	v_pk_mul_f32 v[168:169], v[136:137], v[160:161]
	v_pk_mul_f32 v[138:139], v[138:139], v[178:179]
	v_pk_mul_f32 v[170:171], v[158:159], v[170:171]
	v_pk_mul_f32 v[166:167], v[166:167], v[180:181]
.LBB0_360:
	v_or_b32_e32 v136, 32, v152
	v_ashrrev_i32_e32 v137, 31, v136
	v_lshlrev_b64 v[136:137], 12, v[136:137]
	v_mov_b32_e32 v135, v134
	v_lshl_add_u64 v[136:137], v[132:133], 0, v[136:137]
	v_cvt_pk_bf16_f32 v168, v168, v169
	v_cvt_pk_bf16_f32 v169, v138, v139
	v_cvt_pk_bf16_f32 v170, v170, v171
	v_cvt_pk_bf16_f32 v171, v166, v167
	v_mov_b32_e32 v158, v134
	v_mov_b32_e32 v159, v134
	ds_bpermute_b32 v232, v244, v168
	ds_bpermute_b32 v233, v244, v169
	ds_bpermute_b32 v234, v244, v170
	ds_bpermute_b32 v235, v244, v171
	ds_bpermute_b32 v236, v244, v136
	ds_bpermute_b32 v237, v244, v137
	v_pk_mul_f32 v[138:139], v[88:89], v[158:159]
	v_pk_mul_f32 v[166:167], v[84:85], v[158:159]
	v_pk_mul_f32 v[168:169], v[86:87], v[134:135]
	s_and_b64 vcc, exec, s[40:41]
	v_pk_mul_f32 v[170:171], v[82:83], v[134:135]
	s_waitcnt lgkmcnt(0)
	global_store_dwordx4 v[236:237], v[232:235], off
	s_cbranch_vccnz .LBB0_362
	v_max_f32_e32 v114, v168, v168
	v_max_f32_e32 v134, 0xc2a00000, v114
	v_max_f32_e32 v114, v170, v170
	v_max_f32_e32 v158, 0xc2a00000, v114
	v_mul_f32_e32 v114, 0xbfb8aa3b, v134
	v_exp_f32_e32 v114, v114
	v_mul_f32_e32 v135, 0xbfb8aa3b, v158
	v_exp_f32_e32 v135, v135
	v_max_f32_e32 v155, v171, v171
	v_add_f32_e32 v114, 1.0, v114
	v_rcp_f32_e32 v160, v114
	v_add_f32_e32 v114, 1.0, v135
	v_max_f32_e32 v135, v169, v169
	v_max_f32_e32 v135, 0xc2a00000, v135
	v_max_f32_e32 v159, 0xc2a00000, v155
	v_mul_f32_e32 v155, 0xbfb8aa3b, v135
	v_exp_f32_e32 v155, v155
	v_mul_f32_e32 v161, 0xbfb8aa3b, v159
	v_exp_f32_e32 v168, v161
	v_max_f32_e32 v138, v138, v138
	v_rcp_f32_e32 v170, v114
	v_add_f32_e32 v114, 1.0, v155
	v_max_f32_e32 v138, 0xc2a00000, v138
	v_max_f32_e32 v155, v166, v166
	v_max_f32_e32 v166, 0xc2a00000, v155
	v_mul_f32_e32 v155, 0xbfb8aa3b, v138
	v_exp_f32_e32 v155, v155
	v_rcp_f32_e32 v161, v114
	v_add_f32_e32 v114, 1.0, v168
	v_mul_f32_e32 v168, 0xbfb8aa3b, v166
	v_exp_f32_e32 v168, v168
	v_max_f32_e32 v139, v139, v139
	v_rcp_f32_e32 v171, v114
	v_add_f32_e32 v114, 1.0, v155
	v_max_f32_e32 v139, 0xc2a00000, v139
	v_max_f32_e32 v155, v167, v167
	v_max_f32_e32 v167, 0xc2a00000, v155
	v_mul_f32_e32 v155, 0xbfb8aa3b, v139
	v_rcp_f32_e32 v178, v114
	v_add_f32_e32 v114, 1.0, v168
	v_exp_f32_e32 v155, v155
	v_mul_f32_e32 v168, 0xbfb8aa3b, v167
	v_exp_f32_e32 v168, v168
	v_rcp_f32_e32 v180, v114
	v_add_f32_e32 v114, 1.0, v155
	v_rcp_f32_e32 v179, v114
	v_add_f32_e32 v114, 1.0, v168
	v_rcp_f32_e32 v181, v114
	v_pk_mul_f32 v[168:169], v[134:135], v[160:161]
	v_pk_mul_f32 v[138:139], v[138:139], v[178:179]
	v_pk_mul_f32 v[170:171], v[158:159], v[170:171]
	v_pk_mul_f32 v[166:167], v[166:167], v[180:181]
.LBB0_362:
	ds_read_b32 v134, v176 offset:192
	v_cvt_pk_bf16_f32 v168, v168, v169
	v_cvt_pk_bf16_f32 v169, v138, v139
	v_cvt_pk_bf16_f32 v170, v170, v171
	v_cvt_pk_bf16_f32 v171, v166, v167
	ds_bpermute_b32 v238, v244, v168
	ds_bpermute_b32 v239, v244, v169
	ds_bpermute_b32 v240, v244, v170
	ds_bpermute_b32 v241, v244, v171
	ds_bpermute_b32 v242, v244, v136
	ds_bpermute_b32 v243, v244, v137
	s_waitcnt lgkmcnt(0)
	v_pk_mul_f32 v[138:139], v[80:81], v[134:135] op_sel_hi:[1,0]
	v_pk_mul_f32 v[166:167], v[76:77], v[134:135] op_sel_hi:[1,0]
	v_pk_mul_f32 v[168:169], v[78:79], v[134:135] op_sel_hi:[1,0]
	s_and_b64 vcc, exec, s[40:41]
	v_pk_mul_f32 v[170:171], v[74:75], v[134:135] op_sel_hi:[1,0]
	s_waitcnt lgkmcnt(0)
	global_store_dwordx4 v[242:243], v[238:241], off offset:64
	s_cbranch_vccnz .LBB0_364
	v_max_f32_e32 v114, v168, v168
	v_max_f32_e32 v136, 0xc2a00000, v114
	v_max_f32_e32 v114, v170, v170
	v_max_f32_e32 v158, 0xc2a00000, v114
	v_mul_f32_e32 v114, 0xbfb8aa3b, v136
	v_exp_f32_e32 v114, v114
	v_mul_f32_e32 v135, 0xbfb8aa3b, v158
	v_exp_f32_e32 v135, v135
	v_add_f32_e32 v114, 1.0, v114
	v_rcp_f32_e32 v160, v114
	v_add_f32_e32 v114, 1.0, v135
	v_max_f32_e32 v135, v169, v169
	v_max_f32_e32 v137, 0xc2a00000, v135
	v_max_f32_e32 v135, v171, v171
	v_max_f32_e32 v159, 0xc2a00000, v135
	v_mul_f32_e32 v135, 0xbfb8aa3b, v137
	v_exp_f32_e32 v135, v135
	v_mul_f32_e32 v155, 0xbfb8aa3b, v159
	v_rcp_f32_e32 v170, v114
	v_exp_f32_e32 v155, v155
	v_add_f32_e32 v114, 1.0, v135
	v_max_f32_e32 v135, v138, v138
	v_max_f32_e32 v138, 0xc2a00000, v135
	v_max_f32_e32 v135, v166, v166
	v_max_f32_e32 v166, 0xc2a00000, v135
	v_mul_f32_e32 v135, 0xbfb8aa3b, v138
	v_exp_f32_e32 v135, v135
	v_rcp_f32_e32 v161, v114
	v_add_f32_e32 v114, 1.0, v155
	v_mul_f32_e32 v155, 0xbfb8aa3b, v166
	v_exp_f32_e32 v155, v155
	v_rcp_f32_e32 v171, v114
	v_add_f32_e32 v114, 1.0, v135
	v_max_f32_e32 v135, v139, v139
	v_max_f32_e32 v139, 0xc2a00000, v135
	v_max_f32_e32 v135, v167, v167
	v_max_f32_e32 v167, 0xc2a00000, v135
	v_mul_f32_e32 v135, 0xbfb8aa3b, v139
	v_rcp_f32_e32 v178, v114
	v_add_f32_e32 v114, 1.0, v155
	v_exp_f32_e32 v135, v135
	v_mul_f32_e32 v155, 0xbfb8aa3b, v167
	v_exp_f32_e32 v155, v155
	v_rcp_f32_e32 v180, v114
	v_add_f32_e32 v114, 1.0, v135
	v_rcp_f32_e32 v179, v114
	v_add_f32_e32 v114, 1.0, v155
	v_rcp_f32_e32 v181, v114
	v_pk_mul_f32 v[168:169], v[136:137], v[160:161]
	v_pk_mul_f32 v[138:139], v[138:139], v[178:179]
	v_pk_mul_f32 v[170:171], v[158:159], v[170:171]
	v_pk_mul_f32 v[166:167], v[166:167], v[180:181]
.LBB0_364:
	v_or_b32_e32 v136, 48, v152
	v_ashrrev_i32_e32 v137, 31, v136
	v_lshlrev_b64 v[136:137], 12, v[136:137]
	v_mov_b32_e32 v135, v134
	v_lshl_add_u64 v[136:137], v[132:133], 0, v[136:137]
	v_cvt_pk_bf16_f32 v168, v168, v169
	v_cvt_pk_bf16_f32 v169, v138, v139
	v_cvt_pk_bf16_f32 v170, v170, v171
	v_cvt_pk_bf16_f32 v171, v166, v167
	v_mov_b32_e32 v158, v134
	v_mov_b32_e32 v159, v134
	ds_bpermute_b32 v232, v244, v168
	ds_bpermute_b32 v233, v244, v169
	ds_bpermute_b32 v234, v244, v170
	ds_bpermute_b32 v235, v244, v171
	ds_bpermute_b32 v236, v244, v136
	ds_bpermute_b32 v237, v244, v137
	v_pk_mul_f32 v[138:139], v[72:73], v[158:159]
	v_pk_mul_f32 v[166:167], v[68:69], v[158:159]
	v_pk_mul_f32 v[168:169], v[70:71], v[134:135]
	s_and_b64 vcc, exec, s[40:41]
	v_pk_mul_f32 v[170:171], v[66:67], v[134:135]
	s_waitcnt lgkmcnt(0)
	global_store_dwordx4 v[236:237], v[232:235], off
	s_cbranch_vccnz .LBB0_366
	v_max_f32_e32 v114, v168, v168
	v_max_f32_e32 v134, 0xc2a00000, v114
	v_max_f32_e32 v114, v170, v170
	v_max_f32_e32 v158, 0xc2a00000, v114
	v_mul_f32_e32 v114, 0xbfb8aa3b, v134
	v_exp_f32_e32 v114, v114
	v_mul_f32_e32 v135, 0xbfb8aa3b, v158
	v_exp_f32_e32 v135, v135
	v_max_f32_e32 v155, v171, v171
	v_add_f32_e32 v114, 1.0, v114
	v_rcp_f32_e32 v160, v114
	v_add_f32_e32 v114, 1.0, v135
	v_max_f32_e32 v135, v169, v169
	v_max_f32_e32 v135, 0xc2a00000, v135
	v_max_f32_e32 v159, 0xc2a00000, v155
	v_mul_f32_e32 v155, 0xbfb8aa3b, v135
	v_exp_f32_e32 v155, v155
	v_mul_f32_e32 v161, 0xbfb8aa3b, v159
	v_exp_f32_e32 v168, v161
	v_max_f32_e32 v138, v138, v138
	v_rcp_f32_e32 v170, v114
	v_add_f32_e32 v114, 1.0, v155
	v_max_f32_e32 v138, 0xc2a00000, v138
	v_max_f32_e32 v155, v166, v166
	v_max_f32_e32 v166, 0xc2a00000, v155
	v_mul_f32_e32 v155, 0xbfb8aa3b, v138
	v_exp_f32_e32 v155, v155
	v_rcp_f32_e32 v161, v114
	v_add_f32_e32 v114, 1.0, v168
	v_mul_f32_e32 v168, 0xbfb8aa3b, v166
	v_exp_f32_e32 v168, v168
	v_max_f32_e32 v139, v139, v139
	v_rcp_f32_e32 v171, v114
	v_add_f32_e32 v114, 1.0, v155
	v_max_f32_e32 v139, 0xc2a00000, v139
	v_max_f32_e32 v155, v167, v167
	v_max_f32_e32 v167, 0xc2a00000, v155
	v_mul_f32_e32 v155, 0xbfb8aa3b, v139
	v_rcp_f32_e32 v178, v114
	v_add_f32_e32 v114, 1.0, v168
	v_exp_f32_e32 v155, v155
	v_mul_f32_e32 v168, 0xbfb8aa3b, v167
	v_exp_f32_e32 v168, v168
	v_rcp_f32_e32 v180, v114
	v_add_f32_e32 v114, 1.0, v155
	v_rcp_f32_e32 v179, v114
	v_add_f32_e32 v114, 1.0, v168
	v_rcp_f32_e32 v181, v114
	v_pk_mul_f32 v[168:169], v[134:135], v[160:161]
	v_pk_mul_f32 v[138:139], v[138:139], v[178:179]
	v_pk_mul_f32 v[170:171], v[158:159], v[170:171]
	v_pk_mul_f32 v[166:167], v[166:167], v[180:181]
.LBB0_366:
	ds_read_b32 v134, v176 offset:512
	v_cvt_pk_bf16_f32 v168, v168, v169
	v_cvt_pk_bf16_f32 v169, v138, v139
	v_cvt_pk_bf16_f32 v170, v170, v171
	v_cvt_pk_bf16_f32 v171, v166, v167
	ds_bpermute_b32 v238, v244, v168
	ds_bpermute_b32 v239, v244, v169
	ds_bpermute_b32 v240, v244, v170
	ds_bpermute_b32 v241, v244, v171
	ds_bpermute_b32 v242, v244, v136
	ds_bpermute_b32 v243, v244, v137
	s_waitcnt lgkmcnt(0)
	v_pk_mul_f32 v[138:139], v[64:65], v[134:135] op_sel_hi:[1,0]
	v_pk_mul_f32 v[166:167], v[60:61], v[134:135] op_sel_hi:[1,0]
	v_pk_mul_f32 v[168:169], v[62:63], v[134:135] op_sel_hi:[1,0]
	s_and_b64 vcc, exec, s[40:41]
	v_pk_mul_f32 v[170:171], v[58:59], v[134:135] op_sel_hi:[1,0]
	s_waitcnt lgkmcnt(0)
	global_store_dwordx4 v[242:243], v[238:241], off offset:64
	s_cbranch_vccnz .LBB0_368
	v_max_f32_e32 v114, v168, v168
	v_max_f32_e32 v136, 0xc2a00000, v114
	v_max_f32_e32 v114, v170, v170
	v_max_f32_e32 v158, 0xc2a00000, v114
	v_mul_f32_e32 v114, 0xbfb8aa3b, v136
	v_exp_f32_e32 v114, v114
	v_mul_f32_e32 v135, 0xbfb8aa3b, v158
	v_exp_f32_e32 v135, v135
	v_add_f32_e32 v114, 1.0, v114
	v_rcp_f32_e32 v160, v114
	v_add_f32_e32 v114, 1.0, v135
	v_max_f32_e32 v135, v169, v169
	v_max_f32_e32 v137, 0xc2a00000, v135
	v_max_f32_e32 v135, v171, v171
	v_max_f32_e32 v159, 0xc2a00000, v135
	v_mul_f32_e32 v135, 0xbfb8aa3b, v137
	v_exp_f32_e32 v135, v135
	v_mul_f32_e32 v155, 0xbfb8aa3b, v159
	v_rcp_f32_e32 v170, v114
	v_exp_f32_e32 v155, v155
	v_add_f32_e32 v114, 1.0, v135
	v_max_f32_e32 v135, v138, v138
	v_max_f32_e32 v138, 0xc2a00000, v135
	v_max_f32_e32 v135, v166, v166
	v_max_f32_e32 v166, 0xc2a00000, v135
	v_mul_f32_e32 v135, 0xbfb8aa3b, v138
	v_exp_f32_e32 v135, v135
	v_rcp_f32_e32 v161, v114
	v_add_f32_e32 v114, 1.0, v155
	v_mul_f32_e32 v155, 0xbfb8aa3b, v166
	v_exp_f32_e32 v155, v155
	v_rcp_f32_e32 v171, v114
	v_add_f32_e32 v114, 1.0, v135
	v_max_f32_e32 v135, v139, v139
	v_max_f32_e32 v139, 0xc2a00000, v135
	v_max_f32_e32 v135, v167, v167
	v_max_f32_e32 v167, 0xc2a00000, v135
	v_mul_f32_e32 v135, 0xbfb8aa3b, v139
	v_rcp_f32_e32 v178, v114
	v_add_f32_e32 v114, 1.0, v155
	v_exp_f32_e32 v135, v135
	v_mul_f32_e32 v155, 0xbfb8aa3b, v167
	v_exp_f32_e32 v155, v155
	v_rcp_f32_e32 v180, v114
	v_add_f32_e32 v114, 1.0, v135
	v_rcp_f32_e32 v179, v114
	v_add_f32_e32 v114, 1.0, v155
	v_rcp_f32_e32 v181, v114
	v_pk_mul_f32 v[168:169], v[136:137], v[160:161]
	v_pk_mul_f32 v[138:139], v[138:139], v[178:179]
	v_pk_mul_f32 v[170:171], v[158:159], v[170:171]
	v_pk_mul_f32 v[166:167], v[166:167], v[180:181]
.LBB0_368:
	v_lshlrev_b64 v[136:137], 12, v[152:153]
	v_lshl_add_u64 v[136:137], v[132:133], 0, v[136:137]
	s_mov_b32 s14, 0x80000
	v_cvt_pk_bf16_f32 v168, v168, v169
	v_cvt_pk_bf16_f32 v169, v138, v139
	v_add_co_u32_e32 v138, vcc, s14, v136
	v_mov_b32_e32 v135, v134
	v_cvt_pk_bf16_f32 v170, v170, v171
	v_cvt_pk_bf16_f32 v171, v166, v167
	s_nop 0
	v_addc_co_u32_e32 v139, vcc, 0, v137, vcc
	v_mov_b32_e32 v158, v134
	v_mov_b32_e32 v159, v134
	ds_bpermute_b32 v232, v244, v168
	ds_bpermute_b32 v233, v244, v169
	ds_bpermute_b32 v234, v244, v170
	ds_bpermute_b32 v235, v244, v171
	ds_bpermute_b32 v236, v244, v138
	ds_bpermute_b32 v237, v244, v139
	v_pk_mul_f32 v[138:139], v[56:57], v[158:159]
	v_pk_mul_f32 v[166:167], v[52:53], v[158:159]
	v_pk_mul_f32 v[168:169], v[54:55], v[134:135]
	s_and_b64 vcc, exec, s[40:41]
	v_pk_mul_f32 v[170:171], v[50:51], v[134:135]
	s_waitcnt lgkmcnt(0)
	global_store_dwordx4 v[236:237], v[232:235], off
	s_cbranch_vccnz .LBB0_370
	v_max_f32_e32 v114, v168, v168
	v_max_f32_e32 v134, 0xc2a00000, v114
	v_max_f32_e32 v114, v170, v170
	v_max_f32_e32 v158, 0xc2a00000, v114
	v_mul_f32_e32 v114, 0xbfb8aa3b, v134
	v_exp_f32_e32 v114, v114
	v_mul_f32_e32 v135, 0xbfb8aa3b, v158
	v_exp_f32_e32 v135, v135
	v_max_f32_e32 v155, v171, v171
	v_add_f32_e32 v114, 1.0, v114
	v_rcp_f32_e32 v160, v114
	v_add_f32_e32 v114, 1.0, v135
	v_max_f32_e32 v135, v169, v169
	v_max_f32_e32 v135, 0xc2a00000, v135
	v_max_f32_e32 v159, 0xc2a00000, v155
	v_mul_f32_e32 v155, 0xbfb8aa3b, v135
	v_exp_f32_e32 v155, v155
	v_mul_f32_e32 v161, 0xbfb8aa3b, v159
	v_exp_f32_e32 v168, v161
	v_max_f32_e32 v138, v138, v138
	v_rcp_f32_e32 v170, v114
	v_add_f32_e32 v114, 1.0, v155
	v_max_f32_e32 v138, 0xc2a00000, v138
	v_max_f32_e32 v155, v166, v166
	v_max_f32_e32 v166, 0xc2a00000, v155
	v_mul_f32_e32 v155, 0xbfb8aa3b, v138
	v_exp_f32_e32 v155, v155
	v_rcp_f32_e32 v161, v114
	v_add_f32_e32 v114, 1.0, v168
	v_mul_f32_e32 v168, 0xbfb8aa3b, v166
	v_exp_f32_e32 v168, v168
	v_max_f32_e32 v139, v139, v139
	v_rcp_f32_e32 v171, v114
	v_add_f32_e32 v114, 1.0, v155
	v_max_f32_e32 v139, 0xc2a00000, v139
	v_max_f32_e32 v155, v167, v167
	v_max_f32_e32 v167, 0xc2a00000, v155
	v_mul_f32_e32 v155, 0xbfb8aa3b, v139
	v_rcp_f32_e32 v178, v114
	v_add_f32_e32 v114, 1.0, v168
	v_exp_f32_e32 v155, v155
	v_mul_f32_e32 v168, 0xbfb8aa3b, v167
	v_exp_f32_e32 v168, v168
	v_rcp_f32_e32 v180, v114
	v_add_f32_e32 v114, 1.0, v155
	v_rcp_f32_e32 v179, v114
	v_add_f32_e32 v114, 1.0, v168
	v_rcp_f32_e32 v181, v114
	v_pk_mul_f32 v[168:169], v[134:135], v[160:161]
	v_pk_mul_f32 v[138:139], v[138:139], v[178:179]
	v_pk_mul_f32 v[170:171], v[158:159], v[170:171]
	v_pk_mul_f32 v[166:167], v[166:167], v[180:181]
.LBB0_370:
	ds_read_b32 v134, v176 offset:576
	s_mov_b64 s[14:15], 0x80000
	v_lshl_add_u64 v[158:159], v[136:137], 0, s[14:15]
	v_cvt_pk_bf16_f32 v137, v138, v139
	v_cvt_pk_bf16_f32 v138, v170, v171
	v_cvt_pk_bf16_f32 v139, v166, v167
	v_cvt_pk_bf16_f32 v136, v168, v169
	ds_bpermute_b32 v238, v244, v136
	ds_bpermute_b32 v239, v244, v137
	ds_bpermute_b32 v240, v244, v138
	ds_bpermute_b32 v241, v244, v139
	ds_bpermute_b32 v242, v244, v158
	ds_bpermute_b32 v243, v244, v159
	s_waitcnt lgkmcnt(0)
	v_pk_mul_f32 v[168:169], v[46:47], v[134:135] op_sel_hi:[1,0]
	v_pk_mul_f32 v[166:167], v[44:45], v[134:135] op_sel_hi:[1,0]
	v_pk_mul_f32 v[138:139], v[48:49], v[134:135] op_sel_hi:[1,0]
	s_and_b64 vcc, exec, s[40:41]
	v_pk_mul_f32 v[170:171], v[42:43], v[134:135] op_sel_hi:[1,0]
	s_waitcnt lgkmcnt(0)
	global_store_dwordx4 v[242:243], v[238:241], off offset:64
	s_cbranch_vccnz .LBB0_372
	v_max_f32_e32 v114, v168, v168
	v_max_f32_e32 v136, 0xc2a00000, v114
	v_max_f32_e32 v114, v170, v170
	v_max_f32_e32 v158, 0xc2a00000, v114
	v_mul_f32_e32 v114, 0xbfb8aa3b, v136
	v_exp_f32_e32 v114, v114
	v_mul_f32_e32 v135, 0xbfb8aa3b, v158
	v_exp_f32_e32 v135, v135
	v_add_f32_e32 v114, 1.0, v114
	v_rcp_f32_e32 v160, v114
	v_add_f32_e32 v114, 1.0, v135
	v_max_f32_e32 v135, v169, v169
	v_max_f32_e32 v137, 0xc2a00000, v135
	v_max_f32_e32 v135, v171, v171
	v_max_f32_e32 v159, 0xc2a00000, v135
	v_mul_f32_e32 v135, 0xbfb8aa3b, v137
	v_exp_f32_e32 v135, v135
	v_mul_f32_e32 v155, 0xbfb8aa3b, v159
	v_rcp_f32_e32 v170, v114
	v_exp_f32_e32 v155, v155
	v_add_f32_e32 v114, 1.0, v135
	v_max_f32_e32 v135, v138, v138
	v_max_f32_e32 v138, 0xc2a00000, v135
	v_max_f32_e32 v135, v166, v166
	v_max_f32_e32 v166, 0xc2a00000, v135
	v_mul_f32_e32 v135, 0xbfb8aa3b, v138
	v_exp_f32_e32 v135, v135
	v_rcp_f32_e32 v161, v114
	v_add_f32_e32 v114, 1.0, v155
	v_mul_f32_e32 v155, 0xbfb8aa3b, v166
	v_exp_f32_e32 v155, v155
	v_rcp_f32_e32 v171, v114
	v_add_f32_e32 v114, 1.0, v135
	v_max_f32_e32 v135, v139, v139
	v_max_f32_e32 v139, 0xc2a00000, v135
	v_max_f32_e32 v135, v167, v167
	v_max_f32_e32 v167, 0xc2a00000, v135
	v_mul_f32_e32 v135, 0xbfb8aa3b, v139
	v_rcp_f32_e32 v178, v114
	v_add_f32_e32 v114, 1.0, v155
	v_exp_f32_e32 v135, v135
	v_mul_f32_e32 v155, 0xbfb8aa3b, v167
	v_exp_f32_e32 v155, v155
	v_rcp_f32_e32 v180, v114
	v_add_f32_e32 v114, 1.0, v135
	v_rcp_f32_e32 v179, v114
	v_add_f32_e32 v114, 1.0, v155
	v_rcp_f32_e32 v181, v114
	v_pk_mul_f32 v[168:169], v[136:137], v[160:161]
	v_pk_mul_f32 v[138:139], v[138:139], v[178:179]
	v_pk_mul_f32 v[170:171], v[158:159], v[170:171]
	v_pk_mul_f32 v[166:167], v[166:167], v[180:181]
.LBB0_372:
	v_lshlrev_b64 v[136:137], 12, v[152:153]
	v_lshl_add_u64 v[136:137], v[132:133], 0, v[136:137]
	s_mov_b32 s14, 0x90000
	v_cvt_pk_bf16_f32 v168, v168, v169
	v_cvt_pk_bf16_f32 v169, v138, v139
	v_add_co_u32_e32 v138, vcc, s14, v136
	v_mov_b32_e32 v135, v134
	v_cvt_pk_bf16_f32 v170, v170, v171
	v_cvt_pk_bf16_f32 v171, v166, v167
	s_nop 0
	v_addc_co_u32_e32 v139, vcc, 0, v137, vcc
	v_mov_b32_e32 v158, v134
	v_mov_b32_e32 v159, v134
	ds_bpermute_b32 v232, v244, v168
	ds_bpermute_b32 v233, v244, v169
	ds_bpermute_b32 v234, v244, v170
	ds_bpermute_b32 v235, v244, v171
	ds_bpermute_b32 v236, v244, v138
	ds_bpermute_b32 v237, v244, v139
	v_pk_mul_f32 v[138:139], v[40:41], v[158:159]
	v_pk_mul_f32 v[166:167], v[36:37], v[158:159]
	v_pk_mul_f32 v[168:169], v[38:39], v[134:135]
	s_and_b64 vcc, exec, s[40:41]
	v_pk_mul_f32 v[170:171], v[34:35], v[134:135]
	s_waitcnt lgkmcnt(0)
	global_store_dwordx4 v[236:237], v[232:235], off
	s_cbranch_vccnz .LBB0_374
	v_max_f32_e32 v114, v168, v168
	v_max_f32_e32 v134, 0xc2a00000, v114
	v_max_f32_e32 v114, v170, v170
	v_max_f32_e32 v158, 0xc2a00000, v114
	v_mul_f32_e32 v114, 0xbfb8aa3b, v134
	v_exp_f32_e32 v114, v114
	v_mul_f32_e32 v135, 0xbfb8aa3b, v158
	v_exp_f32_e32 v135, v135
	v_max_f32_e32 v155, v171, v171
	v_add_f32_e32 v114, 1.0, v114
	v_rcp_f32_e32 v160, v114
	v_add_f32_e32 v114, 1.0, v135
	v_max_f32_e32 v135, v169, v169
	v_max_f32_e32 v135, 0xc2a00000, v135
	v_max_f32_e32 v159, 0xc2a00000, v155
	v_mul_f32_e32 v155, 0xbfb8aa3b, v135
	v_exp_f32_e32 v155, v155
	v_mul_f32_e32 v161, 0xbfb8aa3b, v159
	v_exp_f32_e32 v168, v161
	v_max_f32_e32 v138, v138, v138
	v_rcp_f32_e32 v170, v114
	v_add_f32_e32 v114, 1.0, v155
	v_max_f32_e32 v138, 0xc2a00000, v138
	v_max_f32_e32 v155, v166, v166
	v_max_f32_e32 v166, 0xc2a00000, v155
	v_mul_f32_e32 v155, 0xbfb8aa3b, v138
	v_exp_f32_e32 v155, v155
	v_rcp_f32_e32 v161, v114
	v_add_f32_e32 v114, 1.0, v168
	v_mul_f32_e32 v168, 0xbfb8aa3b, v166
	v_exp_f32_e32 v168, v168
	v_max_f32_e32 v139, v139, v139
	v_rcp_f32_e32 v171, v114
	v_add_f32_e32 v114, 1.0, v155
	v_max_f32_e32 v139, 0xc2a00000, v139
	v_max_f32_e32 v155, v167, v167
	v_max_f32_e32 v167, 0xc2a00000, v155
	v_mul_f32_e32 v155, 0xbfb8aa3b, v139
	v_rcp_f32_e32 v178, v114
	v_add_f32_e32 v114, 1.0, v168
	v_exp_f32_e32 v155, v155
	v_mul_f32_e32 v168, 0xbfb8aa3b, v167
	v_exp_f32_e32 v168, v168
	v_rcp_f32_e32 v180, v114
	v_add_f32_e32 v114, 1.0, v155
	v_rcp_f32_e32 v179, v114
	v_add_f32_e32 v114, 1.0, v168
	v_rcp_f32_e32 v181, v114
	v_pk_mul_f32 v[168:169], v[134:135], v[160:161]
	v_pk_mul_f32 v[138:139], v[138:139], v[178:179]
	v_pk_mul_f32 v[170:171], v[158:159], v[170:171]
	v_pk_mul_f32 v[166:167], v[166:167], v[180:181]
.LBB0_374:
	ds_read_b32 v134, v176 offset:640
	s_mov_b64 s[14:15], 0x90000
	v_lshl_add_u64 v[158:159], v[136:137], 0, s[14:15]
	v_cvt_pk_bf16_f32 v137, v138, v139
	v_cvt_pk_bf16_f32 v138, v170, v171
	v_cvt_pk_bf16_f32 v139, v166, v167
	v_cvt_pk_bf16_f32 v136, v168, v169
	ds_bpermute_b32 v238, v244, v136
	ds_bpermute_b32 v239, v244, v137
	ds_bpermute_b32 v240, v244, v138
	ds_bpermute_b32 v241, v244, v139
	ds_bpermute_b32 v242, v244, v158
	ds_bpermute_b32 v243, v244, v159
	s_waitcnt lgkmcnt(0)
	v_pk_mul_f32 v[168:169], v[30:31], v[134:135] op_sel_hi:[1,0]
	v_pk_mul_f32 v[166:167], v[28:29], v[134:135] op_sel_hi:[1,0]
	v_pk_mul_f32 v[138:139], v[32:33], v[134:135] op_sel_hi:[1,0]
	s_and_b64 vcc, exec, s[40:41]
	v_pk_mul_f32 v[170:171], v[26:27], v[134:135] op_sel_hi:[1,0]
	s_waitcnt lgkmcnt(0)
	global_store_dwordx4 v[242:243], v[238:241], off offset:64
	s_cbranch_vccnz .LBB0_376
	v_max_f32_e32 v114, v168, v168
	v_max_f32_e32 v136, 0xc2a00000, v114
	v_max_f32_e32 v114, v170, v170
	v_max_f32_e32 v158, 0xc2a00000, v114
	v_mul_f32_e32 v114, 0xbfb8aa3b, v136
	v_exp_f32_e32 v114, v114
	v_mul_f32_e32 v135, 0xbfb8aa3b, v158
	v_exp_f32_e32 v135, v135
	v_add_f32_e32 v114, 1.0, v114
	v_rcp_f32_e32 v160, v114
	v_add_f32_e32 v114, 1.0, v135
	v_max_f32_e32 v135, v169, v169
	v_max_f32_e32 v137, 0xc2a00000, v135
	v_max_f32_e32 v135, v171, v171
	v_max_f32_e32 v159, 0xc2a00000, v135
	v_mul_f32_e32 v135, 0xbfb8aa3b, v137
	v_exp_f32_e32 v135, v135
	v_mul_f32_e32 v155, 0xbfb8aa3b, v159
	v_rcp_f32_e32 v170, v114
	v_exp_f32_e32 v155, v155
	v_add_f32_e32 v114, 1.0, v135
	v_max_f32_e32 v135, v138, v138
	v_max_f32_e32 v138, 0xc2a00000, v135
	v_max_f32_e32 v135, v166, v166
	v_max_f32_e32 v166, 0xc2a00000, v135
	v_mul_f32_e32 v135, 0xbfb8aa3b, v138
	v_exp_f32_e32 v135, v135
	v_rcp_f32_e32 v161, v114
	v_add_f32_e32 v114, 1.0, v155
	v_mul_f32_e32 v155, 0xbfb8aa3b, v166
	v_exp_f32_e32 v155, v155
	v_rcp_f32_e32 v171, v114
	v_add_f32_e32 v114, 1.0, v135
	v_max_f32_e32 v135, v139, v139
	v_max_f32_e32 v139, 0xc2a00000, v135
	v_max_f32_e32 v135, v167, v167
	v_max_f32_e32 v167, 0xc2a00000, v135
	v_mul_f32_e32 v135, 0xbfb8aa3b, v139
	v_rcp_f32_e32 v178, v114
	v_add_f32_e32 v114, 1.0, v155
	v_exp_f32_e32 v135, v135
	v_mul_f32_e32 v155, 0xbfb8aa3b, v167
	v_exp_f32_e32 v155, v155
	v_rcp_f32_e32 v180, v114
	v_add_f32_e32 v114, 1.0, v135
	v_rcp_f32_e32 v179, v114
	v_add_f32_e32 v114, 1.0, v155
	v_rcp_f32_e32 v181, v114
	v_pk_mul_f32 v[168:169], v[136:137], v[160:161]
	v_pk_mul_f32 v[138:139], v[138:139], v[178:179]
	v_pk_mul_f32 v[170:171], v[158:159], v[170:171]
	v_pk_mul_f32 v[166:167], v[166:167], v[180:181]
.LBB0_376:
	v_lshlrev_b64 v[136:137], 12, v[152:153]
	v_lshl_add_u64 v[136:137], v[132:133], 0, v[136:137]
	s_mov_b32 s14, 0xa0000
	v_cvt_pk_bf16_f32 v168, v168, v169
	v_cvt_pk_bf16_f32 v169, v138, v139
	v_add_co_u32_e32 v138, vcc, s14, v136
	v_mov_b32_e32 v135, v134
	v_cvt_pk_bf16_f32 v170, v170, v171
	v_cvt_pk_bf16_f32 v171, v166, v167
	s_nop 0
	v_addc_co_u32_e32 v139, vcc, 0, v137, vcc
	v_mov_b32_e32 v158, v134
	v_mov_b32_e32 v159, v134
	ds_bpermute_b32 v232, v244, v168
	ds_bpermute_b32 v233, v244, v169
	ds_bpermute_b32 v234, v244, v170
	ds_bpermute_b32 v235, v244, v171
	ds_bpermute_b32 v236, v244, v138
	ds_bpermute_b32 v237, v244, v139
	v_pk_mul_f32 v[138:139], v[24:25], v[158:159]
	v_pk_mul_f32 v[166:167], v[20:21], v[158:159]
	v_pk_mul_f32 v[168:169], v[22:23], v[134:135]
	s_and_b64 vcc, exec, s[40:41]
	v_pk_mul_f32 v[170:171], v[18:19], v[134:135]
	s_waitcnt lgkmcnt(0)
	global_store_dwordx4 v[236:237], v[232:235], off
	s_cbranch_vccnz .LBB0_378
	v_max_f32_e32 v114, v168, v168
	v_max_f32_e32 v134, 0xc2a00000, v114
	v_max_f32_e32 v114, v170, v170
	v_max_f32_e32 v158, 0xc2a00000, v114
	v_mul_f32_e32 v114, 0xbfb8aa3b, v134
	v_exp_f32_e32 v114, v114
	v_mul_f32_e32 v135, 0xbfb8aa3b, v158
	v_exp_f32_e32 v135, v135
	v_max_f32_e32 v155, v171, v171
	v_add_f32_e32 v114, 1.0, v114
	v_rcp_f32_e32 v160, v114
	v_add_f32_e32 v114, 1.0, v135
	v_max_f32_e32 v135, v169, v169
	v_max_f32_e32 v135, 0xc2a00000, v135
	v_max_f32_e32 v159, 0xc2a00000, v155
	v_mul_f32_e32 v155, 0xbfb8aa3b, v135
	v_exp_f32_e32 v155, v155
	v_mul_f32_e32 v161, 0xbfb8aa3b, v159
	v_exp_f32_e32 v168, v161
	v_max_f32_e32 v138, v138, v138
	v_rcp_f32_e32 v170, v114
	v_add_f32_e32 v114, 1.0, v155
	v_max_f32_e32 v138, 0xc2a00000, v138
	v_max_f32_e32 v155, v166, v166
	v_max_f32_e32 v166, 0xc2a00000, v155
	v_mul_f32_e32 v155, 0xbfb8aa3b, v138
	v_exp_f32_e32 v155, v155
	v_rcp_f32_e32 v161, v114
	v_add_f32_e32 v114, 1.0, v168
	v_mul_f32_e32 v168, 0xbfb8aa3b, v166
	v_exp_f32_e32 v168, v168
	v_max_f32_e32 v139, v139, v139
	v_rcp_f32_e32 v171, v114
	v_add_f32_e32 v114, 1.0, v155
	v_max_f32_e32 v139, 0xc2a00000, v139
	v_max_f32_e32 v155, v167, v167
	v_max_f32_e32 v167, 0xc2a00000, v155
	v_mul_f32_e32 v155, 0xbfb8aa3b, v139
	v_rcp_f32_e32 v178, v114
	v_add_f32_e32 v114, 1.0, v168
	v_exp_f32_e32 v155, v155
	v_mul_f32_e32 v168, 0xbfb8aa3b, v167
	v_exp_f32_e32 v168, v168
	v_rcp_f32_e32 v180, v114
	v_add_f32_e32 v114, 1.0, v155
	v_rcp_f32_e32 v179, v114
	v_add_f32_e32 v114, 1.0, v168
	v_rcp_f32_e32 v181, v114
	v_pk_mul_f32 v[168:169], v[134:135], v[160:161]
	v_pk_mul_f32 v[138:139], v[138:139], v[178:179]
	v_pk_mul_f32 v[170:171], v[158:159], v[170:171]
	v_pk_mul_f32 v[166:167], v[166:167], v[180:181]
.LBB0_378:
	ds_read_b32 v134, v176 offset:704
	s_mov_b64 s[14:15], 0xa0000
	v_lshl_add_u64 v[158:159], v[136:137], 0, s[14:15]
	v_cvt_pk_bf16_f32 v136, v168, v169
	v_cvt_pk_bf16_f32 v137, v138, v139
	v_cvt_pk_bf16_f32 v138, v170, v171
	v_cvt_pk_bf16_f32 v139, v166, v167
	ds_bpermute_b32 v238, v244, v136
	ds_bpermute_b32 v239, v244, v137
	ds_bpermute_b32 v240, v244, v138
	ds_bpermute_b32 v241, v244, v139
	ds_bpermute_b32 v242, v244, v158
	ds_bpermute_b32 v243, v244, v159
	s_waitcnt lgkmcnt(0)
	v_pk_mul_f32 v[166:167], v[14:15], v[134:135] op_sel_hi:[1,0]
	s_and_b64 vcc, exec, s[40:41]
	v_pk_mul_f32 v[136:137], v[16:17], v[134:135] op_sel_hi:[1,0]
	v_pk_mul_f32 v[138:139], v[12:13], v[134:135] op_sel_hi:[1,0]
	v_pk_mul_f32 v[168:169], v[10:11], v[134:135] op_sel_hi:[1,0]
	s_waitcnt lgkmcnt(0)
	global_store_dwordx4 v[242:243], v[238:241], off offset:64
	s_cbranch_vccnz .LBB0_380
	v_max_f32_e32 v114, v166, v166
	v_max_f32_e32 v158, 0xc2a00000, v114
	v_max_f32_e32 v114, v168, v168
	v_max_f32_e32 v160, 0xc2a00000, v114
	v_mul_f32_e32 v114, 0xbfb8aa3b, v158
	v_exp_f32_e32 v114, v114
	v_mul_f32_e32 v135, 0xbfb8aa3b, v160
	v_exp_f32_e32 v135, v135
	v_add_f32_e32 v114, 1.0, v114
	v_rcp_f32_e32 v166, v114
	v_add_f32_e32 v114, 1.0, v135
	v_max_f32_e32 v135, v167, v167
	v_max_f32_e32 v159, 0xc2a00000, v135
	v_max_f32_e32 v135, v169, v169
	v_max_f32_e32 v161, 0xc2a00000, v135
	v_mul_f32_e32 v135, 0xbfb8aa3b, v159
	v_exp_f32_e32 v135, v135
	v_mul_f32_e32 v155, 0xbfb8aa3b, v161
	v_rcp_f32_e32 v168, v114
	v_exp_f32_e32 v155, v155
	v_add_f32_e32 v114, 1.0, v135
	v_max_f32_e32 v135, v136, v136
	v_max_f32_e32 v136, 0xc2a00000, v135
	v_max_f32_e32 v135, v138, v138
	v_max_f32_e32 v138, 0xc2a00000, v135
	v_mul_f32_e32 v135, 0xbfb8aa3b, v136
	v_exp_f32_e32 v135, v135
	v_rcp_f32_e32 v167, v114
	v_add_f32_e32 v114, 1.0, v155
	v_mul_f32_e32 v155, 0xbfb8aa3b, v138
	v_exp_f32_e32 v155, v155
	v_rcp_f32_e32 v169, v114
	v_add_f32_e32 v114, 1.0, v135
	v_max_f32_e32 v135, v137, v137
	v_max_f32_e32 v137, 0xc2a00000, v135
	v_max_f32_e32 v135, v139, v139
	v_max_f32_e32 v139, 0xc2a00000, v135
	v_mul_f32_e32 v135, 0xbfb8aa3b, v137
	v_rcp_f32_e32 v170, v114
	v_add_f32_e32 v114, 1.0, v155
	v_exp_f32_e32 v135, v135
	v_mul_f32_e32 v155, 0xbfb8aa3b, v139
	v_exp_f32_e32 v155, v155
	v_rcp_f32_e32 v178, v114
	v_add_f32_e32 v114, 1.0, v135
	v_rcp_f32_e32 v171, v114
	v_add_f32_e32 v114, 1.0, v155
	v_rcp_f32_e32 v179, v114
	v_pk_mul_f32 v[166:167], v[158:159], v[166:167]
	v_pk_mul_f32 v[136:137], v[136:137], v[170:171]
	v_pk_mul_f32 v[168:169], v[160:161], v[168:169]
	v_pk_mul_f32 v[138:139], v[138:139], v[178:179]
.LBB0_380:
	v_lshlrev_b64 v[158:159], 12, v[152:153]
	v_lshl_add_u64 v[132:133], v[132:133], 0, v[158:159]
	s_mov_b32 s14, 0xb0000
	v_cvt_pk_bf16_f32 v166, v166, v167
	v_cvt_pk_bf16_f32 v167, v136, v137
	v_add_co_u32_e32 v136, vcc, s14, v132
	v_mov_b32_e32 v135, v134
	s_nop 0
	v_addc_co_u32_e32 v137, vcc, 0, v133, vcc
	v_cvt_pk_bf16_f32 v168, v168, v169
	v_cvt_pk_bf16_f32 v169, v138, v139
	ds_bpermute_b32 v232, v244, v166
	ds_bpermute_b32 v233, v244, v167
	ds_bpermute_b32 v234, v244, v168
	ds_bpermute_b32 v235, v244, v169
	ds_bpermute_b32 v236, v244, v136
	ds_bpermute_b32 v237, v244, v137
	v_mov_b32_e32 v136, v134
	v_mov_b32_e32 v137, v134
	v_pk_mul_f32 v[138:139], v[8:9], v[136:137]
	v_pk_mul_f32 v[168:169], v[6:7], v[134:135]
	v_pk_mul_f32 v[166:167], v[4:5], v[136:137]
	s_and_b64 vcc, exec, s[40:41]
	v_pk_mul_f32 v[134:135], v[2:3], v[134:135]
	s_waitcnt lgkmcnt(0)
	global_store_dwordx4 v[236:237], v[232:235], off
	s_cbranch_vccnz .LBB0_382
	v_max_f32_e32 v114, v168, v168
	v_max_f32_e32 v136, 0xc2a00000, v114
	v_max_f32_e32 v114, v134, v134
	v_max_f32_e32 v134, 0xc2a00000, v114
	v_mul_f32_e32 v114, 0xbfb8aa3b, v136
	v_exp_f32_e32 v114, v114
	v_mul_f32_e32 v137, 0xbfb8aa3b, v134
	v_exp_f32_e32 v137, v137
	v_max_f32_e32 v135, v135, v135
	v_add_f32_e32 v114, 1.0, v114
	v_rcp_f32_e32 v158, v114
	v_add_f32_e32 v114, 1.0, v137
	v_max_f32_e32 v137, v169, v169
	v_max_f32_e32 v137, 0xc2a00000, v137
	v_mul_f32_e32 v153, 0xbfb8aa3b, v137
	v_exp_f32_e32 v153, v153
	v_max_f32_e32 v135, 0xc2a00000, v135
	v_mul_f32_e32 v155, 0xbfb8aa3b, v135
	v_exp_f32_e32 v155, v155
	v_max_f32_e32 v138, v138, v138
	v_rcp_f32_e32 v160, v114
	v_add_f32_e32 v114, 1.0, v153
	v_max_f32_e32 v138, 0xc2a00000, v138
	v_max_f32_e32 v153, v166, v166
	v_max_f32_e32 v166, 0xc2a00000, v153
	v_mul_f32_e32 v153, 0xbfb8aa3b, v138
	v_exp_f32_e32 v153, v153
	v_rcp_f32_e32 v159, v114
	v_add_f32_e32 v114, 1.0, v155
	v_mul_f32_e32 v155, 0xbfb8aa3b, v166
	v_exp_f32_e32 v155, v155
	v_max_f32_e32 v139, v139, v139
	v_rcp_f32_e32 v161, v114
	v_add_f32_e32 v114, 1.0, v153
	v_max_f32_e32 v139, 0xc2a00000, v139
	v_max_f32_e32 v153, v167, v167
	v_max_f32_e32 v167, 0xc2a00000, v153
	v_mul_f32_e32 v153, 0xbfb8aa3b, v139
	v_rcp_f32_e32 v170, v114
	v_add_f32_e32 v114, 1.0, v155
	v_exp_f32_e32 v153, v153
	v_mul_f32_e32 v155, 0xbfb8aa3b, v167
	v_exp_f32_e32 v155, v155
	v_rcp_f32_e32 v178, v114
	v_add_f32_e32 v114, 1.0, v153
	v_rcp_f32_e32 v171, v114
	v_add_f32_e32 v114, 1.0, v155
	v_rcp_f32_e32 v179, v114
	v_pk_mul_f32 v[168:169], v[136:137], v[158:159]
	v_pk_mul_f32 v[138:139], v[138:139], v[170:171]
	v_pk_mul_f32 v[134:135], v[134:135], v[160:161]
	v_pk_mul_f32 v[166:167], v[166:167], v[178:179]

.LBB0_384:
	s_and_b64 vcc, exec, s[40:41]
	s_cbranch_vccz .LBB0_383
	v_lshlrev_b32_e32 v155, 2, v177
	global_load_dwordx4 v[136:139], v155, s[44:45]
	global_load_dwordx4 v[132:135], v155, s[44:45] offset:16
	s_waitcnt lgkmcnt(0)
	v_mul_f32_e32 v160, v128, v154
	v_mul_f32_e32 v161, v129, v154
	v_mul_f32_e32 v166, v130, v154
	v_mul_f32_e32 v167, v131, v154
	v_mul_f32_e32 v168, v124, v154
	v_mul_f32_e32 v169, v125, v154
	v_mul_f32_e32 v170, v126, v154
	v_mul_f32_e32 v171, v127, v154
	global_load_dwordx4 v[124:127], v155, s[44:45] offset:144
	global_load_dwordx4 v[128:131], v155, s[44:45] offset:128
	v_ashrrev_i32_e32 v153, 31, v152
	v_lshlrev_b64 v[158:159], 12, v[152:153]
	v_max_f32_e32 v153, 0xc2a00000, v160
	v_max_f32_e32 v155, 0xc2a00000, v161
	v_max_f32_e32 v160, 0xc2a00000, v166
	v_max_f32_e32 v161, 0xc2a00000, v167
	v_max_f32_e32 v166, 0xc2a00000, v168
	v_max_f32_e32 v167, 0xc2a00000, v169
	v_max_f32_e32 v168, 0xc2a00000, v170
	v_max_f32_e32 v169, 0xc2a00000, v171
	v_mul_f32_e32 v153, 0xbfb8aa3b, v153
	v_mul_f32_e32 v155, 0xbfb8aa3b, v155
	v_mul_f32_e32 v168, 0xbfb8aa3b, v168
	v_mul_f32_e32 v169, 0xbfb8aa3b, v169
	v_exp_f32_e32 v153, v153
	v_exp_f32_e32 v155, v155
	v_mul_f32_e32 v160, 0xbfb8aa3b, v160
	v_mul_f32_e32 v161, 0xbfb8aa3b, v161
	v_exp_f32_e32 v168, v168
	v_exp_f32_e32 v169, v169
	v_exp_f32_e32 v160, v160
	v_exp_f32_e32 v161, v161
	v_mul_f32_e32 v120, v120, v154
	v_max_f32_e32 v120, 0xc2a00000, v120
	v_add_f32_e32 v153, 1.0, v153
	v_add_f32_e32 v155, 1.0, v155
	v_mul_f32_e32 v121, v121, v154
	v_lshlrev_b32_e32 v114, 1, v177
	v_mul_f32_e32 v166, 0xbfb8aa3b, v166
	v_mul_f32_e32 v167, 0xbfb8aa3b, v167
	v_lshl_add_u64 v[158:159], s[42:43], 0, v[158:159]
	v_add_f32_e32 v168, 1.0, v168
	v_add_f32_e32 v169, 1.0, v169
	v_rcp_f32_e32 v153, v153
	v_rcp_f32_e32 v181, v155
	v_mul_f32_e32 v120, 0xbfb8aa3b, v120
	v_max_f32_e32 v121, 0xc2a00000, v121
	v_exp_f32_e32 v170, v166
	v_exp_f32_e32 v171, v167
	v_lshl_add_u64 v[166:167], v[158:159], 0, v[114:115]
	v_add_f32_e32 v158, 1.0, v160
	v_add_f32_e32 v159, 1.0, v161
	v_rcp_f32_e32 v168, v168
	v_rcp_f32_e32 v182, v169
	v_exp_f32_e32 v120, v120
	v_mul_f32_e32 v121, 0xbfb8aa3b, v121
	v_rcp_f32_e32 v158, v158
	v_rcp_f32_e32 v159, v159
	v_exp_f32_e32 v121, v121
	v_add_f32_e32 v120, 1.0, v120
	v_rcp_f32_e32 v120, v120
	v_mul_f32_e32 v116, v116, v154
	v_add_f32_e32 v121, 1.0, v121
	v_rcp_f32_e32 v121, v121
	v_add_f32_e32 v160, 1.0, v170
	v_add_f32_e32 v161, 1.0, v171
	v_max_f32_e32 v116, 0xc2a00000, v116
	v_mul_f32_e32 v117, v117, v154
	v_rcp_f32_e32 v160, v160
	v_rcp_f32_e32 v161, v161
	v_mul_f32_e32 v116, 0xbfb8aa3b, v116
	v_max_f32_e32 v117, 0xc2a00000, v117
	v_exp_f32_e32 v116, v116
	v_mul_f32_e32 v117, 0xbfb8aa3b, v117
	v_exp_f32_e32 v117, v117
	s_mov_b64 s[14:15], 0x80000
	v_add_f32_e32 v116, 1.0, v116
	v_rcp_f32_e32 v116, v116
	v_add_f32_e32 v117, 1.0, v117
	s_waitcnt vmcnt(0)
	v_sub_f32_e32 v180, 1.0, v136
	v_sub_f32_e32 v179, 1.0, v137
	v_sub_f32_e32 v169, 1.0, v134
	v_sub_f32_e32 v155, 1.0, v135
	v_fma_f32 v153, v180, v153, v136
	v_fma_f32 v181, v179, v181, v137
	v_sub_f32_e32 v178, 1.0, v138
	v_sub_f32_e32 v177, 1.0, v139
	v_fma_f32 v168, v169, v168, v134
	v_fma_f32 v182, v155, v182, v135
	v_log_f32_e32 v153, v153
	v_log_f32_e32 v181, v181
	v_fma_f32 v158, v178, v158, v138
	v_fma_f32 v159, v177, v159, v139
	v_log_f32_e32 v168, v168
	v_log_f32_e32 v182, v182
	v_log_f32_e32 v158, v158
	v_log_f32_e32 v159, v159
	v_cvt_pk_f16_f32 v194, v153, v181
	v_sub_f32_e32 v153, 1.0, v128
	v_cvt_pk_f16_f32 v197, v168, v182
	v_fma_f32 v120, v153, v120, v128
	v_sub_f32_e32 v168, 1.0, v129
	v_cvt_pk_f16_f32 v195, v158, v159
	v_log_f32_e32 v158, v120
	v_fma_f32 v120, v168, v121, v129
	v_log_f32_e32 v159, v120
	v_mul_f32_e32 v120, v122, v154
	v_max_f32_e32 v120, 0xc2a00000, v120
	v_mul_f32_e32 v121, v123, v154
	v_mul_f32_e32 v120, 0xbfb8aa3b, v120
	v_max_f32_e32 v121, 0xc2a00000, v121
	v_exp_f32_e32 v120, v120
	v_mul_f32_e32 v121, 0xbfb8aa3b, v121
	v_exp_f32_e32 v122, v121
	v_sub_f32_e32 v171, 1.0, v132
	v_sub_f32_e32 v170, 1.0, v133
	v_add_f32_e32 v120, 1.0, v120
	v_fma_f32 v160, v171, v160, v132
	v_fma_f32 v161, v170, v161, v133
	v_rcp_f32_e32 v120, v120
	v_add_f32_e32 v122, 1.0, v122
	v_log_f32_e32 v160, v160
	v_log_f32_e32 v161, v161
	v_rcp_f32_e32 v123, v122
	v_sub_f32_e32 v121, 1.0, v130
	v_rcp_f32_e32 v117, v117
	v_fma_f32 v120, v121, v120, v130
	v_sub_f32_e32 v122, 1.0, v131
	v_cvt_pk_f16_f32 v196, v160, v161
	v_log_f32_e32 v160, v120
	v_fma_f32 v120, v122, v123, v131
	v_sub_f32_e32 v123, 1.0, v124
	v_log_f32_e32 v161, v120
	v_fma_f32 v116, v123, v116, v124
	v_sub_f32_e32 v120, 1.0, v125
	v_log_f32_e32 v181, v116
	v_fma_f32 v116, v120, v117, v125
	v_log_f32_e32 v182, v116
	v_mul_f32_e32 v116, v118, v154
	v_max_f32_e32 v116, 0xc2a00000, v116
	v_mul_f32_e32 v117, v119, v154
	v_mul_f32_e32 v116, 0xbfb8aa3b, v116
	v_max_f32_e32 v117, 0xc2a00000, v117
	v_exp_f32_e32 v116, v116
	v_mul_f32_e32 v117, 0xbfb8aa3b, v117
	v_exp_f32_e32 v117, v117
	v_sub_f32_e32 v118, 1.0, v126
	v_add_f32_e32 v116, 1.0, v116
	v_rcp_f32_e32 v116, v116
	v_add_f32_e32 v117, 1.0, v117
	v_rcp_f32_e32 v117, v117
	v_sub_f32_e32 v119, 1.0, v127
	v_fma_f32 v116, v118, v116, v126
	v_log_f32_e32 v154, v116
	v_fma_f32 v116, v119, v117, v127
	v_log_f32_e32 v183, v116
	ds_read2_b32 v[116:117], v176 offset0:16 offset1:32
	ds_bpermute_b32 v232, v244, v194
	ds_bpermute_b32 v233, v244, v195
	ds_bpermute_b32 v234, v244, v196
	ds_bpermute_b32 v235, v244, v197
	ds_bpermute_b32 v236, v244, v166
	ds_bpermute_b32 v237, v244, v167
	s_waitcnt lgkmcnt(0)
	v_mul_f32_e32 v106, v106, v116
	v_max_f32_e32 v106, 0xc2a00000, v106
	v_mul_f32_e32 v106, 0xbfb8aa3b, v106
	v_exp_f32_e32 v106, v106
	v_mul_f32_e32 v110, v110, v116
	v_max_f32_e32 v110, 0xc2a00000, v110
	v_mul_f32_e32 v111, v111, v116
	v_mul_f32_e32 v110, 0xbfb8aa3b, v110
	v_max_f32_e32 v111, 0xc2a00000, v111
	v_mul_f32_e32 v107, v107, v116
	v_exp_f32_e32 v110, v110
	v_mul_f32_e32 v111, 0xbfb8aa3b, v111
	v_add_f32_e32 v106, 1.0, v106
	v_max_f32_e32 v107, 0xc2a00000, v107
	v_exp_f32_e32 v111, v111
	v_rcp_f32_e32 v106, v106
	v_mul_f32_e32 v107, 0xbfb8aa3b, v107
	v_exp_f32_e32 v107, v107
	v_cvt_pk_f16_f32 v194, v158, v159
	v_or_b32_e32 v158, 16, v152
	v_add_f32_e32 v110, 1.0, v110
	v_mul_f32_e32 v112, v112, v116
	v_mul_f32_e32 v113, v113, v116
	v_cvt_pk_f16_f32 v197, v154, v183
	v_ashrrev_i32_e32 v159, 31, v158
	v_rcp_f32_e32 v154, v110
	v_add_f32_e32 v110, 1.0, v111
	v_max_f32_e32 v112, 0xc2a00000, v112
	v_max_f32_e32 v113, 0xc2a00000, v113
	v_fma_f32 v106, v171, v106, v132
	v_cvt_pk_f16_f32 v195, v160, v161
	v_rcp_f32_e32 v160, v110
	v_lshlrev_b64 v[110:111], 12, v[158:159]
	v_mul_f32_e32 v112, 0xbfb8aa3b, v112
	v_mul_f32_e32 v113, 0xbfb8aa3b, v113
	v_log_f32_e32 v159, v106
	v_add_f32_e32 v106, 1.0, v107
	v_mul_f32_e32 v107, v108, v116
	v_exp_f32_e32 v112, v112
	v_exp_f32_e32 v113, v113
	v_max_f32_e32 v107, 0xc2a00000, v107
	v_mul_f32_e32 v108, v109, v116
	v_mul_f32_e32 v107, 0xbfb8aa3b, v107
	v_max_f32_e32 v108, 0xc2a00000, v108
	v_exp_f32_e32 v107, v107
	v_mul_f32_e32 v108, 0xbfb8aa3b, v108
	v_exp_f32_e32 v108, v108
	v_add_f32_e32 v112, 1.0, v112
	v_add_f32_e32 v113, 1.0, v113
	v_rcp_f32_e32 v112, v112
	v_rcp_f32_e32 v113, v113
	v_mul_f32_e32 v98, v98, v116
	v_rcp_f32_e32 v106, v106
	v_add_f32_e32 v107, 1.0, v107
	v_max_f32_e32 v98, 0xc2a00000, v98
	v_rcp_f32_e32 v107, v107
	v_add_f32_e32 v108, 1.0, v108
	v_mul_f32_e32 v98, 0xbfb8aa3b, v98
	v_rcp_f32_e32 v108, v108
	v_exp_f32_e32 v98, v98
	v_fma_f32 v112, v178, v112, v138
	v_fma_f32 v113, v177, v113, v139
	v_log_f32_e32 v112, v112
	v_log_f32_e32 v113, v113
	v_fma_f32 v106, v170, v106, v133
	v_log_f32_e32 v109, v106
	v_fma_f32 v106, v169, v107, v134
	v_mul_f32_e32 v102, v102, v116
	v_mul_f32_e32 v99, v99, v116
	v_fma_f32 v154, v180, v154, v136
	v_fma_f32 v158, v179, v160, v137
	v_log_f32_e32 v160, v106
	v_fma_f32 v106, v155, v108, v135
	v_max_f32_e32 v102, 0xc2a00000, v102
	v_add_f32_e32 v98, 1.0, v98
	v_max_f32_e32 v99, 0xc2a00000, v99
	v_log_f32_e32 v154, v154
	v_log_f32_e32 v158, v158
	v_log_f32_e32 v161, v106
	v_mul_f32_e32 v102, 0xbfb8aa3b, v102
	v_rcp_f32_e32 v98, v98
	v_mul_f32_e32 v99, 0xbfb8aa3b, v99
	v_cvt_pk_f16_f32 v107, v112, v113
	v_exp_f32_e32 v112, v102
	v_mul_f32_e32 v102, v103, v116
	v_exp_f32_e32 v99, v99
	v_max_f32_e32 v102, 0xc2a00000, v102
	v_lshl_add_u64 v[110:111], s[42:43], 0, v[110:111]
	v_mul_f32_e32 v102, 0xbfb8aa3b, v102
	v_cvt_pk_f16_f32 v106, v154, v158
	v_cvt_pk_f16_f32 v108, v159, v109
	v_cvt_pk_f16_f32 v109, v160, v161
	v_exp_f32_e32 v113, v102
	v_lshl_add_u64 v[102:103], v[110:111], 0, v[114:115]
	v_fma_f32 v98, v123, v98, v124
	s_waitcnt lgkmcnt(0)
	global_store_dwordx4 v[236:237], v[232:235], off
	ds_bpermute_b32 v238, v244, v106
	ds_bpermute_b32 v239, v244, v107
	ds_bpermute_b32 v240, v244, v108
	ds_bpermute_b32 v241, v244, v109
	ds_bpermute_b32 v242, v244, v102
	ds_bpermute_b32 v243, v244, v103
	v_mul_f32_e32 v104, v104, v116
	v_mul_f32_e32 v105, v105, v116
	v_log_f32_e32 v108, v98
	v_add_f32_e32 v98, 1.0, v99
	v_mul_f32_e32 v99, v100, v116
	v_max_f32_e32 v99, 0xc2a00000, v99
	v_mul_f32_e32 v100, v101, v116
	v_max_f32_e32 v104, 0xc2a00000, v104
	v_max_f32_e32 v105, 0xc2a00000, v105
	v_mul_f32_e32 v99, 0xbfb8aa3b, v99
	v_max_f32_e32 v100, 0xc2a00000, v100
	v_mul_f32_e32 v104, 0xbfb8aa3b, v104
	v_mul_f32_e32 v105, 0xbfb8aa3b, v105
	v_exp_f32_e32 v99, v99
	v_mul_f32_e32 v100, 0xbfb8aa3b, v100
	v_exp_f32_e32 v104, v104
	v_exp_f32_e32 v105, v105
	v_exp_f32_e32 v100, v100
	v_rcp_f32_e32 v98, v98
	v_add_f32_e32 v99, 1.0, v99
	v_add_f32_e32 v110, 1.0, v112
	v_add_f32_e32 v111, 1.0, v113
	v_add_f32_e32 v104, 1.0, v104
	v_add_f32_e32 v105, 1.0, v105
	v_rcp_f32_e32 v99, v99
	v_add_f32_e32 v100, 1.0, v100
	v_rcp_f32_e32 v110, v110
	v_rcp_f32_e32 v111, v111
	v_rcp_f32_e32 v104, v104
	v_rcp_f32_e32 v105, v105
	v_rcp_f32_e32 v100, v100
	v_mul_f32_e32 v90, v90, v117
	v_fma_f32 v98, v120, v98, v125
	v_mul_f32_e32 v94, v94, v117
	v_max_f32_e32 v90, 0xc2a00000, v90
	v_log_f32_e32 v101, v98
	v_fma_f32 v98, v118, v99, v126
	v_max_f32_e32 v94, 0xc2a00000, v94
	v_mul_f32_e32 v90, 0xbfb8aa3b, v90
	v_fma_f32 v106, v153, v110, v128
	v_fma_f32 v107, v168, v111, v129
	v_fma_f32 v104, v121, v104, v130
	v_fma_f32 v105, v122, v105, v131
	v_log_f32_e32 v109, v98
	v_fma_f32 v98, v119, v100, v127
	v_mul_f32_e32 v94, 0xbfb8aa3b, v94
	v_exp_f32_e32 v90, v90
	v_log_f32_e32 v106, v106
	v_log_f32_e32 v107, v107
	v_log_f32_e32 v104, v104
	v_log_f32_e32 v105, v105
	v_log_f32_e32 v110, v98
	v_exp_f32_e32 v94, v94
	v_mul_f32_e32 v95, v95, v117
	v_max_f32_e32 v95, 0xc2a00000, v95
	v_mul_f32_e32 v91, v91, v117
	v_mul_f32_e32 v95, 0xbfb8aa3b, v95
	v_add_f32_e32 v90, 1.0, v90
	v_max_f32_e32 v91, 0xc2a00000, v91
	v_cvt_pk_f16_f32 v98, v106, v107
	v_cvt_pk_f16_f32 v99, v104, v105
	v_cvt_pk_f16_f32 v100, v108, v101
	v_cvt_pk_f16_f32 v101, v109, v110
	v_exp_f32_e32 v95, v95
	v_add_f32_e32 v94, 1.0, v94
	v_rcp_f32_e32 v90, v90
	v_mul_f32_e32 v91, 0xbfb8aa3b, v91
	s_waitcnt lgkmcnt(0)
	global_store_dwordx4 v[242:243], v[238:241], off
	ds_bpermute_b32 v232, v244, v98
	ds_bpermute_b32 v233, v244, v99
	ds_bpermute_b32 v234, v244, v100
	ds_bpermute_b32 v235, v244, v101
	ds_bpermute_b32 v236, v244, v102
	ds_bpermute_b32 v237, v244, v103
	v_exp_f32_e32 v91, v91
	v_fma_f32 v90, v171, v90, v132
	v_rcp_f32_e32 v100, v94
	v_or_b32_e32 v98, 32, v152
	v_ashrrev_i32_e32 v99, 31, v98
	v_add_f32_e32 v94, 1.0, v95
	v_rcp_f32_e32 v101, v94
	v_lshlrev_b64 v[94:95], 12, v[98:99]
	v_fma_f32 v98, v180, v100, v136
	v_log_f32_e32 v100, v90
	v_add_f32_e32 v90, 1.0, v91
	v_mul_f32_e32 v91, v92, v117
	v_mul_f32_e32 v96, v96, v117
	v_mul_f32_e32 v97, v97, v117
	v_max_f32_e32 v91, 0xc2a00000, v91
	v_mul_f32_e32 v92, v93, v117
	v_max_f32_e32 v96, 0xc2a00000, v96
	v_max_f32_e32 v97, 0xc2a00000, v97
	v_mul_f32_e32 v91, 0xbfb8aa3b, v91
	v_max_f32_e32 v92, 0xc2a00000, v92
	v_mul_f32_e32 v96, 0xbfb8aa3b, v96
	v_mul_f32_e32 v97, 0xbfb8aa3b, v97
	v_exp_f32_e32 v91, v91
	v_mul_f32_e32 v92, 0xbfb8aa3b, v92
	v_exp_f32_e32 v96, v96
	v_exp_f32_e32 v97, v97
	v_exp_f32_e32 v92, v92
	v_mul_f32_e32 v82, v82, v117
	v_rcp_f32_e32 v90, v90
	v_add_f32_e32 v91, 1.0, v91
	v_max_f32_e32 v82, 0xc2a00000, v82
	v_add_f32_e32 v96, 1.0, v96
	v_add_f32_e32 v97, 1.0, v97
	v_rcp_f32_e32 v91, v91
	v_add_f32_e32 v92, 1.0, v92
	v_mul_f32_e32 v82, 0xbfb8aa3b, v82
	v_rcp_f32_e32 v96, v96
	v_rcp_f32_e32 v97, v97
	v_rcp_f32_e32 v92, v92
	v_exp_f32_e32 v82, v82
	v_fma_f32 v90, v170, v90, v133
	v_log_f32_e32 v93, v90
	v_fma_f32 v90, v169, v91, v134
	v_mul_f32_e32 v83, v83, v117
	v_fma_f32 v99, v179, v101, v137
	v_fma_f32 v96, v178, v96, v138
	v_fma_f32 v97, v177, v97, v139
	v_log_f32_e32 v101, v90
	v_fma_f32 v90, v155, v92, v135
	v_add_f32_e32 v82, 1.0, v82
	v_max_f32_e32 v83, 0xc2a00000, v83
	v_log_f32_e32 v98, v98
	v_log_f32_e32 v99, v99
	v_log_f32_e32 v96, v96
	v_log_f32_e32 v97, v97
	v_log_f32_e32 v102, v90
	v_rcp_f32_e32 v82, v82
	v_mul_f32_e32 v83, 0xbfb8aa3b, v83
	v_exp_f32_e32 v83, v83
	v_lshl_add_u64 v[94:95], s[42:43], 0, v[94:95]
	v_cvt_pk_f16_f32 v90, v98, v99
	v_cvt_pk_f16_f32 v91, v96, v97
	v_cvt_pk_f16_f32 v92, v100, v93
	v_cvt_pk_f16_f32 v93, v101, v102
	v_lshl_add_u64 v[94:95], v[94:95], 0, v[114:115]
	v_fma_f32 v82, v123, v82, v124
	s_waitcnt lgkmcnt(0)
	global_store_dwordx4 v[236:237], v[232:235], off offset:64
	ds_bpermute_b32 v238, v244, v90
	ds_bpermute_b32 v239, v244, v91
	ds_bpermute_b32 v240, v244, v92
	ds_bpermute_b32 v241, v244, v93
	ds_bpermute_b32 v242, v244, v94
	ds_bpermute_b32 v243, v244, v95
	v_mul_f32_e32 v86, v86, v117
	v_mul_f32_e32 v87, v87, v117
	v_log_f32_e32 v90, v82
	v_add_f32_e32 v82, 1.0, v83
	v_mul_f32_e32 v83, v84, v117
	v_max_f32_e32 v83, 0xc2a00000, v83
	v_mul_f32_e32 v84, v85, v117
	v_mul_f32_e32 v83, 0xbfb8aa3b, v83
	v_max_f32_e32 v84, 0xc2a00000, v84
	v_exp_f32_e32 v83, v83
	v_mul_f32_e32 v84, 0xbfb8aa3b, v84
	v_exp_f32_e32 v84, v84
	v_rcp_f32_e32 v82, v82
	v_add_f32_e32 v83, 1.0, v83
	v_rcp_f32_e32 v83, v83
	v_add_f32_e32 v84, 1.0, v84
	v_rcp_f32_e32 v84, v84
	v_mul_f32_e32 v88, v88, v117
	v_mul_f32_e32 v89, v89, v117
	v_max_f32_e32 v86, 0xc2a00000, v86
	v_max_f32_e32 v87, 0xc2a00000, v87
	v_max_f32_e32 v88, 0xc2a00000, v88
	v_max_f32_e32 v89, 0xc2a00000, v89
	v_fma_f32 v82, v120, v82, v125
	v_mul_f32_e32 v86, 0xbfb8aa3b, v86
	v_mul_f32_e32 v87, 0xbfb8aa3b, v87
	v_mul_f32_e32 v88, 0xbfb8aa3b, v88
	v_mul_f32_e32 v89, 0xbfb8aa3b, v89
	v_log_f32_e32 v91, v82
	v_fma_f32 v82, v118, v83, v126
	v_exp_f32_e32 v86, v86
	v_exp_f32_e32 v87, v87
	v_exp_f32_e32 v88, v88
	v_exp_f32_e32 v89, v89
	v_log_f32_e32 v92, v82
	v_fma_f32 v82, v119, v84, v127
	v_log_f32_e32 v93, v82
	ds_read2_b32 v[82:83], v176 offset0:48 offset1:128
	v_add_f32_e32 v86, 1.0, v86
	v_add_f32_e32 v87, 1.0, v87
	v_add_f32_e32 v88, 1.0, v88
	v_add_f32_e32 v89, 1.0, v89
	v_rcp_f32_e32 v86, v86
	v_rcp_f32_e32 v87, v87
	v_rcp_f32_e32 v88, v88
	v_rcp_f32_e32 v89, v89
	s_waitcnt lgkmcnt(0)
	v_mul_f32_e32 v74, v74, v82
	v_mul_f32_e32 v78, v78, v82
	v_max_f32_e32 v74, 0xc2a00000, v74
	v_max_f32_e32 v78, 0xc2a00000, v78
	v_mul_f32_e32 v74, 0xbfb8aa3b, v74
	v_fma_f32 v86, v153, v86, v128
	v_fma_f32 v87, v168, v87, v129
	v_fma_f32 v88, v121, v88, v130
	v_fma_f32 v89, v122, v89, v131
	v_mul_f32_e32 v78, 0xbfb8aa3b, v78
	v_exp_f32_e32 v74, v74
	v_log_f32_e32 v86, v86
	v_log_f32_e32 v87, v87
	v_log_f32_e32 v88, v88
	v_log_f32_e32 v89, v89
	v_exp_f32_e32 v78, v78
	v_mul_f32_e32 v79, v79, v82
	v_max_f32_e32 v79, 0xc2a00000, v79
	v_mul_f32_e32 v75, v75, v82
	v_mul_f32_e32 v79, 0xbfb8aa3b, v79
	v_add_f32_e32 v74, 1.0, v74
	v_max_f32_e32 v75, 0xc2a00000, v75
	v_cvt_pk_f16_f32 v84, v86, v87
	v_cvt_pk_f16_f32 v85, v88, v89
	v_cvt_pk_f16_f32 v86, v90, v91
	v_cvt_pk_f16_f32 v87, v92, v93
	v_exp_f32_e32 v79, v79
	v_add_f32_e32 v78, 1.0, v78
	v_rcp_f32_e32 v74, v74
	v_mul_f32_e32 v75, 0xbfb8aa3b, v75
	s_waitcnt lgkmcnt(0)
	global_store_dwordx4 v[242:243], v[238:241], off
	ds_bpermute_b32 v232, v244, v84
	ds_bpermute_b32 v233, v244, v85
	ds_bpermute_b32 v234, v244, v86
	ds_bpermute_b32 v235, v244, v87
	ds_bpermute_b32 v236, v244, v94
	ds_bpermute_b32 v237, v244, v95
	v_exp_f32_e32 v75, v75
	v_mul_f32_e32 v80, v80, v82
	v_rcp_f32_e32 v86, v78
	v_or_b32_e32 v84, 48, v152
	v_mul_f32_e32 v81, v81, v82
	v_ashrrev_i32_e32 v85, 31, v84
	v_add_f32_e32 v78, 1.0, v79
	v_max_f32_e32 v80, 0xc2a00000, v80
	v_max_f32_e32 v81, 0xc2a00000, v81
	v_fma_f32 v74, v171, v74, v132
	v_rcp_f32_e32 v87, v78
	v_lshlrev_b64 v[78:79], 12, v[84:85]
	v_fma_f32 v84, v180, v86, v136
	v_mul_f32_e32 v80, 0xbfb8aa3b, v80
	v_mul_f32_e32 v81, 0xbfb8aa3b, v81
	v_log_f32_e32 v86, v74
	v_add_f32_e32 v74, 1.0, v75
	v_mul_f32_e32 v75, v76, v82
	v_exp_f32_e32 v80, v80
	v_exp_f32_e32 v81, v81
	v_max_f32_e32 v75, 0xc2a00000, v75
	v_mul_f32_e32 v76, v77, v82
	v_mul_f32_e32 v75, 0xbfb8aa3b, v75
	v_max_f32_e32 v76, 0xc2a00000, v76
	v_exp_f32_e32 v75, v75
	v_mul_f32_e32 v76, 0xbfb8aa3b, v76
	v_exp_f32_e32 v76, v76
	v_add_f32_e32 v80, 1.0, v80
	v_add_f32_e32 v81, 1.0, v81
	v_rcp_f32_e32 v80, v80
	v_rcp_f32_e32 v81, v81
	v_mul_f32_e32 v66, v66, v82
	v_rcp_f32_e32 v74, v74
	v_add_f32_e32 v75, 1.0, v75
	v_max_f32_e32 v66, 0xc2a00000, v66
	v_rcp_f32_e32 v75, v75
	v_add_f32_e32 v76, 1.0, v76
	v_mul_f32_e32 v66, 0xbfb8aa3b, v66
	v_rcp_f32_e32 v76, v76
	v_exp_f32_e32 v66, v66
	v_fma_f32 v80, v178, v80, v138
	v_fma_f32 v81, v177, v81, v139
	v_log_f32_e32 v80, v80
	v_log_f32_e32 v81, v81
	v_fma_f32 v74, v170, v74, v133
	v_log_f32_e32 v77, v74
	v_fma_f32 v74, v169, v75, v134
	v_mul_f32_e32 v70, v70, v82
	v_mul_f32_e32 v67, v67, v82
	v_fma_f32 v85, v179, v87, v137
	v_log_f32_e32 v87, v74
	v_fma_f32 v74, v155, v76, v135
	v_max_f32_e32 v70, 0xc2a00000, v70
	v_add_f32_e32 v66, 1.0, v66
	v_max_f32_e32 v67, 0xc2a00000, v67
	v_log_f32_e32 v84, v84
	v_log_f32_e32 v85, v85
	v_log_f32_e32 v88, v74
	v_mul_f32_e32 v70, 0xbfb8aa3b, v70
	v_rcp_f32_e32 v66, v66
	v_mul_f32_e32 v67, 0xbfb8aa3b, v67
	v_cvt_pk_f16_f32 v75, v80, v81
	v_exp_f32_e32 v80, v70
	v_mul_f32_e32 v70, v71, v82
	v_exp_f32_e32 v67, v67
	v_max_f32_e32 v70, 0xc2a00000, v70
	v_lshl_add_u64 v[78:79], s[42:43], 0, v[78:79]
	v_mul_f32_e32 v70, 0xbfb8aa3b, v70
	v_cvt_pk_f16_f32 v74, v84, v85
	v_cvt_pk_f16_f32 v76, v86, v77
	v_cvt_pk_f16_f32 v77, v87, v88
	v_exp_f32_e32 v81, v70
	v_lshl_add_u64 v[70:71], v[78:79], 0, v[114:115]
	v_fma_f32 v66, v123, v66, v124
	s_waitcnt lgkmcnt(0)
	global_store_dwordx4 v[236:237], v[232:235], off offset:64
	ds_bpermute_b32 v238, v244, v74
	ds_bpermute_b32 v239, v244, v75
	ds_bpermute_b32 v240, v244, v76
	ds_bpermute_b32 v241, v244, v77
	ds_bpermute_b32 v242, v244, v70
	ds_bpermute_b32 v243, v244, v71
	v_mul_f32_e32 v72, v72, v82
	v_mul_f32_e32 v73, v73, v82
	v_log_f32_e32 v76, v66
	v_add_f32_e32 v66, 1.0, v67
	v_mul_f32_e32 v67, v68, v82
	v_max_f32_e32 v67, 0xc2a00000, v67
	v_mul_f32_e32 v68, v69, v82
	v_max_f32_e32 v72, 0xc2a00000, v72
	v_max_f32_e32 v73, 0xc2a00000, v73
	v_mul_f32_e32 v67, 0xbfb8aa3b, v67
	v_max_f32_e32 v68, 0xc2a00000, v68
	v_mul_f32_e32 v72, 0xbfb8aa3b, v72
	v_mul_f32_e32 v73, 0xbfb8aa3b, v73
	v_exp_f32_e32 v67, v67
	v_mul_f32_e32 v68, 0xbfb8aa3b, v68
	v_exp_f32_e32 v72, v72
	v_exp_f32_e32 v73, v73
	v_exp_f32_e32 v68, v68
	v_mul_f32_e32 v58, v58, v83
	v_rcp_f32_e32 v66, v66
	v_add_f32_e32 v67, 1.0, v67
	v_max_f32_e32 v58, 0xc2a00000, v58
	v_add_f32_e32 v78, 1.0, v80
	v_add_f32_e32 v79, 1.0, v81
	v_add_f32_e32 v72, 1.0, v72
	v_add_f32_e32 v73, 1.0, v73
	v_rcp_f32_e32 v67, v67
	v_add_f32_e32 v68, 1.0, v68
	v_mul_f32_e32 v58, 0xbfb8aa3b, v58
	v_rcp_f32_e32 v78, v78
	v_rcp_f32_e32 v79, v79
	v_rcp_f32_e32 v72, v72
	v_rcp_f32_e32 v73, v73
	v_rcp_f32_e32 v68, v68
	v_exp_f32_e32 v58, v58
	v_fma_f32 v66, v120, v66, v125
	v_log_f32_e32 v69, v66
	v_fma_f32 v66, v118, v67, v126
	v_mul_f32_e32 v59, v59, v83
	v_fma_f32 v74, v153, v78, v128
	v_fma_f32 v75, v168, v79, v129
	v_fma_f32 v72, v121, v72, v130
	v_fma_f32 v73, v122, v73, v131
	v_log_f32_e32 v77, v66
	v_fma_f32 v66, v119, v68, v127
	v_add_f32_e32 v58, 1.0, v58
	v_max_f32_e32 v59, 0xc2a00000, v59
	v_log_f32_e32 v74, v74
	v_log_f32_e32 v75, v75
	v_log_f32_e32 v72, v72
	v_log_f32_e32 v73, v73
	v_log_f32_e32 v78, v66
	v_rcp_f32_e32 v58, v58
	v_mul_f32_e32 v59, 0xbfb8aa3b, v59
	v_exp_f32_e32 v59, v59
	v_mul_f32_e32 v64, v64, v83
	v_mul_f32_e32 v65, v65, v83
	v_max_f32_e32 v64, 0xc2a00000, v64
	v_max_f32_e32 v65, 0xc2a00000, v65
	v_cvt_pk_f16_f32 v66, v74, v75
	v_cvt_pk_f16_f32 v67, v72, v73
	v_cvt_pk_f16_f32 v68, v76, v69
	v_mul_f32_e32 v62, v62, v83
	v_mul_f32_e32 v63, v63, v83
	v_cvt_pk_f16_f32 v69, v77, v78
	v_mul_f32_e32 v64, 0xbfb8aa3b, v64
	v_mul_f32_e32 v65, 0xbfb8aa3b, v65
	v_fma_f32 v58, v171, v58, v132
	v_max_f32_e32 v62, 0xc2a00000, v62
	v_max_f32_e32 v63, 0xc2a00000, v63
	s_waitcnt lgkmcnt(0)
	global_store_dwordx4 v[242:243], v[238:241], off
	ds_bpermute_b32 v232, v244, v66
	ds_bpermute_b32 v233, v244, v67
	ds_bpermute_b32 v234, v244, v68
	ds_bpermute_b32 v235, v244, v69
	ds_bpermute_b32 v236, v244, v70
	ds_bpermute_b32 v237, v244, v71
	v_exp_f32_e32 v64, v64
	v_exp_f32_e32 v65, v65
	v_log_f32_e32 v66, v58
	v_add_f32_e32 v58, 1.0, v59
	v_mul_f32_e32 v59, v60, v83
	v_mul_f32_e32 v62, 0xbfb8aa3b, v62
	v_mul_f32_e32 v63, 0xbfb8aa3b, v63
	v_max_f32_e32 v59, 0xc2a00000, v59
	v_mul_f32_e32 v60, v61, v83
	v_exp_f32_e32 v62, v62
	v_exp_f32_e32 v63, v63
	v_mul_f32_e32 v59, 0xbfb8aa3b, v59
	v_max_f32_e32 v60, 0xc2a00000, v60
	v_exp_f32_e32 v59, v59
	v_mul_f32_e32 v60, 0xbfb8aa3b, v60
	v_add_f32_e32 v64, 1.0, v64
	v_add_f32_e32 v65, 1.0, v65
	v_exp_f32_e32 v60, v60
	v_rcp_f32_e32 v64, v64
	v_rcp_f32_e32 v65, v65
	v_add_f32_e32 v62, 1.0, v62
	v_add_f32_e32 v63, 1.0, v63
	v_mul_f32_e32 v50, v50, v83
	v_rcp_f32_e32 v62, v62
	v_rcp_f32_e32 v63, v63
	v_rcp_f32_e32 v58, v58
	v_add_f32_e32 v59, 1.0, v59
	v_max_f32_e32 v50, 0xc2a00000, v50
	v_rcp_f32_e32 v59, v59
	v_add_f32_e32 v60, 1.0, v60
	v_mul_f32_e32 v50, 0xbfb8aa3b, v50
	v_fma_f32 v64, v178, v64, v138
	v_fma_f32 v65, v177, v65, v139
	v_rcp_f32_e32 v60, v60
	v_exp_f32_e32 v50, v50
	v_log_f32_e32 v64, v64
	v_log_f32_e32 v65, v65
	v_fma_f32 v62, v180, v62, v136
	v_fma_f32 v63, v179, v63, v137
	v_fma_f32 v58, v170, v58, v133
	v_mul_f32_e32 v54, v54, v83
	v_log_f32_e32 v62, v62
	v_log_f32_e32 v63, v63
	v_log_f32_e32 v61, v58
	v_fma_f32 v58, v169, v59, v134
	v_max_f32_e32 v54, 0xc2a00000, v54
	v_mul_f32_e32 v51, v51, v83
	v_log_f32_e32 v67, v58
	v_fma_f32 v58, v155, v60, v135
	v_mul_f32_e32 v54, 0xbfb8aa3b, v54
	v_add_f32_e32 v50, 1.0, v50
	v_max_f32_e32 v51, 0xc2a00000, v51
	v_log_f32_e32 v68, v58
	v_cvt_pk_f16_f32 v59, v64, v65
	v_exp_f32_e32 v64, v54
	v_mul_f32_e32 v54, v55, v83
	v_rcp_f32_e32 v50, v50
	v_mul_f32_e32 v51, 0xbfb8aa3b, v51
	v_max_f32_e32 v54, 0xc2a00000, v54
	v_exp_f32_e32 v51, v51
	v_cvt_pk_f16_f32 v58, v62, v63
	v_lshl_add_u64 v[62:63], v[166:167], 0, s[14:15]
	v_mul_f32_e32 v54, 0xbfb8aa3b, v54
	s_mov_b32 s14, 0x80000
	v_exp_f32_e32 v65, v54
	v_add_co_u32_e32 v54, vcc, s14, v166
	v_cvt_pk_f16_f32 v60, v66, v61
	v_cvt_pk_f16_f32 v61, v67, v68
	v_addc_co_u32_e32 v55, vcc, 0, v167, vcc
	v_fma_f32 v50, v123, v50, v124
	s_waitcnt lgkmcnt(0)
	global_store_dwordx4 v[236:237], v[232:235], off offset:64
	ds_bpermute_b32 v238, v244, v58
	ds_bpermute_b32 v239, v244, v59
	ds_bpermute_b32 v240, v244, v60
	ds_bpermute_b32 v241, v244, v61
	ds_bpermute_b32 v242, v244, v54
	ds_bpermute_b32 v243, v244, v55
	v_mul_f32_e32 v56, v56, v83
	v_mul_f32_e32 v57, v57, v83
	v_log_f32_e32 v58, v50
	v_add_f32_e32 v50, 1.0, v51
	v_mul_f32_e32 v51, v52, v83
	v_max_f32_e32 v51, 0xc2a00000, v51
	v_mul_f32_e32 v51, 0xbfb8aa3b, v51
	v_exp_f32_e32 v51, v51
	v_rcp_f32_e32 v50, v50
	v_mul_f32_e32 v52, v53, v83
	v_max_f32_e32 v56, 0xc2a00000, v56
	v_add_f32_e32 v51, 1.0, v51
	v_rcp_f32_e32 v51, v51
	v_fma_f32 v50, v120, v50, v125
	v_log_f32_e32 v59, v50
	v_max_f32_e32 v57, 0xc2a00000, v57
	v_fma_f32 v50, v118, v51, v126
	v_log_f32_e32 v60, v50
	ds_read2_b32 v[50:51], v176 offset0:144 offset1:160
	v_max_f32_e32 v52, 0xc2a00000, v52
	v_mul_f32_e32 v56, 0xbfb8aa3b, v56
	v_mul_f32_e32 v57, 0xbfb8aa3b, v57
	v_mul_f32_e32 v52, 0xbfb8aa3b, v52
	v_exp_f32_e32 v56, v56
	v_exp_f32_e32 v57, v57
	v_exp_f32_e32 v52, v52
	s_waitcnt lgkmcnt(0)
	v_mul_f32_e32 v42, v42, v50
	v_max_f32_e32 v42, 0xc2a00000, v42
	v_add_f32_e32 v64, 1.0, v64
	v_add_f32_e32 v65, 1.0, v65
	v_add_f32_e32 v56, 1.0, v56
	v_add_f32_e32 v57, 1.0, v57
	v_add_f32_e32 v52, 1.0, v52
	v_mul_f32_e32 v42, 0xbfb8aa3b, v42
	v_rcp_f32_e32 v64, v64
	v_rcp_f32_e32 v65, v65
	v_rcp_f32_e32 v56, v56
	v_rcp_f32_e32 v57, v57
	v_rcp_f32_e32 v52, v52
	v_exp_f32_e32 v42, v42
	v_mul_f32_e32 v43, v43, v50
	v_fma_f32 v54, v153, v64, v128
	v_fma_f32 v55, v168, v65, v129
	v_fma_f32 v56, v121, v56, v130
	v_fma_f32 v57, v122, v57, v131
	v_fma_f32 v52, v119, v52, v127
	v_add_f32_e32 v42, 1.0, v42
	v_max_f32_e32 v43, 0xc2a00000, v43
	v_log_f32_e32 v54, v54
	v_log_f32_e32 v55, v55
	v_log_f32_e32 v56, v56
	v_log_f32_e32 v57, v57
	v_log_f32_e32 v61, v52
	v_rcp_f32_e32 v42, v42
	v_mul_f32_e32 v43, 0xbfb8aa3b, v43
	v_exp_f32_e32 v43, v43
	v_mul_f32_e32 v48, v48, v50
	v_mul_f32_e32 v49, v49, v50
	v_max_f32_e32 v48, 0xc2a00000, v48
	v_max_f32_e32 v49, 0xc2a00000, v49
	v_cvt_pk_f16_f32 v52, v54, v55
	v_cvt_pk_f16_f32 v53, v56, v57
	v_cvt_pk_f16_f32 v54, v58, v59
	v_mul_f32_e32 v46, v46, v50
	v_mul_f32_e32 v47, v47, v50
	v_cvt_pk_f16_f32 v55, v60, v61
	v_mul_f32_e32 v48, 0xbfb8aa3b, v48
	v_mul_f32_e32 v49, 0xbfb8aa3b, v49
	v_fma_f32 v42, v171, v42, v132
	v_max_f32_e32 v46, 0xc2a00000, v46
	v_max_f32_e32 v47, 0xc2a00000, v47
	s_waitcnt lgkmcnt(0)
	global_store_dwordx4 v[242:243], v[238:241], off
	ds_bpermute_b32 v232, v244, v52
	ds_bpermute_b32 v233, v244, v53
	ds_bpermute_b32 v234, v244, v54
	ds_bpermute_b32 v235, v244, v55
	ds_bpermute_b32 v236, v244, v62
	ds_bpermute_b32 v237, v244, v63
	v_exp_f32_e32 v48, v48
	v_exp_f32_e32 v49, v49
	v_log_f32_e32 v52, v42
	v_add_f32_e32 v42, 1.0, v43
	v_mul_f32_e32 v43, v44, v50
	v_mul_f32_e32 v46, 0xbfb8aa3b, v46
	v_mul_f32_e32 v47, 0xbfb8aa3b, v47
	v_max_f32_e32 v43, 0xc2a00000, v43
	v_mul_f32_e32 v44, v45, v50
	v_exp_f32_e32 v46, v46
	v_exp_f32_e32 v47, v47
	v_mul_f32_e32 v43, 0xbfb8aa3b, v43
	v_max_f32_e32 v44, 0xc2a00000, v44
	v_exp_f32_e32 v43, v43
	v_mul_f32_e32 v44, 0xbfb8aa3b, v44
	v_add_f32_e32 v48, 1.0, v48
	v_add_f32_e32 v49, 1.0, v49
	v_exp_f32_e32 v44, v44
	v_rcp_f32_e32 v48, v48
	v_rcp_f32_e32 v49, v49
	v_add_f32_e32 v46, 1.0, v46
	v_add_f32_e32 v47, 1.0, v47
	v_mul_f32_e32 v34, v34, v50
	v_rcp_f32_e32 v46, v46
	v_rcp_f32_e32 v47, v47
	v_rcp_f32_e32 v42, v42
	v_add_f32_e32 v43, 1.0, v43
	v_max_f32_e32 v34, 0xc2a00000, v34
	v_rcp_f32_e32 v43, v43
	v_add_f32_e32 v44, 1.0, v44
	v_mul_f32_e32 v34, 0xbfb8aa3b, v34
	v_fma_f32 v48, v178, v48, v138
	v_fma_f32 v49, v177, v49, v139
	v_rcp_f32_e32 v44, v44
	v_exp_f32_e32 v34, v34
	v_log_f32_e32 v48, v48
	v_log_f32_e32 v49, v49
	v_fma_f32 v46, v180, v46, v136
	v_fma_f32 v47, v179, v47, v137
	v_fma_f32 v42, v170, v42, v133
	v_mul_f32_e32 v38, v38, v50
	v_log_f32_e32 v46, v46
	v_log_f32_e32 v47, v47
	v_log_f32_e32 v45, v42
	v_fma_f32 v42, v169, v43, v134
	v_max_f32_e32 v38, 0xc2a00000, v38
	v_mul_f32_e32 v35, v35, v50
	v_log_f32_e32 v53, v42
	v_fma_f32 v42, v155, v44, v135
	v_mul_f32_e32 v38, 0xbfb8aa3b, v38
	v_add_f32_e32 v34, 1.0, v34
	v_max_f32_e32 v35, 0xc2a00000, v35
	v_log_f32_e32 v54, v42
	v_cvt_pk_f16_f32 v43, v48, v49
	v_exp_f32_e32 v48, v38
	v_mul_f32_e32 v38, v39, v50
	v_rcp_f32_e32 v34, v34
	v_mul_f32_e32 v35, 0xbfb8aa3b, v35
	s_mov_b64 s[14:15], 0x90000
	v_max_f32_e32 v38, 0xc2a00000, v38
	v_exp_f32_e32 v35, v35
	v_cvt_pk_f16_f32 v42, v46, v47
	v_lshl_add_u64 v[46:47], v[166:167], 0, s[14:15]
	v_mul_f32_e32 v38, 0xbfb8aa3b, v38
	s_mov_b32 s14, 0x90000
	v_exp_f32_e32 v49, v38
	v_add_co_u32_e32 v38, vcc, s14, v166
	v_cvt_pk_f16_f32 v44, v52, v45
	v_cvt_pk_f16_f32 v45, v53, v54
	v_addc_co_u32_e32 v39, vcc, 0, v167, vcc
	v_fma_f32 v34, v123, v34, v124
	s_waitcnt lgkmcnt(0)
	global_store_dwordx4 v[236:237], v[232:235], off offset:64
	ds_bpermute_b32 v238, v244, v42
	ds_bpermute_b32 v239, v244, v43
	ds_bpermute_b32 v240, v244, v44
	ds_bpermute_b32 v241, v244, v45
	ds_bpermute_b32 v242, v244, v38
	ds_bpermute_b32 v243, v244, v39
	v_mul_f32_e32 v40, v40, v50
	v_mul_f32_e32 v41, v41, v50
	v_log_f32_e32 v42, v34
	v_add_f32_e32 v34, 1.0, v35
	v_mul_f32_e32 v35, v36, v50
	v_max_f32_e32 v35, 0xc2a00000, v35
	v_mul_f32_e32 v36, v37, v50
	v_max_f32_e32 v40, 0xc2a00000, v40
	v_max_f32_e32 v41, 0xc2a00000, v41
	v_mul_f32_e32 v35, 0xbfb8aa3b, v35
	v_max_f32_e32 v36, 0xc2a00000, v36
	v_mul_f32_e32 v40, 0xbfb8aa3b, v40
	v_mul_f32_e32 v41, 0xbfb8aa3b, v41
	v_exp_f32_e32 v35, v35
	v_mul_f32_e32 v36, 0xbfb8aa3b, v36
	v_exp_f32_e32 v40, v40
	v_exp_f32_e32 v41, v41
	v_exp_f32_e32 v36, v36
	v_mul_f32_e32 v26, v26, v51
	v_rcp_f32_e32 v34, v34
	v_add_f32_e32 v35, 1.0, v35
	v_max_f32_e32 v26, 0xc2a00000, v26
	v_add_f32_e32 v48, 1.0, v48
	v_add_f32_e32 v49, 1.0, v49
	v_add_f32_e32 v40, 1.0, v40
	v_add_f32_e32 v41, 1.0, v41
	v_rcp_f32_e32 v35, v35
	v_add_f32_e32 v36, 1.0, v36
	v_mul_f32_e32 v26, 0xbfb8aa3b, v26
	v_rcp_f32_e32 v48, v48
	v_rcp_f32_e32 v49, v49
	v_rcp_f32_e32 v40, v40
	v_rcp_f32_e32 v41, v41
	v_rcp_f32_e32 v36, v36
	v_exp_f32_e32 v26, v26
	v_fma_f32 v34, v120, v34, v125
	v_log_f32_e32 v37, v34
	v_fma_f32 v34, v118, v35, v126
	v_mul_f32_e32 v27, v27, v51
	v_fma_f32 v38, v153, v48, v128
	v_fma_f32 v39, v168, v49, v129
	v_fma_f32 v40, v121, v40, v130
	v_fma_f32 v41, v122, v41, v131
	v_log_f32_e32 v43, v34
	v_fma_f32 v34, v119, v36, v127
	v_add_f32_e32 v26, 1.0, v26
	v_max_f32_e32 v27, 0xc2a00000, v27
	v_log_f32_e32 v38, v38
	v_log_f32_e32 v39, v39
	v_log_f32_e32 v40, v40
	v_log_f32_e32 v41, v41
	v_log_f32_e32 v44, v34
	v_rcp_f32_e32 v26, v26
	v_mul_f32_e32 v27, 0xbfb8aa3b, v27
	v_exp_f32_e32 v27, v27
	v_mul_f32_e32 v32, v32, v51
	v_mul_f32_e32 v33, v33, v51
	v_max_f32_e32 v32, 0xc2a00000, v32
	v_max_f32_e32 v33, 0xc2a00000, v33
	v_cvt_pk_f16_f32 v34, v38, v39
	v_cvt_pk_f16_f32 v35, v40, v41
	v_cvt_pk_f16_f32 v36, v42, v37
	v_mul_f32_e32 v30, v30, v51
	v_mul_f32_e32 v31, v31, v51
	v_cvt_pk_f16_f32 v37, v43, v44
	v_mul_f32_e32 v32, 0xbfb8aa3b, v32
	v_mul_f32_e32 v33, 0xbfb8aa3b, v33
	v_fma_f32 v26, v171, v26, v132
	v_max_f32_e32 v30, 0xc2a00000, v30
	v_max_f32_e32 v31, 0xc2a00000, v31
	s_waitcnt lgkmcnt(0)
	global_store_dwordx4 v[242:243], v[238:241], off
	ds_bpermute_b32 v232, v244, v34
	ds_bpermute_b32 v233, v244, v35
	ds_bpermute_b32 v234, v244, v36
	ds_bpermute_b32 v235, v244, v37
	ds_bpermute_b32 v236, v244, v46
	ds_bpermute_b32 v237, v244, v47
	v_exp_f32_e32 v32, v32
	v_exp_f32_e32 v33, v33
	v_log_f32_e32 v34, v26
	v_add_f32_e32 v26, 1.0, v27
	v_mul_f32_e32 v27, v28, v51
	v_mul_f32_e32 v30, 0xbfb8aa3b, v30
	v_mul_f32_e32 v31, 0xbfb8aa3b, v31
	v_max_f32_e32 v27, 0xc2a00000, v27
	v_mul_f32_e32 v28, v29, v51
	v_exp_f32_e32 v30, v30
	v_exp_f32_e32 v31, v31
	v_mul_f32_e32 v27, 0xbfb8aa3b, v27
	v_max_f32_e32 v28, 0xc2a00000, v28
	v_exp_f32_e32 v27, v27
	v_mul_f32_e32 v28, 0xbfb8aa3b, v28
	v_add_f32_e32 v32, 1.0, v32
	v_add_f32_e32 v33, 1.0, v33
	v_exp_f32_e32 v28, v28
	v_rcp_f32_e32 v32, v32
	v_rcp_f32_e32 v33, v33
	v_add_f32_e32 v30, 1.0, v30
	v_add_f32_e32 v31, 1.0, v31
	v_mul_f32_e32 v18, v18, v51
	v_rcp_f32_e32 v30, v30
	v_rcp_f32_e32 v31, v31
	v_rcp_f32_e32 v26, v26
	v_add_f32_e32 v27, 1.0, v27
	v_max_f32_e32 v18, 0xc2a00000, v18
	v_rcp_f32_e32 v27, v27
	v_add_f32_e32 v28, 1.0, v28
	v_mul_f32_e32 v18, 0xbfb8aa3b, v18
	v_fma_f32 v32, v178, v32, v138
	v_fma_f32 v33, v177, v33, v139
	v_rcp_f32_e32 v28, v28
	v_exp_f32_e32 v18, v18
	v_log_f32_e32 v32, v32
	v_log_f32_e32 v33, v33
	v_fma_f32 v30, v180, v30, v136
	v_fma_f32 v31, v179, v31, v137
	v_fma_f32 v26, v170, v26, v133
	v_mul_f32_e32 v22, v22, v51
	v_log_f32_e32 v30, v30
	v_log_f32_e32 v31, v31
	v_log_f32_e32 v29, v26
	v_fma_f32 v26, v169, v27, v134
	v_max_f32_e32 v22, 0xc2a00000, v22
	v_mul_f32_e32 v19, v19, v51
	v_log_f32_e32 v35, v26
	v_fma_f32 v26, v155, v28, v135
	v_mul_f32_e32 v22, 0xbfb8aa3b, v22
	v_add_f32_e32 v18, 1.0, v18
	v_max_f32_e32 v19, 0xc2a00000, v19
	v_log_f32_e32 v36, v26
	v_cvt_pk_f16_f32 v27, v32, v33
	v_exp_f32_e32 v32, v22
	v_mul_f32_e32 v22, v23, v51
	v_rcp_f32_e32 v18, v18
	v_mul_f32_e32 v19, 0xbfb8aa3b, v19
	s_mov_b64 s[14:15], 0xa0000
	v_max_f32_e32 v22, 0xc2a00000, v22
	v_exp_f32_e32 v19, v19
	v_cvt_pk_f16_f32 v26, v30, v31
	v_lshl_add_u64 v[30:31], v[166:167], 0, s[14:15]
	v_mul_f32_e32 v22, 0xbfb8aa3b, v22
	s_mov_b32 s14, 0xa0000
	v_exp_f32_e32 v33, v22
	v_add_co_u32_e32 v22, vcc, s14, v166
	v_cvt_pk_f16_f32 v28, v34, v29
	v_cvt_pk_f16_f32 v29, v35, v36
	v_addc_co_u32_e32 v23, vcc, 0, v167, vcc
	v_fma_f32 v18, v123, v18, v124
	s_waitcnt lgkmcnt(0)
	global_store_dwordx4 v[236:237], v[232:235], off offset:64
	ds_bpermute_b32 v238, v244, v26
	ds_bpermute_b32 v239, v244, v27
	ds_bpermute_b32 v240, v244, v28
	ds_bpermute_b32 v241, v244, v29
	ds_bpermute_b32 v242, v244, v22
	ds_bpermute_b32 v243, v244, v23
	v_mul_f32_e32 v24, v24, v51
	v_mul_f32_e32 v25, v25, v51
	v_log_f32_e32 v26, v18
	v_add_f32_e32 v18, 1.0, v19
	v_mul_f32_e32 v19, v20, v51
	v_max_f32_e32 v19, 0xc2a00000, v19
	v_mul_f32_e32 v20, v21, v51
	ds_read_b32 v28, v176 offset:704
	v_max_f32_e32 v24, 0xc2a00000, v24
	v_max_f32_e32 v25, 0xc2a00000, v25
	v_mul_f32_e32 v19, 0xbfb8aa3b, v19
	v_max_f32_e32 v20, 0xc2a00000, v20
	v_mul_f32_e32 v24, 0xbfb8aa3b, v24
	v_mul_f32_e32 v25, 0xbfb8aa3b, v25
	v_exp_f32_e32 v19, v19
	v_mul_f32_e32 v20, 0xbfb8aa3b, v20
	v_exp_f32_e32 v24, v24
	v_exp_f32_e32 v25, v25
	v_exp_f32_e32 v20, v20
	s_waitcnt lgkmcnt(0)
	v_mul_f32_e32 v10, v10, v28
	v_rcp_f32_e32 v18, v18
	v_add_f32_e32 v19, 1.0, v19
	v_max_f32_e32 v10, 0xc2a00000, v10
	v_add_f32_e32 v32, 1.0, v32
	v_add_f32_e32 v33, 1.0, v33
	v_add_f32_e32 v24, 1.0, v24
	v_add_f32_e32 v25, 1.0, v25
	v_rcp_f32_e32 v19, v19
	v_add_f32_e32 v20, 1.0, v20
	v_mul_f32_e32 v10, 0xbfb8aa3b, v10
	v_rcp_f32_e32 v32, v32
	v_rcp_f32_e32 v33, v33
	v_rcp_f32_e32 v24, v24
	v_rcp_f32_e32 v25, v25
	v_rcp_f32_e32 v20, v20
	v_exp_f32_e32 v10, v10
	v_fma_f32 v18, v120, v18, v125
	v_log_f32_e32 v21, v18
	v_fma_f32 v18, v118, v19, v126
	v_mul_f32_e32 v11, v11, v28
	v_fma_f32 v22, v153, v32, v128
	v_fma_f32 v23, v168, v33, v129
	v_fma_f32 v24, v121, v24, v130
	v_fma_f32 v25, v122, v25, v131
	v_log_f32_e32 v27, v18
	v_fma_f32 v18, v119, v20, v127
	v_add_f32_e32 v10, 1.0, v10
	v_max_f32_e32 v11, 0xc2a00000, v11
	v_log_f32_e32 v22, v22
	v_log_f32_e32 v23, v23
	v_log_f32_e32 v24, v24
	v_log_f32_e32 v25, v25
	v_log_f32_e32 v29, v18
	v_rcp_f32_e32 v10, v10
	v_mul_f32_e32 v11, 0xbfb8aa3b, v11
	v_mul_f32_e32 v14, v14, v28
	v_mul_f32_e32 v15, v15, v28
	v_exp_f32_e32 v11, v11
	v_max_f32_e32 v14, 0xc2a00000, v14
	v_max_f32_e32 v15, 0xc2a00000, v15
	v_mul_f32_e32 v14, 0xbfb8aa3b, v14
	v_mul_f32_e32 v15, 0xbfb8aa3b, v15
	v_cvt_pk_f16_f32 v18, v22, v23
	v_cvt_pk_f16_f32 v19, v24, v25
	v_cvt_pk_f16_f32 v20, v26, v21
	v_exp_f32_e32 v14, v14
	v_exp_f32_e32 v15, v15
	v_cvt_pk_f16_f32 v21, v27, v29
	v_fma_f32 v10, v171, v10, v132
	s_waitcnt lgkmcnt(0)
	global_store_dwordx4 v[242:243], v[238:241], off
	ds_bpermute_b32 v232, v244, v18
	ds_bpermute_b32 v233, v244, v19
	ds_bpermute_b32 v234, v244, v20
	ds_bpermute_b32 v235, v244, v21
	ds_bpermute_b32 v236, v244, v30
	ds_bpermute_b32 v237, v244, v31
	v_add_f32_e32 v14, 1.0, v14
	v_add_f32_e32 v15, 1.0, v15
	v_log_f32_e32 v18, v10
	v_add_f32_e32 v10, 1.0, v11
	v_mul_f32_e32 v11, v12, v28
	v_max_f32_e32 v11, 0xc2a00000, v11
	v_mul_f32_e32 v11, 0xbfb8aa3b, v11
	v_exp_f32_e32 v11, v11
	v_rcp_f32_e32 v14, v14
	v_rcp_f32_e32 v15, v15
	v_mul_f32_e32 v16, v16, v28
	v_mul_f32_e32 v17, v17, v28
	v_rcp_f32_e32 v10, v10
	v_mul_f32_e32 v12, v13, v28
	v_add_f32_e32 v11, 1.0, v11
	v_fma_f32 v14, v180, v14, v136
	v_fma_f32 v15, v179, v15, v137
	v_max_f32_e32 v16, 0xc2a00000, v16
	v_max_f32_e32 v17, 0xc2a00000, v17
	v_max_f32_e32 v12, 0xc2a00000, v12
	v_rcp_f32_e32 v11, v11
	v_log_f32_e32 v14, v14
	v_mul_f32_e32 v16, 0xbfb8aa3b, v16
	v_mul_f32_e32 v17, 0xbfb8aa3b, v17
	v_log_f32_e32 v15, v15
	v_mul_f32_e32 v12, 0xbfb8aa3b, v12
	v_exp_f32_e32 v16, v16
	v_exp_f32_e32 v17, v17
	v_exp_f32_e32 v12, v12
	v_mul_f32_e32 v6, v6, v28
	v_fma_f32 v10, v170, v10, v133
	v_max_f32_e32 v6, 0xc2a00000, v6
	v_log_f32_e32 v13, v10
	v_fma_f32 v10, v169, v11, v134
	v_mul_f32_e32 v6, 0xbfb8aa3b, v6
	v_log_f32_e32 v19, v10
	v_cvt_pk_f16_f32 v10, v14, v15
	v_exp_f32_e32 v14, v6
	v_mul_f32_e32 v6, v7, v28
	v_mul_f32_e32 v8, v8, v28
	v_mul_f32_e32 v9, v9, v28
	v_mul_f32_e32 v2, v2, v28
	v_mul_f32_e32 v3, v3, v28
	v_mul_f32_e32 v4, v4, v28
	v_mul_f32_e32 v5, v5, v28
	v_add_f32_e32 v16, 1.0, v16
	v_add_f32_e32 v17, 1.0, v17
	v_add_f32_e32 v12, 1.0, v12
	v_max_f32_e32 v6, 0xc2a00000, v6
	v_max_f32_e32 v8, 0xc2a00000, v8
	v_max_f32_e32 v9, 0xc2a00000, v9
	v_max_f32_e32 v2, 0xc2a00000, v2
	v_max_f32_e32 v3, 0xc2a00000, v3
	v_max_f32_e32 v4, 0xc2a00000, v4
	v_max_f32_e32 v5, 0xc2a00000, v5
	v_rcp_f32_e32 v16, v16
	v_rcp_f32_e32 v17, v17
	v_rcp_f32_e32 v12, v12
	v_mul_f32_e32 v6, 0xbfb8aa3b, v6
	v_mul_f32_e32 v8, 0xbfb8aa3b, v8
	v_mul_f32_e32 v9, 0xbfb8aa3b, v9
	v_mul_f32_e32 v2, 0xbfb8aa3b, v2
	v_mul_f32_e32 v3, 0xbfb8aa3b, v3
	v_mul_f32_e32 v4, 0xbfb8aa3b, v4
	v_mul_f32_e32 v5, 0xbfb8aa3b, v5
	v_exp_f32_e32 v15, v6
	v_exp_f32_e32 v8, v8
	v_exp_f32_e32 v9, v9
	v_exp_f32_e32 v2, v2
	v_exp_f32_e32 v3, v3
	v_exp_f32_e32 v4, v4
	v_exp_f32_e32 v5, v5
	v_fma_f32 v16, v178, v16, v138
	v_fmac_f32_e32 v139, v177, v17
	v_fmac_f32_e32 v135, v155, v12
	v_log_f32_e32 v16, v16
	v_log_f32_e32 v17, v139
	v_log_f32_e32 v20, v135
	v_add_f32_e32 v14, 1.0, v14
	v_add_f32_e32 v15, 1.0, v15
	v_add_f32_e32 v8, 1.0, v8
	v_add_f32_e32 v9, 1.0, v9
	v_add_f32_e32 v2, 1.0, v2
	v_add_f32_e32 v3, 1.0, v3
	v_add_f32_e32 v4, 1.0, v4
	v_add_f32_e32 v5, 1.0, v5
	s_mov_b64 s[14:15], 0xb0000
	v_rcp_f32_e32 v14, v14
	v_rcp_f32_e32 v15, v15
	v_rcp_f32_e32 v8, v8
	v_rcp_f32_e32 v9, v9
	v_rcp_f32_e32 v2, v2
	v_rcp_f32_e32 v3, v3
	v_rcp_f32_e32 v4, v4
	v_rcp_f32_e32 v5, v5
	v_lshl_add_u64 v[136:137], v[166:167], 0, s[14:15]
	s_mov_b32 s14, 0xb0000
	v_add_co_u32_e32 v6, vcc, s14, v166
	v_cvt_pk_f16_f32 v11, v16, v17
	v_cvt_pk_f16_f32 v12, v18, v13
	v_cvt_pk_f16_f32 v13, v19, v20
	v_addc_co_u32_e32 v7, vcc, 0, v167, vcc
	s_waitcnt lgkmcnt(0)
	global_store_dwordx4 v[236:237], v[232:235], off offset:64
	ds_bpermute_b32 v238, v244, v10
	ds_bpermute_b32 v239, v244, v11
	ds_bpermute_b32 v240, v244, v12
	ds_bpermute_b32 v241, v244, v13
	ds_bpermute_b32 v242, v244, v6
	ds_bpermute_b32 v243, v244, v7
	v_fma_f32 v6, v153, v14, v128
	v_fma_f32 v7, v168, v15, v129
	v_fma_f32 v8, v121, v8, v130
	v_fmac_f32_e32 v131, v122, v9
	v_fma_f32 v2, v123, v2, v124
	v_fma_f32 v3, v120, v3, v125
	v_fma_f32 v4, v118, v4, v126
	v_fmac_f32_e32 v127, v119, v5
	v_log_f32_e32 v6, v6
	v_log_f32_e32 v7, v7
	v_log_f32_e32 v8, v8
	v_log_f32_e32 v9, v131
	v_log_f32_e32 v2, v2
	v_log_f32_e32 v3, v3
	v_log_f32_e32 v4, v4
	v_log_f32_e32 v5, v127
	v_cvt_pk_f16_f32 v196, v181, v182
	v_cvt_pk_f16_f32 v132, v6, v7
	v_cvt_pk_f16_f32 v133, v8, v9
	v_cvt_pk_f16_f32 v134, v2, v3
	v_cvt_pk_f16_f32 v135, v4, v5
	s_waitcnt lgkmcnt(0)
	global_store_dwordx4 v[242:243], v[238:241], off
	ds_bpermute_b32 v232, v244, v194
	ds_bpermute_b32 v233, v244, v195
	ds_bpermute_b32 v234, v244, v196
	ds_bpermute_b32 v235, v244, v197
	ds_bpermute_b32 v236, v244, v166
	ds_bpermute_b32 v237, v244, v167
	s_andn2_b64 vcc, exec, s[38:39]
	s_mov_b64 s[28:29], -1
	s_waitcnt lgkmcnt(0)
	global_store_dwordx4 v[236:237], v[232:235], off offset:64
	ds_bpermute_b32 v238, v244, v132
	ds_bpermute_b32 v239, v244, v133
	ds_bpermute_b32 v240, v244, v134
	ds_bpermute_b32 v241, v244, v135
	ds_bpermute_b32 v242, v244, v136
	ds_bpermute_b32 v243, v244, v137
	s_waitcnt lgkmcnt(0)
	global_store_dwordx4 v[242:243], v[238:241], off offset:64
	s_cbranch_vccnz .LBB0_338

.LBB0_509:
	s_ashr_i32 s57, s56, 31
	s_lshl_b64 s[14:15], s[56:57], 25
	s_add_u32 s14, s24, s14
	s_addc_u32 s15, s37, s15
	v_lshlrev_b32_e32 v114, 1, v177
	v_ashrrev_i32_e32 v153, 31, v152
	v_lshl_add_u64 v[132:133], s[14:15], 0, v[114:115]
	v_lshlrev_b64 v[136:137], 12, v[152:153]
	v_mov_b32_e32 v155, v154
	v_lshl_add_u64 v[136:137], v[132:133], 0, v[136:137]
	v_cvt_pk_bf16_f32 v166, v166, v167
	v_cvt_pk_bf16_f32 v167, v134, v135
	v_cvt_pk_bf16_f32 v168, v168, v169
	v_cvt_pk_bf16_f32 v169, v138, v139
	v_mov_b32_e32 v158, v154
	v_mov_b32_e32 v159, v154
	v_cndmask_b32_e64 v114, 0, 1, s[54:55]
	ds_bpermute_b32 v232, v244, v166
	ds_bpermute_b32 v233, v244, v167
	ds_bpermute_b32 v234, v244, v168
	ds_bpermute_b32 v235, v244, v169
	ds_bpermute_b32 v236, v244, v136
	ds_bpermute_b32 v237, v244, v137
	v_pk_mul_f32 v[138:139], v[122:123], v[158:159]
	v_pk_mul_f32 v[134:135], v[120:121], v[154:155]
	v_pk_mul_f32 v[166:167], v[118:119], v[158:159]
	v_cmp_ne_u32_e64 s[40:41], 1, v114
	s_andn2_b64 vcc, exec, s[54:55]
	v_pk_mul_f32 v[168:169], v[116:117], v[154:155]
	s_waitcnt lgkmcnt(0)
	global_store_dwordx4 v[236:237], v[232:235], off
	s_cbranch_vccnz .LBB0_511
	v_max_f32_e32 v114, v134, v134
	v_max_f32_e32 v134, 0xc2a00000, v114
	v_max_f32_e32 v114, v168, v168
	v_max_f32_e32 v158, 0xc2a00000, v114
	v_mul_f32_e32 v114, 0xbfb8aa3b, v134
	v_exp_f32_e32 v114, v114
	v_mul_f32_e32 v155, 0xbfb8aa3b, v158
	v_exp_f32_e32 v155, v155
	v_max_f32_e32 v135, v135, v135
	v_add_f32_e32 v114, 1.0, v114
	v_rcp_f32_e32 v160, v114
	v_add_f32_e32 v114, 1.0, v155
	v_max_f32_e32 v135, 0xc2a00000, v135
	v_max_f32_e32 v155, v169, v169
	v_max_f32_e32 v159, 0xc2a00000, v155
	v_mul_f32_e32 v155, 0xbfb8aa3b, v135
	v_exp_f32_e32 v155, v155
	v_mul_f32_e32 v161, 0xbfb8aa3b, v159
	v_exp_f32_e32 v169, v161
	v_max_f32_e32 v138, v138, v138
	v_rcp_f32_e32 v168, v114
	v_add_f32_e32 v114, 1.0, v155
	v_max_f32_e32 v138, 0xc2a00000, v138
	v_max_f32_e32 v155, v166, v166
	v_max_f32_e32 v166, 0xc2a00000, v155
	v_mul_f32_e32 v155, 0xbfb8aa3b, v138
	v_exp_f32_e32 v155, v155
	v_rcp_f32_e32 v161, v114
	v_add_f32_e32 v114, 1.0, v169
	v_mul_f32_e32 v169, 0xbfb8aa3b, v166
	v_exp_f32_e32 v171, v169
	v_max_f32_e32 v139, v139, v139
	v_rcp_f32_e32 v169, v114
	v_add_f32_e32 v114, 1.0, v155
	v_max_f32_e32 v139, 0xc2a00000, v139
	v_max_f32_e32 v155, v167, v167
	v_max_f32_e32 v167, 0xc2a00000, v155
	v_mul_f32_e32 v155, 0xbfb8aa3b, v139
	v_rcp_f32_e32 v170, v114
	v_add_f32_e32 v114, 1.0, v171
	v_exp_f32_e32 v155, v155
	v_mul_f32_e32 v171, 0xbfb8aa3b, v167
	v_exp_f32_e32 v179, v171
	v_rcp_f32_e32 v178, v114
	v_add_f32_e32 v114, 1.0, v155
	v_rcp_f32_e32 v171, v114
	v_add_f32_e32 v114, 1.0, v179
	v_rcp_f32_e32 v179, v114
	v_pk_mul_f32 v[134:135], v[134:135], v[160:161]
	v_pk_mul_f32 v[138:139], v[138:139], v[170:171]
	v_pk_mul_f32 v[168:169], v[158:159], v[168:169]
	v_pk_mul_f32 v[166:167], v[166:167], v[178:179]

.LBB0_541:
	s_and_b64 vcc, exec, s[40:41]
	s_cbranch_vccz .LBB0_540
	v_lshlrev_b32_e32 v155, 2, v177
	global_load_dwordx4 v[136:139], v155, s[42:43]
	global_load_dwordx4 v[132:135], v155, s[42:43] offset:16
	s_waitcnt lgkmcnt(0)
	v_mul_f32_e32 v160, v128, v154
	v_mul_f32_e32 v161, v129, v154
	v_mul_f32_e32 v166, v130, v154
	v_mul_f32_e32 v167, v131, v154
	v_mul_f32_e32 v168, v124, v154
	v_mul_f32_e32 v169, v125, v154
	v_mul_f32_e32 v170, v126, v154
	v_mul_f32_e32 v171, v127, v154
	global_load_dwordx4 v[124:127], v155, s[42:43] offset:144
	global_load_dwordx4 v[128:131], v155, s[42:43] offset:128
	v_ashrrev_i32_e32 v153, 31, v152
	v_lshlrev_b64 v[158:159], 12, v[152:153]
	v_max_f32_e32 v153, 0xc2a00000, v160
	v_max_f32_e32 v155, 0xc2a00000, v161
	v_max_f32_e32 v160, 0xc2a00000, v166
	v_max_f32_e32 v161, 0xc2a00000, v167
	v_max_f32_e32 v166, 0xc2a00000, v168
	v_max_f32_e32 v167, 0xc2a00000, v169
	v_max_f32_e32 v168, 0xc2a00000, v170
	v_max_f32_e32 v169, 0xc2a00000, v171
	v_mul_f32_e32 v153, 0xbfb8aa3b, v153
	v_mul_f32_e32 v155, 0xbfb8aa3b, v155
	v_mul_f32_e32 v168, 0xbfb8aa3b, v168
	v_mul_f32_e32 v169, 0xbfb8aa3b, v169
	v_exp_f32_e32 v153, v153
	v_exp_f32_e32 v155, v155
	v_mul_f32_e32 v160, 0xbfb8aa3b, v160
	v_mul_f32_e32 v161, 0xbfb8aa3b, v161
	v_exp_f32_e32 v168, v168
	v_exp_f32_e32 v169, v169
	v_exp_f32_e32 v160, v160
	v_exp_f32_e32 v161, v161
	v_mul_f32_e32 v120, v120, v154
	v_max_f32_e32 v120, 0xc2a00000, v120
	v_add_f32_e32 v153, 1.0, v153
	v_add_f32_e32 v155, 1.0, v155
	v_mul_f32_e32 v121, v121, v154
	v_lshlrev_b32_e32 v114, 1, v177
	v_mul_f32_e32 v166, 0xbfb8aa3b, v166
	v_mul_f32_e32 v167, 0xbfb8aa3b, v167
	v_lshl_add_u64 v[158:159], s[26:27], 0, v[158:159]
	v_add_f32_e32 v168, 1.0, v168
	v_add_f32_e32 v169, 1.0, v169
	v_rcp_f32_e32 v153, v153
	v_rcp_f32_e32 v181, v155
	v_mul_f32_e32 v120, 0xbfb8aa3b, v120
	v_max_f32_e32 v121, 0xc2a00000, v121
	v_exp_f32_e32 v170, v166
	v_exp_f32_e32 v171, v167
	v_lshl_add_u64 v[166:167], v[158:159], 0, v[114:115]
	v_add_f32_e32 v158, 1.0, v160
	v_add_f32_e32 v159, 1.0, v161
	v_rcp_f32_e32 v168, v168
	v_rcp_f32_e32 v182, v169
	v_exp_f32_e32 v120, v120
	v_mul_f32_e32 v121, 0xbfb8aa3b, v121
	v_rcp_f32_e32 v158, v158
	v_rcp_f32_e32 v159, v159
	v_exp_f32_e32 v121, v121
	v_add_f32_e32 v120, 1.0, v120
	v_rcp_f32_e32 v120, v120
	v_mul_f32_e32 v116, v116, v154
	v_add_f32_e32 v121, 1.0, v121
	v_rcp_f32_e32 v121, v121
	v_add_f32_e32 v160, 1.0, v170
	v_add_f32_e32 v161, 1.0, v171
	v_max_f32_e32 v116, 0xc2a00000, v116
	v_mul_f32_e32 v117, v117, v154
	v_rcp_f32_e32 v160, v160
	v_rcp_f32_e32 v161, v161
	v_mul_f32_e32 v116, 0xbfb8aa3b, v116
	v_max_f32_e32 v117, 0xc2a00000, v117
	v_exp_f32_e32 v116, v116
	v_mul_f32_e32 v117, 0xbfb8aa3b, v117
	v_exp_f32_e32 v117, v117
	s_mov_b64 s[14:15], 0x80000
	v_add_f32_e32 v116, 1.0, v116
	v_rcp_f32_e32 v116, v116
	v_add_f32_e32 v117, 1.0, v117
	s_waitcnt vmcnt(0)
	v_sub_f32_e32 v180, 1.0, v136
	v_sub_f32_e32 v179, 1.0, v137
	v_sub_f32_e32 v169, 1.0, v134
	v_sub_f32_e32 v155, 1.0, v135
	v_fma_f32 v153, v180, v153, v136
	v_fma_f32 v181, v179, v181, v137
	v_sub_f32_e32 v178, 1.0, v138
	v_sub_f32_e32 v177, 1.0, v139
	v_fma_f32 v168, v169, v168, v134
	v_fma_f32 v182, v155, v182, v135
	v_log_f32_e32 v153, v153
	v_log_f32_e32 v181, v181
	v_fma_f32 v158, v178, v158, v138
	v_fma_f32 v159, v177, v159, v139
	v_log_f32_e32 v168, v168
	v_log_f32_e32 v182, v182
	v_log_f32_e32 v158, v158
	v_log_f32_e32 v159, v159
	v_cvt_pk_f16_f32 v194, v153, v181
	v_sub_f32_e32 v153, 1.0, v128
	v_cvt_pk_f16_f32 v197, v168, v182
	v_fma_f32 v120, v153, v120, v128
	v_sub_f32_e32 v168, 1.0, v129
	v_cvt_pk_f16_f32 v195, v158, v159
	v_log_f32_e32 v158, v120
	v_fma_f32 v120, v168, v121, v129
	v_log_f32_e32 v159, v120
	v_mul_f32_e32 v120, v122, v154
	v_max_f32_e32 v120, 0xc2a00000, v120
	v_mul_f32_e32 v121, v123, v154
	v_mul_f32_e32 v120, 0xbfb8aa3b, v120
	v_max_f32_e32 v121, 0xc2a00000, v121
	v_exp_f32_e32 v120, v120
	v_mul_f32_e32 v121, 0xbfb8aa3b, v121
	v_exp_f32_e32 v122, v121
	v_sub_f32_e32 v171, 1.0, v132
	v_sub_f32_e32 v170, 1.0, v133
	v_add_f32_e32 v120, 1.0, v120
	v_fma_f32 v160, v171, v160, v132
	v_fma_f32 v161, v170, v161, v133
	v_rcp_f32_e32 v120, v120
	v_add_f32_e32 v122, 1.0, v122
	v_log_f32_e32 v160, v160
	v_log_f32_e32 v161, v161
	v_rcp_f32_e32 v123, v122
	v_sub_f32_e32 v121, 1.0, v130
	v_rcp_f32_e32 v117, v117
	v_fma_f32 v120, v121, v120, v130
	v_sub_f32_e32 v122, 1.0, v131
	v_cvt_pk_f16_f32 v196, v160, v161
	v_log_f32_e32 v160, v120
	v_fma_f32 v120, v122, v123, v131
	v_sub_f32_e32 v123, 1.0, v124
	v_log_f32_e32 v161, v120
	v_fma_f32 v116, v123, v116, v124
	v_sub_f32_e32 v120, 1.0, v125
	v_log_f32_e32 v181, v116
	v_fma_f32 v116, v120, v117, v125
	v_log_f32_e32 v182, v116
	v_mul_f32_e32 v116, v118, v154
	v_max_f32_e32 v116, 0xc2a00000, v116
	v_mul_f32_e32 v117, v119, v154
	v_mul_f32_e32 v116, 0xbfb8aa3b, v116
	v_max_f32_e32 v117, 0xc2a00000, v117
	v_exp_f32_e32 v116, v116
	v_mul_f32_e32 v117, 0xbfb8aa3b, v117
	v_exp_f32_e32 v117, v117
	v_sub_f32_e32 v118, 1.0, v126
	v_add_f32_e32 v116, 1.0, v116
	v_rcp_f32_e32 v116, v116
	v_add_f32_e32 v117, 1.0, v117
	v_rcp_f32_e32 v117, v117
	v_sub_f32_e32 v119, 1.0, v127
	v_fma_f32 v116, v118, v116, v126
	v_log_f32_e32 v154, v116
	v_fma_f32 v116, v119, v117, v127
	v_log_f32_e32 v183, v116
	ds_read2_b32 v[116:117], v176 offset0:16 offset1:32
	ds_bpermute_b32 v232, v244, v194
	ds_bpermute_b32 v233, v244, v195
	ds_bpermute_b32 v234, v244, v196
	ds_bpermute_b32 v235, v244, v197
	ds_bpermute_b32 v236, v244, v166
	ds_bpermute_b32 v237, v244, v167
	s_waitcnt lgkmcnt(0)
	v_mul_f32_e32 v106, v106, v116
	v_max_f32_e32 v106, 0xc2a00000, v106
	v_mul_f32_e32 v106, 0xbfb8aa3b, v106
	v_exp_f32_e32 v106, v106
	v_mul_f32_e32 v110, v110, v116
	v_max_f32_e32 v110, 0xc2a00000, v110
	v_mul_f32_e32 v111, v111, v116
	v_mul_f32_e32 v110, 0xbfb8aa3b, v110
	v_max_f32_e32 v111, 0xc2a00000, v111
	v_mul_f32_e32 v107, v107, v116
	v_exp_f32_e32 v110, v110
	v_mul_f32_e32 v111, 0xbfb8aa3b, v111
	v_add_f32_e32 v106, 1.0, v106
	v_max_f32_e32 v107, 0xc2a00000, v107
	v_exp_f32_e32 v111, v111
	v_rcp_f32_e32 v106, v106
	v_mul_f32_e32 v107, 0xbfb8aa3b, v107
	v_exp_f32_e32 v107, v107
	v_cvt_pk_f16_f32 v194, v158, v159
	v_or_b32_e32 v158, 16, v152
	v_add_f32_e32 v110, 1.0, v110
	v_mul_f32_e32 v112, v112, v116
	v_mul_f32_e32 v113, v113, v116
	v_cvt_pk_f16_f32 v197, v154, v183
	v_ashrrev_i32_e32 v159, 31, v158
	v_rcp_f32_e32 v154, v110
	v_add_f32_e32 v110, 1.0, v111
	v_max_f32_e32 v112, 0xc2a00000, v112
	v_max_f32_e32 v113, 0xc2a00000, v113
	v_fma_f32 v106, v171, v106, v132
	v_cvt_pk_f16_f32 v195, v160, v161
	v_rcp_f32_e32 v160, v110
	v_lshlrev_b64 v[110:111], 12, v[158:159]
	v_mul_f32_e32 v112, 0xbfb8aa3b, v112
	v_mul_f32_e32 v113, 0xbfb8aa3b, v113
	v_log_f32_e32 v159, v106
	v_add_f32_e32 v106, 1.0, v107
	v_mul_f32_e32 v107, v108, v116
	v_exp_f32_e32 v112, v112
	v_exp_f32_e32 v113, v113
	v_max_f32_e32 v107, 0xc2a00000, v107
	v_mul_f32_e32 v108, v109, v116
	v_mul_f32_e32 v107, 0xbfb8aa3b, v107
	v_max_f32_e32 v108, 0xc2a00000, v108
	v_exp_f32_e32 v107, v107
	v_mul_f32_e32 v108, 0xbfb8aa3b, v108
	v_exp_f32_e32 v108, v108
	v_add_f32_e32 v112, 1.0, v112
	v_add_f32_e32 v113, 1.0, v113
	v_rcp_f32_e32 v112, v112
	v_rcp_f32_e32 v113, v113
	v_mul_f32_e32 v98, v98, v116
	v_rcp_f32_e32 v106, v106
	v_add_f32_e32 v107, 1.0, v107
	v_max_f32_e32 v98, 0xc2a00000, v98
	v_rcp_f32_e32 v107, v107
	v_add_f32_e32 v108, 1.0, v108
	v_mul_f32_e32 v98, 0xbfb8aa3b, v98
	v_rcp_f32_e32 v108, v108
	v_exp_f32_e32 v98, v98
	v_fma_f32 v112, v178, v112, v138
	v_fma_f32 v113, v177, v113, v139
	v_log_f32_e32 v112, v112
	v_log_f32_e32 v113, v113
	v_fma_f32 v106, v170, v106, v133
	v_log_f32_e32 v109, v106
	v_fma_f32 v106, v169, v107, v134
	v_mul_f32_e32 v102, v102, v116
	v_mul_f32_e32 v99, v99, v116
	v_fma_f32 v154, v180, v154, v136
	v_fma_f32 v158, v179, v160, v137
	v_log_f32_e32 v160, v106
	v_fma_f32 v106, v155, v108, v135
	v_max_f32_e32 v102, 0xc2a00000, v102
	v_add_f32_e32 v98, 1.0, v98
	v_max_f32_e32 v99, 0xc2a00000, v99
	v_log_f32_e32 v154, v154
	v_log_f32_e32 v158, v158
	v_log_f32_e32 v161, v106
	v_mul_f32_e32 v102, 0xbfb8aa3b, v102
	v_rcp_f32_e32 v98, v98
	v_mul_f32_e32 v99, 0xbfb8aa3b, v99
	v_cvt_pk_f16_f32 v107, v112, v113
	v_exp_f32_e32 v112, v102
	v_mul_f32_e32 v102, v103, v116
	v_exp_f32_e32 v99, v99
	v_max_f32_e32 v102, 0xc2a00000, v102
	v_lshl_add_u64 v[110:111], s[26:27], 0, v[110:111]
	v_mul_f32_e32 v102, 0xbfb8aa3b, v102
	v_cvt_pk_f16_f32 v106, v154, v158
	v_cvt_pk_f16_f32 v108, v159, v109
	v_cvt_pk_f16_f32 v109, v160, v161
	v_exp_f32_e32 v113, v102
	v_lshl_add_u64 v[102:103], v[110:111], 0, v[114:115]
	v_fma_f32 v98, v123, v98, v124
	s_waitcnt lgkmcnt(0)
	global_store_dwordx4 v[236:237], v[232:235], off
	ds_bpermute_b32 v238, v244, v106
	ds_bpermute_b32 v239, v244, v107
	ds_bpermute_b32 v240, v244, v108
	ds_bpermute_b32 v241, v244, v109
	ds_bpermute_b32 v242, v244, v102
	ds_bpermute_b32 v243, v244, v103
	v_mul_f32_e32 v104, v104, v116
	v_mul_f32_e32 v105, v105, v116
	v_log_f32_e32 v108, v98
	v_add_f32_e32 v98, 1.0, v99
	v_mul_f32_e32 v99, v100, v116
	v_max_f32_e32 v99, 0xc2a00000, v99
	v_mul_f32_e32 v100, v101, v116
	v_max_f32_e32 v104, 0xc2a00000, v104
	v_max_f32_e32 v105, 0xc2a00000, v105
	v_mul_f32_e32 v99, 0xbfb8aa3b, v99
	v_max_f32_e32 v100, 0xc2a00000, v100
	v_mul_f32_e32 v104, 0xbfb8aa3b, v104
	v_mul_f32_e32 v105, 0xbfb8aa3b, v105
	v_exp_f32_e32 v99, v99
	v_mul_f32_e32 v100, 0xbfb8aa3b, v100
	v_exp_f32_e32 v104, v104
	v_exp_f32_e32 v105, v105
	v_exp_f32_e32 v100, v100
	v_rcp_f32_e32 v98, v98
	v_add_f32_e32 v99, 1.0, v99
	v_add_f32_e32 v110, 1.0, v112
	v_add_f32_e32 v111, 1.0, v113
	v_add_f32_e32 v104, 1.0, v104
	v_add_f32_e32 v105, 1.0, v105
	v_rcp_f32_e32 v99, v99
	v_add_f32_e32 v100, 1.0, v100
	v_rcp_f32_e32 v110, v110
	v_rcp_f32_e32 v111, v111
	v_rcp_f32_e32 v104, v104
	v_rcp_f32_e32 v105, v105
	v_rcp_f32_e32 v100, v100
	v_mul_f32_e32 v90, v90, v117
	v_fma_f32 v98, v120, v98, v125
	v_mul_f32_e32 v94, v94, v117
	v_max_f32_e32 v90, 0xc2a00000, v90
	v_log_f32_e32 v101, v98
	v_fma_f32 v98, v118, v99, v126
	v_max_f32_e32 v94, 0xc2a00000, v94
	v_mul_f32_e32 v90, 0xbfb8aa3b, v90
	v_fma_f32 v106, v153, v110, v128
	v_fma_f32 v107, v168, v111, v129
	v_fma_f32 v104, v121, v104, v130
	v_fma_f32 v105, v122, v105, v131
	v_log_f32_e32 v109, v98
	v_fma_f32 v98, v119, v100, v127
	v_mul_f32_e32 v94, 0xbfb8aa3b, v94
	v_exp_f32_e32 v90, v90
	v_log_f32_e32 v106, v106
	v_log_f32_e32 v107, v107
	v_log_f32_e32 v104, v104
	v_log_f32_e32 v105, v105
	v_log_f32_e32 v110, v98
	v_exp_f32_e32 v94, v94
	v_mul_f32_e32 v95, v95, v117
	v_max_f32_e32 v95, 0xc2a00000, v95
	v_mul_f32_e32 v91, v91, v117
	v_mul_f32_e32 v95, 0xbfb8aa3b, v95
	v_add_f32_e32 v90, 1.0, v90
	v_max_f32_e32 v91, 0xc2a00000, v91
	v_cvt_pk_f16_f32 v98, v106, v107
	v_cvt_pk_f16_f32 v99, v104, v105
	v_cvt_pk_f16_f32 v100, v108, v101
	v_cvt_pk_f16_f32 v101, v109, v110
	v_exp_f32_e32 v95, v95
	v_add_f32_e32 v94, 1.0, v94
	v_rcp_f32_e32 v90, v90
	v_mul_f32_e32 v91, 0xbfb8aa3b, v91
	s_waitcnt lgkmcnt(0)
	global_store_dwordx4 v[242:243], v[238:241], off
	ds_bpermute_b32 v232, v244, v98
	ds_bpermute_b32 v233, v244, v99
	ds_bpermute_b32 v234, v244, v100
	ds_bpermute_b32 v235, v244, v101
	ds_bpermute_b32 v236, v244, v102
	ds_bpermute_b32 v237, v244, v103
	v_exp_f32_e32 v91, v91
	v_fma_f32 v90, v171, v90, v132
	v_rcp_f32_e32 v100, v94
	v_or_b32_e32 v98, 32, v152
	v_ashrrev_i32_e32 v99, 31, v98
	v_add_f32_e32 v94, 1.0, v95
	v_rcp_f32_e32 v101, v94
	v_lshlrev_b64 v[94:95], 12, v[98:99]
	v_fma_f32 v98, v180, v100, v136
	v_log_f32_e32 v100, v90
	v_add_f32_e32 v90, 1.0, v91
	v_mul_f32_e32 v91, v92, v117
	v_mul_f32_e32 v96, v96, v117
	v_mul_f32_e32 v97, v97, v117
	v_max_f32_e32 v91, 0xc2a00000, v91
	v_mul_f32_e32 v92, v93, v117
	v_max_f32_e32 v96, 0xc2a00000, v96
	v_max_f32_e32 v97, 0xc2a00000, v97
	v_mul_f32_e32 v91, 0xbfb8aa3b, v91
	v_max_f32_e32 v92, 0xc2a00000, v92
	v_mul_f32_e32 v96, 0xbfb8aa3b, v96
	v_mul_f32_e32 v97, 0xbfb8aa3b, v97
	v_exp_f32_e32 v91, v91
	v_mul_f32_e32 v92, 0xbfb8aa3b, v92
	v_exp_f32_e32 v96, v96
	v_exp_f32_e32 v97, v97
	v_exp_f32_e32 v92, v92
	v_mul_f32_e32 v82, v82, v117
	v_rcp_f32_e32 v90, v90
	v_add_f32_e32 v91, 1.0, v91
	v_max_f32_e32 v82, 0xc2a00000, v82
	v_add_f32_e32 v96, 1.0, v96
	v_add_f32_e32 v97, 1.0, v97
	v_rcp_f32_e32 v91, v91
	v_add_f32_e32 v92, 1.0, v92
	v_mul_f32_e32 v82, 0xbfb8aa3b, v82
	v_rcp_f32_e32 v96, v96
	v_rcp_f32_e32 v97, v97
	v_rcp_f32_e32 v92, v92
	v_exp_f32_e32 v82, v82
	v_fma_f32 v90, v170, v90, v133
	v_log_f32_e32 v93, v90
	v_fma_f32 v90, v169, v91, v134
	v_mul_f32_e32 v83, v83, v117
	v_fma_f32 v99, v179, v101, v137
	v_fma_f32 v96, v178, v96, v138
	v_fma_f32 v97, v177, v97, v139
	v_log_f32_e32 v101, v90
	v_fma_f32 v90, v155, v92, v135
	v_add_f32_e32 v82, 1.0, v82
	v_max_f32_e32 v83, 0xc2a00000, v83
	v_log_f32_e32 v98, v98
	v_log_f32_e32 v99, v99
	v_log_f32_e32 v96, v96
	v_log_f32_e32 v97, v97
	v_log_f32_e32 v102, v90
	v_rcp_f32_e32 v82, v82
	v_mul_f32_e32 v83, 0xbfb8aa3b, v83
	v_exp_f32_e32 v83, v83
	v_lshl_add_u64 v[94:95], s[26:27], 0, v[94:95]
	v_cvt_pk_f16_f32 v90, v98, v99
	v_cvt_pk_f16_f32 v91, v96, v97
	v_cvt_pk_f16_f32 v92, v100, v93
	v_cvt_pk_f16_f32 v93, v101, v102
	v_lshl_add_u64 v[94:95], v[94:95], 0, v[114:115]
	v_fma_f32 v82, v123, v82, v124
	s_waitcnt lgkmcnt(0)
	global_store_dwordx4 v[236:237], v[232:235], off offset:64
	ds_bpermute_b32 v238, v244, v90
	ds_bpermute_b32 v239, v244, v91
	ds_bpermute_b32 v240, v244, v92
	ds_bpermute_b32 v241, v244, v93
	ds_bpermute_b32 v242, v244, v94
	ds_bpermute_b32 v243, v244, v95
	v_mul_f32_e32 v86, v86, v117
	v_mul_f32_e32 v87, v87, v117
	v_log_f32_e32 v90, v82
	v_add_f32_e32 v82, 1.0, v83
	v_mul_f32_e32 v83, v84, v117
	v_max_f32_e32 v83, 0xc2a00000, v83
	v_mul_f32_e32 v84, v85, v117
	v_mul_f32_e32 v83, 0xbfb8aa3b, v83
	v_max_f32_e32 v84, 0xc2a00000, v84
	v_exp_f32_e32 v83, v83
	v_mul_f32_e32 v84, 0xbfb8aa3b, v84
	v_exp_f32_e32 v84, v84
	v_rcp_f32_e32 v82, v82
	v_add_f32_e32 v83, 1.0, v83
	v_rcp_f32_e32 v83, v83
	v_add_f32_e32 v84, 1.0, v84
	v_rcp_f32_e32 v84, v84
	v_mul_f32_e32 v88, v88, v117
	v_mul_f32_e32 v89, v89, v117
	v_max_f32_e32 v86, 0xc2a00000, v86
	v_max_f32_e32 v87, 0xc2a00000, v87
	v_max_f32_e32 v88, 0xc2a00000, v88
	v_max_f32_e32 v89, 0xc2a00000, v89
	v_fma_f32 v82, v120, v82, v125
	v_mul_f32_e32 v86, 0xbfb8aa3b, v86
	v_mul_f32_e32 v87, 0xbfb8aa3b, v87
	v_mul_f32_e32 v88, 0xbfb8aa3b, v88
	v_mul_f32_e32 v89, 0xbfb8aa3b, v89
	v_log_f32_e32 v91, v82
	v_fma_f32 v82, v118, v83, v126
	v_exp_f32_e32 v86, v86
	v_exp_f32_e32 v87, v87
	v_exp_f32_e32 v88, v88
	v_exp_f32_e32 v89, v89
	v_log_f32_e32 v92, v82
	v_fma_f32 v82, v119, v84, v127
	v_log_f32_e32 v93, v82
	ds_read2_b32 v[82:83], v176 offset0:48 offset1:128
	v_add_f32_e32 v86, 1.0, v86
	v_add_f32_e32 v87, 1.0, v87
	v_add_f32_e32 v88, 1.0, v88
	v_add_f32_e32 v89, 1.0, v89
	v_rcp_f32_e32 v86, v86
	v_rcp_f32_e32 v87, v87
	v_rcp_f32_e32 v88, v88
	v_rcp_f32_e32 v89, v89
	s_waitcnt lgkmcnt(0)
	v_mul_f32_e32 v74, v74, v82
	v_mul_f32_e32 v78, v78, v82
	v_max_f32_e32 v74, 0xc2a00000, v74
	v_max_f32_e32 v78, 0xc2a00000, v78
	v_mul_f32_e32 v74, 0xbfb8aa3b, v74
	v_fma_f32 v86, v153, v86, v128
	v_fma_f32 v87, v168, v87, v129
	v_fma_f32 v88, v121, v88, v130
	v_fma_f32 v89, v122, v89, v131
	v_mul_f32_e32 v78, 0xbfb8aa3b, v78
	v_exp_f32_e32 v74, v74
	v_log_f32_e32 v86, v86
	v_log_f32_e32 v87, v87
	v_log_f32_e32 v88, v88
	v_log_f32_e32 v89, v89
	v_exp_f32_e32 v78, v78
	v_mul_f32_e32 v79, v79, v82
	v_max_f32_e32 v79, 0xc2a00000, v79
	v_mul_f32_e32 v75, v75, v82
	v_mul_f32_e32 v79, 0xbfb8aa3b, v79
	v_add_f32_e32 v74, 1.0, v74
	v_max_f32_e32 v75, 0xc2a00000, v75
	v_cvt_pk_f16_f32 v84, v86, v87
	v_cvt_pk_f16_f32 v85, v88, v89
	v_cvt_pk_f16_f32 v86, v90, v91
	v_cvt_pk_f16_f32 v87, v92, v93
	v_exp_f32_e32 v79, v79
	v_add_f32_e32 v78, 1.0, v78
	v_rcp_f32_e32 v74, v74
	v_mul_f32_e32 v75, 0xbfb8aa3b, v75
	s_waitcnt lgkmcnt(0)
	global_store_dwordx4 v[242:243], v[238:241], off
	ds_bpermute_b32 v232, v244, v84
	ds_bpermute_b32 v233, v244, v85
	ds_bpermute_b32 v234, v244, v86
	ds_bpermute_b32 v235, v244, v87
	ds_bpermute_b32 v236, v244, v94
	ds_bpermute_b32 v237, v244, v95
	v_exp_f32_e32 v75, v75
	v_mul_f32_e32 v80, v80, v82
	v_rcp_f32_e32 v86, v78
	v_or_b32_e32 v84, 48, v152
	v_mul_f32_e32 v81, v81, v82
	v_ashrrev_i32_e32 v85, 31, v84
	v_add_f32_e32 v78, 1.0, v79
	v_max_f32_e32 v80, 0xc2a00000, v80
	v_max_f32_e32 v81, 0xc2a00000, v81
	v_fma_f32 v74, v171, v74, v132
	v_rcp_f32_e32 v87, v78
	v_lshlrev_b64 v[78:79], 12, v[84:85]
	v_fma_f32 v84, v180, v86, v136
	v_mul_f32_e32 v80, 0xbfb8aa3b, v80
	v_mul_f32_e32 v81, 0xbfb8aa3b, v81
	v_log_f32_e32 v86, v74
	v_add_f32_e32 v74, 1.0, v75
	v_mul_f32_e32 v75, v76, v82
	v_exp_f32_e32 v80, v80
	v_exp_f32_e32 v81, v81
	v_max_f32_e32 v75, 0xc2a00000, v75
	v_mul_f32_e32 v76, v77, v82
	v_mul_f32_e32 v75, 0xbfb8aa3b, v75
	v_max_f32_e32 v76, 0xc2a00000, v76
	v_exp_f32_e32 v75, v75
	v_mul_f32_e32 v76, 0xbfb8aa3b, v76
	v_exp_f32_e32 v76, v76
	v_add_f32_e32 v80, 1.0, v80
	v_add_f32_e32 v81, 1.0, v81
	v_rcp_f32_e32 v80, v80
	v_rcp_f32_e32 v81, v81
	v_mul_f32_e32 v66, v66, v82
	v_rcp_f32_e32 v74, v74
	v_add_f32_e32 v75, 1.0, v75
	v_max_f32_e32 v66, 0xc2a00000, v66
	v_rcp_f32_e32 v75, v75
	v_add_f32_e32 v76, 1.0, v76
	v_mul_f32_e32 v66, 0xbfb8aa3b, v66
	v_rcp_f32_e32 v76, v76
	v_exp_f32_e32 v66, v66
	v_fma_f32 v80, v178, v80, v138
	v_fma_f32 v81, v177, v81, v139
	v_log_f32_e32 v80, v80
	v_log_f32_e32 v81, v81
	v_fma_f32 v74, v170, v74, v133
	v_log_f32_e32 v77, v74
	v_fma_f32 v74, v169, v75, v134
	v_mul_f32_e32 v70, v70, v82
	v_mul_f32_e32 v67, v67, v82
	v_fma_f32 v85, v179, v87, v137
	v_log_f32_e32 v87, v74
	v_fma_f32 v74, v155, v76, v135
	v_max_f32_e32 v70, 0xc2a00000, v70
	v_add_f32_e32 v66, 1.0, v66
	v_max_f32_e32 v67, 0xc2a00000, v67
	v_log_f32_e32 v84, v84
	v_log_f32_e32 v85, v85
	v_log_f32_e32 v88, v74
	v_mul_f32_e32 v70, 0xbfb8aa3b, v70
	v_rcp_f32_e32 v66, v66
	v_mul_f32_e32 v67, 0xbfb8aa3b, v67
	v_cvt_pk_f16_f32 v75, v80, v81
	v_exp_f32_e32 v80, v70
	v_mul_f32_e32 v70, v71, v82
	v_exp_f32_e32 v67, v67
	v_max_f32_e32 v70, 0xc2a00000, v70
	v_lshl_add_u64 v[78:79], s[26:27], 0, v[78:79]
	v_mul_f32_e32 v70, 0xbfb8aa3b, v70
	v_cvt_pk_f16_f32 v74, v84, v85
	v_cvt_pk_f16_f32 v76, v86, v77
	v_cvt_pk_f16_f32 v77, v87, v88
	v_exp_f32_e32 v81, v70
	v_lshl_add_u64 v[70:71], v[78:79], 0, v[114:115]
	v_fma_f32 v66, v123, v66, v124
	s_waitcnt lgkmcnt(0)
	global_store_dwordx4 v[236:237], v[232:235], off offset:64
	ds_bpermute_b32 v238, v244, v74
	ds_bpermute_b32 v239, v244, v75
	ds_bpermute_b32 v240, v244, v76
	ds_bpermute_b32 v241, v244, v77
	ds_bpermute_b32 v242, v244, v70
	ds_bpermute_b32 v243, v244, v71
	v_mul_f32_e32 v72, v72, v82
	v_mul_f32_e32 v73, v73, v82
	v_log_f32_e32 v76, v66
	v_add_f32_e32 v66, 1.0, v67
	v_mul_f32_e32 v67, v68, v82
	v_max_f32_e32 v67, 0xc2a00000, v67
	v_mul_f32_e32 v68, v69, v82
	v_max_f32_e32 v72, 0xc2a00000, v72
	v_max_f32_e32 v73, 0xc2a00000, v73
	v_mul_f32_e32 v67, 0xbfb8aa3b, v67
	v_max_f32_e32 v68, 0xc2a00000, v68
	v_mul_f32_e32 v72, 0xbfb8aa3b, v72
	v_mul_f32_e32 v73, 0xbfb8aa3b, v73
	v_exp_f32_e32 v67, v67
	v_mul_f32_e32 v68, 0xbfb8aa3b, v68
	v_exp_f32_e32 v72, v72
	v_exp_f32_e32 v73, v73
	v_exp_f32_e32 v68, v68
	v_mul_f32_e32 v58, v58, v83
	v_rcp_f32_e32 v66, v66
	v_add_f32_e32 v67, 1.0, v67
	v_max_f32_e32 v58, 0xc2a00000, v58
	v_add_f32_e32 v78, 1.0, v80
	v_add_f32_e32 v79, 1.0, v81
	v_add_f32_e32 v72, 1.0, v72
	v_add_f32_e32 v73, 1.0, v73
	v_rcp_f32_e32 v67, v67
	v_add_f32_e32 v68, 1.0, v68
	v_mul_f32_e32 v58, 0xbfb8aa3b, v58
	v_rcp_f32_e32 v78, v78
	v_rcp_f32_e32 v79, v79
	v_rcp_f32_e32 v72, v72
	v_rcp_f32_e32 v73, v73
	v_rcp_f32_e32 v68, v68
	v_exp_f32_e32 v58, v58
	v_fma_f32 v66, v120, v66, v125
	v_log_f32_e32 v69, v66
	v_fma_f32 v66, v118, v67, v126
	v_mul_f32_e32 v59, v59, v83
	v_fma_f32 v74, v153, v78, v128
	v_fma_f32 v75, v168, v79, v129
	v_fma_f32 v72, v121, v72, v130
	v_fma_f32 v73, v122, v73, v131
	v_log_f32_e32 v77, v66
	v_fma_f32 v66, v119, v68, v127
	v_add_f32_e32 v58, 1.0, v58
	v_max_f32_e32 v59, 0xc2a00000, v59
	v_log_f32_e32 v74, v74
	v_log_f32_e32 v75, v75
	v_log_f32_e32 v72, v72
	v_log_f32_e32 v73, v73
	v_log_f32_e32 v78, v66
	v_rcp_f32_e32 v58, v58
	v_mul_f32_e32 v59, 0xbfb8aa3b, v59
	v_exp_f32_e32 v59, v59
	v_mul_f32_e32 v64, v64, v83
	v_mul_f32_e32 v65, v65, v83
	v_max_f32_e32 v64, 0xc2a00000, v64
	v_max_f32_e32 v65, 0xc2a00000, v65
	v_cvt_pk_f16_f32 v66, v74, v75
	v_cvt_pk_f16_f32 v67, v72, v73
	v_cvt_pk_f16_f32 v68, v76, v69
	v_mul_f32_e32 v62, v62, v83
	v_mul_f32_e32 v63, v63, v83
	v_cvt_pk_f16_f32 v69, v77, v78
	v_mul_f32_e32 v64, 0xbfb8aa3b, v64
	v_mul_f32_e32 v65, 0xbfb8aa3b, v65
	v_fma_f32 v58, v171, v58, v132
	v_max_f32_e32 v62, 0xc2a00000, v62
	v_max_f32_e32 v63, 0xc2a00000, v63
	s_waitcnt lgkmcnt(0)
	global_store_dwordx4 v[242:243], v[238:241], off
	ds_bpermute_b32 v232, v244, v66
	ds_bpermute_b32 v233, v244, v67
	ds_bpermute_b32 v234, v244, v68
	ds_bpermute_b32 v235, v244, v69
	ds_bpermute_b32 v236, v244, v70
	ds_bpermute_b32 v237, v244, v71
	v_exp_f32_e32 v64, v64
	v_exp_f32_e32 v65, v65
	v_log_f32_e32 v66, v58
	v_add_f32_e32 v58, 1.0, v59
	v_mul_f32_e32 v59, v60, v83
	v_mul_f32_e32 v62, 0xbfb8aa3b, v62
	v_mul_f32_e32 v63, 0xbfb8aa3b, v63
	v_max_f32_e32 v59, 0xc2a00000, v59
	v_mul_f32_e32 v60, v61, v83
	v_exp_f32_e32 v62, v62
	v_exp_f32_e32 v63, v63
	v_mul_f32_e32 v59, 0xbfb8aa3b, v59
	v_max_f32_e32 v60, 0xc2a00000, v60
	v_exp_f32_e32 v59, v59
	v_mul_f32_e32 v60, 0xbfb8aa3b, v60
	v_add_f32_e32 v64, 1.0, v64
	v_add_f32_e32 v65, 1.0, v65
	v_exp_f32_e32 v60, v60
	v_rcp_f32_e32 v64, v64
	v_rcp_f32_e32 v65, v65
	v_add_f32_e32 v62, 1.0, v62
	v_add_f32_e32 v63, 1.0, v63
	v_mul_f32_e32 v50, v50, v83
	v_rcp_f32_e32 v62, v62
	v_rcp_f32_e32 v63, v63
	v_rcp_f32_e32 v58, v58
	v_add_f32_e32 v59, 1.0, v59
	v_max_f32_e32 v50, 0xc2a00000, v50
	v_rcp_f32_e32 v59, v59
	v_add_f32_e32 v60, 1.0, v60
	v_mul_f32_e32 v50, 0xbfb8aa3b, v50
	v_fma_f32 v64, v178, v64, v138
	v_fma_f32 v65, v177, v65, v139
	v_rcp_f32_e32 v60, v60
	v_exp_f32_e32 v50, v50
	v_log_f32_e32 v64, v64
	v_log_f32_e32 v65, v65
	v_fma_f32 v62, v180, v62, v136
	v_fma_f32 v63, v179, v63, v137
	v_fma_f32 v58, v170, v58, v133
	v_mul_f32_e32 v54, v54, v83
	v_log_f32_e32 v62, v62
	v_log_f32_e32 v63, v63
	v_log_f32_e32 v61, v58
	v_fma_f32 v58, v169, v59, v134
	v_max_f32_e32 v54, 0xc2a00000, v54
	v_mul_f32_e32 v51, v51, v83
	v_log_f32_e32 v67, v58
	v_fma_f32 v58, v155, v60, v135
	v_mul_f32_e32 v54, 0xbfb8aa3b, v54
	v_add_f32_e32 v50, 1.0, v50
	v_max_f32_e32 v51, 0xc2a00000, v51
	v_log_f32_e32 v68, v58
	v_cvt_pk_f16_f32 v59, v64, v65
	v_exp_f32_e32 v64, v54
	v_mul_f32_e32 v54, v55, v83
	v_rcp_f32_e32 v50, v50
	v_mul_f32_e32 v51, 0xbfb8aa3b, v51
	v_max_f32_e32 v54, 0xc2a00000, v54
	v_exp_f32_e32 v51, v51
	v_cvt_pk_f16_f32 v58, v62, v63
	v_lshl_add_u64 v[62:63], v[166:167], 0, s[14:15]
	v_mul_f32_e32 v54, 0xbfb8aa3b, v54
	s_mov_b32 s14, 0x80000
	v_exp_f32_e32 v65, v54
	v_add_co_u32_e32 v54, vcc, s14, v166
	v_cvt_pk_f16_f32 v60, v66, v61
	v_cvt_pk_f16_f32 v61, v67, v68
	v_addc_co_u32_e32 v55, vcc, 0, v167, vcc
	v_fma_f32 v50, v123, v50, v124
	s_waitcnt lgkmcnt(0)
	global_store_dwordx4 v[236:237], v[232:235], off offset:64
	ds_bpermute_b32 v238, v244, v58
	ds_bpermute_b32 v239, v244, v59
	ds_bpermute_b32 v240, v244, v60
	ds_bpermute_b32 v241, v244, v61
	ds_bpermute_b32 v242, v244, v54
	ds_bpermute_b32 v243, v244, v55
	v_mul_f32_e32 v56, v56, v83
	v_mul_f32_e32 v57, v57, v83
	v_log_f32_e32 v58, v50
	v_add_f32_e32 v50, 1.0, v51
	v_mul_f32_e32 v51, v52, v83
	v_max_f32_e32 v51, 0xc2a00000, v51
	v_mul_f32_e32 v51, 0xbfb8aa3b, v51
	v_exp_f32_e32 v51, v51
	v_rcp_f32_e32 v50, v50
	v_mul_f32_e32 v52, v53, v83
	v_max_f32_e32 v56, 0xc2a00000, v56
	v_add_f32_e32 v51, 1.0, v51
	v_rcp_f32_e32 v51, v51
	v_fma_f32 v50, v120, v50, v125
	v_log_f32_e32 v59, v50
	v_max_f32_e32 v57, 0xc2a00000, v57
	v_fma_f32 v50, v118, v51, v126
	v_log_f32_e32 v60, v50
	ds_read2_b32 v[50:51], v176 offset0:144 offset1:160
	v_max_f32_e32 v52, 0xc2a00000, v52
	v_mul_f32_e32 v56, 0xbfb8aa3b, v56
	v_mul_f32_e32 v57, 0xbfb8aa3b, v57
	v_mul_f32_e32 v52, 0xbfb8aa3b, v52
	v_exp_f32_e32 v56, v56
	v_exp_f32_e32 v57, v57
	v_exp_f32_e32 v52, v52
	s_waitcnt lgkmcnt(0)
	v_mul_f32_e32 v42, v42, v50
	v_max_f32_e32 v42, 0xc2a00000, v42
	v_add_f32_e32 v64, 1.0, v64
	v_add_f32_e32 v65, 1.0, v65
	v_add_f32_e32 v56, 1.0, v56
	v_add_f32_e32 v57, 1.0, v57
	v_add_f32_e32 v52, 1.0, v52
	v_mul_f32_e32 v42, 0xbfb8aa3b, v42
	v_rcp_f32_e32 v64, v64
	v_rcp_f32_e32 v65, v65
	v_rcp_f32_e32 v56, v56
	v_rcp_f32_e32 v57, v57
	v_rcp_f32_e32 v52, v52
	v_exp_f32_e32 v42, v42
	v_mul_f32_e32 v43, v43, v50
	v_fma_f32 v54, v153, v64, v128
	v_fma_f32 v55, v168, v65, v129
	v_fma_f32 v56, v121, v56, v130
	v_fma_f32 v57, v122, v57, v131
	v_fma_f32 v52, v119, v52, v127
	v_add_f32_e32 v42, 1.0, v42
	v_max_f32_e32 v43, 0xc2a00000, v43
	v_log_f32_e32 v54, v54
	v_log_f32_e32 v55, v55
	v_log_f32_e32 v56, v56
	v_log_f32_e32 v57, v57
	v_log_f32_e32 v61, v52
	v_rcp_f32_e32 v42, v42
	v_mul_f32_e32 v43, 0xbfb8aa3b, v43
	v_exp_f32_e32 v43, v43
	v_mul_f32_e32 v48, v48, v50
	v_mul_f32_e32 v49, v49, v50
	v_max_f32_e32 v48, 0xc2a00000, v48
	v_max_f32_e32 v49, 0xc2a00000, v49
	v_cvt_pk_f16_f32 v52, v54, v55
	v_cvt_pk_f16_f32 v53, v56, v57
	v_cvt_pk_f16_f32 v54, v58, v59
	v_mul_f32_e32 v46, v46, v50
	v_mul_f32_e32 v47, v47, v50
	v_cvt_pk_f16_f32 v55, v60, v61
	v_mul_f32_e32 v48, 0xbfb8aa3b, v48
	v_mul_f32_e32 v49, 0xbfb8aa3b, v49
	v_fma_f32 v42, v171, v42, v132
	v_max_f32_e32 v46, 0xc2a00000, v46
	v_max_f32_e32 v47, 0xc2a00000, v47
	s_waitcnt lgkmcnt(0)
	global_store_dwordx4 v[242:243], v[238:241], off
	ds_bpermute_b32 v232, v244, v52
	ds_bpermute_b32 v233, v244, v53
	ds_bpermute_b32 v234, v244, v54
	ds_bpermute_b32 v235, v244, v55
	ds_bpermute_b32 v236, v244, v62
	ds_bpermute_b32 v237, v244, v63
	v_exp_f32_e32 v48, v48
	v_exp_f32_e32 v49, v49
	v_log_f32_e32 v52, v42
	v_add_f32_e32 v42, 1.0, v43
	v_mul_f32_e32 v43, v44, v50
	v_mul_f32_e32 v46, 0xbfb8aa3b, v46
	v_mul_f32_e32 v47, 0xbfb8aa3b, v47
	v_max_f32_e32 v43, 0xc2a00000, v43
	v_mul_f32_e32 v44, v45, v50
	v_exp_f32_e32 v46, v46
	v_exp_f32_e32 v47, v47
	v_mul_f32_e32 v43, 0xbfb8aa3b, v43
	v_max_f32_e32 v44, 0xc2a00000, v44
	v_exp_f32_e32 v43, v43
	v_mul_f32_e32 v44, 0xbfb8aa3b, v44
	v_add_f32_e32 v48, 1.0, v48
	v_add_f32_e32 v49, 1.0, v49
	v_exp_f32_e32 v44, v44
	v_rcp_f32_e32 v48, v48
	v_rcp_f32_e32 v49, v49
	v_add_f32_e32 v46, 1.0, v46
	v_add_f32_e32 v47, 1.0, v47
	v_mul_f32_e32 v34, v34, v50
	v_rcp_f32_e32 v46, v46
	v_rcp_f32_e32 v47, v47
	v_rcp_f32_e32 v42, v42
	v_add_f32_e32 v43, 1.0, v43
	v_max_f32_e32 v34, 0xc2a00000, v34
	v_rcp_f32_e32 v43, v43
	v_add_f32_e32 v44, 1.0, v44
	v_mul_f32_e32 v34, 0xbfb8aa3b, v34
	v_fma_f32 v48, v178, v48, v138
	v_fma_f32 v49, v177, v49, v139
	v_rcp_f32_e32 v44, v44
	v_exp_f32_e32 v34, v34
	v_log_f32_e32 v48, v48
	v_log_f32_e32 v49, v49
	v_fma_f32 v46, v180, v46, v136
	v_fma_f32 v47, v179, v47, v137
	v_fma_f32 v42, v170, v42, v133
	v_mul_f32_e32 v38, v38, v50
	v_log_f32_e32 v46, v46
	v_log_f32_e32 v47, v47
	v_log_f32_e32 v45, v42
	v_fma_f32 v42, v169, v43, v134
	v_max_f32_e32 v38, 0xc2a00000, v38
	v_mul_f32_e32 v35, v35, v50
	v_log_f32_e32 v53, v42
	v_fma_f32 v42, v155, v44, v135
	v_mul_f32_e32 v38, 0xbfb8aa3b, v38
	v_add_f32_e32 v34, 1.0, v34
	v_max_f32_e32 v35, 0xc2a00000, v35
	v_log_f32_e32 v54, v42
	v_cvt_pk_f16_f32 v43, v48, v49
	v_exp_f32_e32 v48, v38
	v_mul_f32_e32 v38, v39, v50
	v_rcp_f32_e32 v34, v34
	v_mul_f32_e32 v35, 0xbfb8aa3b, v35
	s_mov_b64 s[14:15], 0x90000
	v_max_f32_e32 v38, 0xc2a00000, v38
	v_exp_f32_e32 v35, v35
	v_cvt_pk_f16_f32 v42, v46, v47
	v_lshl_add_u64 v[46:47], v[166:167], 0, s[14:15]
	v_mul_f32_e32 v38, 0xbfb8aa3b, v38
	s_mov_b32 s14, 0x90000
	v_exp_f32_e32 v49, v38
	v_add_co_u32_e32 v38, vcc, s14, v166
	v_cvt_pk_f16_f32 v44, v52, v45
	v_cvt_pk_f16_f32 v45, v53, v54
	v_addc_co_u32_e32 v39, vcc, 0, v167, vcc
	v_fma_f32 v34, v123, v34, v124
	s_waitcnt lgkmcnt(0)
	global_store_dwordx4 v[236:237], v[232:235], off offset:64
	ds_bpermute_b32 v238, v244, v42
	ds_bpermute_b32 v239, v244, v43
	ds_bpermute_b32 v240, v244, v44
	ds_bpermute_b32 v241, v244, v45
	ds_bpermute_b32 v242, v244, v38
	ds_bpermute_b32 v243, v244, v39
	v_mul_f32_e32 v40, v40, v50
	v_mul_f32_e32 v41, v41, v50
	v_log_f32_e32 v42, v34
	v_add_f32_e32 v34, 1.0, v35
	v_mul_f32_e32 v35, v36, v50
	v_max_f32_e32 v35, 0xc2a00000, v35
	v_mul_f32_e32 v36, v37, v50
	v_max_f32_e32 v40, 0xc2a00000, v40
	v_max_f32_e32 v41, 0xc2a00000, v41
	v_mul_f32_e32 v35, 0xbfb8aa3b, v35
	v_max_f32_e32 v36, 0xc2a00000, v36
	v_mul_f32_e32 v40, 0xbfb8aa3b, v40
	v_mul_f32_e32 v41, 0xbfb8aa3b, v41
	v_exp_f32_e32 v35, v35
	v_mul_f32_e32 v36, 0xbfb8aa3b, v36
	v_exp_f32_e32 v40, v40
	v_exp_f32_e32 v41, v41
	v_exp_f32_e32 v36, v36
	v_mul_f32_e32 v26, v26, v51
	v_rcp_f32_e32 v34, v34
	v_add_f32_e32 v35, 1.0, v35
	v_max_f32_e32 v26, 0xc2a00000, v26
	v_add_f32_e32 v48, 1.0, v48
	v_add_f32_e32 v49, 1.0, v49
	v_add_f32_e32 v40, 1.0, v40
	v_add_f32_e32 v41, 1.0, v41
	v_rcp_f32_e32 v35, v35
	v_add_f32_e32 v36, 1.0, v36
	v_mul_f32_e32 v26, 0xbfb8aa3b, v26
	v_rcp_f32_e32 v48, v48
	v_rcp_f32_e32 v49, v49
	v_rcp_f32_e32 v40, v40
	v_rcp_f32_e32 v41, v41
	v_rcp_f32_e32 v36, v36
	v_exp_f32_e32 v26, v26
	v_fma_f32 v34, v120, v34, v125
	v_log_f32_e32 v37, v34
	v_fma_f32 v34, v118, v35, v126
	v_mul_f32_e32 v27, v27, v51
	v_fma_f32 v38, v153, v48, v128
	v_fma_f32 v39, v168, v49, v129
	v_fma_f32 v40, v121, v40, v130
	v_fma_f32 v41, v122, v41, v131
	v_log_f32_e32 v43, v34
	v_fma_f32 v34, v119, v36, v127
	v_add_f32_e32 v26, 1.0, v26
	v_max_f32_e32 v27, 0xc2a00000, v27
	v_log_f32_e32 v38, v38
	v_log_f32_e32 v39, v39
	v_log_f32_e32 v40, v40
	v_log_f32_e32 v41, v41
	v_log_f32_e32 v44, v34
	v_rcp_f32_e32 v26, v26
	v_mul_f32_e32 v27, 0xbfb8aa3b, v27
	v_exp_f32_e32 v27, v27
	v_mul_f32_e32 v32, v32, v51
	v_mul_f32_e32 v33, v33, v51
	v_max_f32_e32 v32, 0xc2a00000, v32
	v_max_f32_e32 v33, 0xc2a00000, v33
	v_cvt_pk_f16_f32 v34, v38, v39
	v_cvt_pk_f16_f32 v35, v40, v41
	v_cvt_pk_f16_f32 v36, v42, v37
	v_mul_f32_e32 v30, v30, v51
	v_mul_f32_e32 v31, v31, v51
	v_cvt_pk_f16_f32 v37, v43, v44
	v_mul_f32_e32 v32, 0xbfb8aa3b, v32
	v_mul_f32_e32 v33, 0xbfb8aa3b, v33
	v_fma_f32 v26, v171, v26, v132
	v_max_f32_e32 v30, 0xc2a00000, v30
	v_max_f32_e32 v31, 0xc2a00000, v31
	s_waitcnt lgkmcnt(0)
	global_store_dwordx4 v[242:243], v[238:241], off
	ds_bpermute_b32 v232, v244, v34
	ds_bpermute_b32 v233, v244, v35
	ds_bpermute_b32 v234, v244, v36
	ds_bpermute_b32 v235, v244, v37
	ds_bpermute_b32 v236, v244, v46
	ds_bpermute_b32 v237, v244, v47
	v_exp_f32_e32 v32, v32
	v_exp_f32_e32 v33, v33
	v_log_f32_e32 v34, v26
	v_add_f32_e32 v26, 1.0, v27
	v_mul_f32_e32 v27, v28, v51
	v_mul_f32_e32 v30, 0xbfb8aa3b, v30
	v_mul_f32_e32 v31, 0xbfb8aa3b, v31
	v_max_f32_e32 v27, 0xc2a00000, v27
	v_mul_f32_e32 v28, v29, v51
	v_exp_f32_e32 v30, v30
	v_exp_f32_e32 v31, v31
	v_mul_f32_e32 v27, 0xbfb8aa3b, v27
	v_max_f32_e32 v28, 0xc2a00000, v28
	v_exp_f32_e32 v27, v27
	v_mul_f32_e32 v28, 0xbfb8aa3b, v28
	v_add_f32_e32 v32, 1.0, v32
	v_add_f32_e32 v33, 1.0, v33
	v_exp_f32_e32 v28, v28
	v_rcp_f32_e32 v32, v32
	v_rcp_f32_e32 v33, v33
	v_add_f32_e32 v30, 1.0, v30
	v_add_f32_e32 v31, 1.0, v31
	v_mul_f32_e32 v18, v18, v51
	v_rcp_f32_e32 v30, v30
	v_rcp_f32_e32 v31, v31
	v_rcp_f32_e32 v26, v26
	v_add_f32_e32 v27, 1.0, v27
	v_max_f32_e32 v18, 0xc2a00000, v18
	v_rcp_f32_e32 v27, v27
	v_add_f32_e32 v28, 1.0, v28
	v_mul_f32_e32 v18, 0xbfb8aa3b, v18
	v_fma_f32 v32, v178, v32, v138
	v_fma_f32 v33, v177, v33, v139
	v_rcp_f32_e32 v28, v28
	v_exp_f32_e32 v18, v18
	v_log_f32_e32 v32, v32
	v_log_f32_e32 v33, v33
	v_fma_f32 v30, v180, v30, v136
	v_fma_f32 v31, v179, v31, v137
	v_fma_f32 v26, v170, v26, v133
	v_mul_f32_e32 v22, v22, v51
	v_log_f32_e32 v30, v30
	v_log_f32_e32 v31, v31
	v_log_f32_e32 v29, v26
	v_fma_f32 v26, v169, v27, v134
	v_max_f32_e32 v22, 0xc2a00000, v22
	v_mul_f32_e32 v19, v19, v51
	v_log_f32_e32 v35, v26
	v_fma_f32 v26, v155, v28, v135
	v_mul_f32_e32 v22, 0xbfb8aa3b, v22
	v_add_f32_e32 v18, 1.0, v18
	v_max_f32_e32 v19, 0xc2a00000, v19
	v_log_f32_e32 v36, v26
	v_cvt_pk_f16_f32 v27, v32, v33
	v_exp_f32_e32 v32, v22
	v_mul_f32_e32 v22, v23, v51
	v_rcp_f32_e32 v18, v18
	v_mul_f32_e32 v19, 0xbfb8aa3b, v19
	s_mov_b64 s[14:15], 0xa0000
	v_max_f32_e32 v22, 0xc2a00000, v22
	v_exp_f32_e32 v19, v19
	v_cvt_pk_f16_f32 v26, v30, v31
	v_lshl_add_u64 v[30:31], v[166:167], 0, s[14:15]
	v_mul_f32_e32 v22, 0xbfb8aa3b, v22
	s_mov_b32 s14, 0xa0000
	v_exp_f32_e32 v33, v22
	v_add_co_u32_e32 v22, vcc, s14, v166
	v_cvt_pk_f16_f32 v28, v34, v29
	v_cvt_pk_f16_f32 v29, v35, v36
	v_addc_co_u32_e32 v23, vcc, 0, v167, vcc
	v_fma_f32 v18, v123, v18, v124
	s_waitcnt lgkmcnt(0)
	global_store_dwordx4 v[236:237], v[232:235], off offset:64
	ds_bpermute_b32 v238, v244, v26
	ds_bpermute_b32 v239, v244, v27
	ds_bpermute_b32 v240, v244, v28
	ds_bpermute_b32 v241, v244, v29
	ds_bpermute_b32 v242, v244, v22
	ds_bpermute_b32 v243, v244, v23
	v_mul_f32_e32 v24, v24, v51
	v_mul_f32_e32 v25, v25, v51
	v_log_f32_e32 v26, v18
	v_add_f32_e32 v18, 1.0, v19
	v_mul_f32_e32 v19, v20, v51
	v_max_f32_e32 v19, 0xc2a00000, v19
	v_mul_f32_e32 v20, v21, v51
	ds_read_b32 v28, v176 offset:704
	v_max_f32_e32 v24, 0xc2a00000, v24
	v_max_f32_e32 v25, 0xc2a00000, v25
	v_mul_f32_e32 v19, 0xbfb8aa3b, v19
	v_max_f32_e32 v20, 0xc2a00000, v20
	v_mul_f32_e32 v24, 0xbfb8aa3b, v24
	v_mul_f32_e32 v25, 0xbfb8aa3b, v25
	v_exp_f32_e32 v19, v19
	v_mul_f32_e32 v20, 0xbfb8aa3b, v20
	v_exp_f32_e32 v24, v24
	v_exp_f32_e32 v25, v25
	v_exp_f32_e32 v20, v20
	s_waitcnt lgkmcnt(0)
	v_mul_f32_e32 v10, v10, v28
	v_rcp_f32_e32 v18, v18
	v_add_f32_e32 v19, 1.0, v19
	v_max_f32_e32 v10, 0xc2a00000, v10
	v_add_f32_e32 v32, 1.0, v32
	v_add_f32_e32 v33, 1.0, v33
	v_add_f32_e32 v24, 1.0, v24
	v_add_f32_e32 v25, 1.0, v25
	v_rcp_f32_e32 v19, v19
	v_add_f32_e32 v20, 1.0, v20
	v_mul_f32_e32 v10, 0xbfb8aa3b, v10
	v_rcp_f32_e32 v32, v32
	v_rcp_f32_e32 v33, v33
	v_rcp_f32_e32 v24, v24
	v_rcp_f32_e32 v25, v25
	v_rcp_f32_e32 v20, v20
	v_exp_f32_e32 v10, v10
	v_fma_f32 v18, v120, v18, v125
	v_log_f32_e32 v21, v18
	v_fma_f32 v18, v118, v19, v126
	v_mul_f32_e32 v11, v11, v28
	v_fma_f32 v22, v153, v32, v128
	v_fma_f32 v23, v168, v33, v129
	v_fma_f32 v24, v121, v24, v130
	v_fma_f32 v25, v122, v25, v131
	v_log_f32_e32 v27, v18
	v_fma_f32 v18, v119, v20, v127
	v_add_f32_e32 v10, 1.0, v10
	v_max_f32_e32 v11, 0xc2a00000, v11
	v_log_f32_e32 v22, v22
	v_log_f32_e32 v23, v23
	v_log_f32_e32 v24, v24
	v_log_f32_e32 v25, v25
	v_log_f32_e32 v29, v18
	v_rcp_f32_e32 v10, v10
	v_mul_f32_e32 v11, 0xbfb8aa3b, v11
	v_mul_f32_e32 v14, v14, v28
	v_mul_f32_e32 v15, v15, v28
	v_exp_f32_e32 v11, v11
	v_max_f32_e32 v14, 0xc2a00000, v14
	v_max_f32_e32 v15, 0xc2a00000, v15
	v_mul_f32_e32 v14, 0xbfb8aa3b, v14
	v_mul_f32_e32 v15, 0xbfb8aa3b, v15
	v_cvt_pk_f16_f32 v18, v22, v23
	v_cvt_pk_f16_f32 v19, v24, v25
	v_cvt_pk_f16_f32 v20, v26, v21
	v_exp_f32_e32 v14, v14
	v_exp_f32_e32 v15, v15
	v_cvt_pk_f16_f32 v21, v27, v29
	v_fma_f32 v10, v171, v10, v132
	s_waitcnt lgkmcnt(0)
	global_store_dwordx4 v[242:243], v[238:241], off
	ds_bpermute_b32 v232, v244, v18
	ds_bpermute_b32 v233, v244, v19
	ds_bpermute_b32 v234, v244, v20
	ds_bpermute_b32 v235, v244, v21
	ds_bpermute_b32 v236, v244, v30
	ds_bpermute_b32 v237, v244, v31
	v_add_f32_e32 v14, 1.0, v14
	v_add_f32_e32 v15, 1.0, v15
	v_log_f32_e32 v18, v10
	v_add_f32_e32 v10, 1.0, v11
	v_mul_f32_e32 v11, v12, v28
	v_max_f32_e32 v11, 0xc2a00000, v11
	v_mul_f32_e32 v11, 0xbfb8aa3b, v11
	v_exp_f32_e32 v11, v11
	v_rcp_f32_e32 v14, v14
	v_rcp_f32_e32 v15, v15
	v_mul_f32_e32 v16, v16, v28
	v_mul_f32_e32 v17, v17, v28
	v_rcp_f32_e32 v10, v10
	v_mul_f32_e32 v12, v13, v28
	v_add_f32_e32 v11, 1.0, v11
	v_fma_f32 v14, v180, v14, v136
	v_fma_f32 v15, v179, v15, v137
	v_max_f32_e32 v16, 0xc2a00000, v16
	v_max_f32_e32 v17, 0xc2a00000, v17
	v_max_f32_e32 v12, 0xc2a00000, v12
	v_rcp_f32_e32 v11, v11
	v_log_f32_e32 v14, v14
	v_mul_f32_e32 v16, 0xbfb8aa3b, v16
	v_mul_f32_e32 v17, 0xbfb8aa3b, v17
	v_log_f32_e32 v15, v15
	v_mul_f32_e32 v12, 0xbfb8aa3b, v12
	v_exp_f32_e32 v16, v16
	v_exp_f32_e32 v17, v17
	v_exp_f32_e32 v12, v12
	v_mul_f32_e32 v6, v6, v28
	v_fma_f32 v10, v170, v10, v133
	v_max_f32_e32 v6, 0xc2a00000, v6
	v_log_f32_e32 v13, v10
	v_fma_f32 v10, v169, v11, v134
	v_mul_f32_e32 v6, 0xbfb8aa3b, v6
	v_log_f32_e32 v19, v10
	v_cvt_pk_f16_f32 v10, v14, v15
	v_exp_f32_e32 v14, v6
	v_mul_f32_e32 v6, v7, v28
	v_mul_f32_e32 v8, v8, v28
	v_mul_f32_e32 v9, v9, v28
	v_mul_f32_e32 v2, v2, v28
	v_mul_f32_e32 v3, v3, v28
	v_mul_f32_e32 v4, v4, v28
	v_mul_f32_e32 v5, v5, v28
	v_add_f32_e32 v16, 1.0, v16
	v_add_f32_e32 v17, 1.0, v17
	v_add_f32_e32 v12, 1.0, v12
	v_max_f32_e32 v6, 0xc2a00000, v6
	v_max_f32_e32 v8, 0xc2a00000, v8
	v_max_f32_e32 v9, 0xc2a00000, v9
	v_max_f32_e32 v2, 0xc2a00000, v2
	v_max_f32_e32 v3, 0xc2a00000, v3
	v_max_f32_e32 v4, 0xc2a00000, v4
	v_max_f32_e32 v5, 0xc2a00000, v5
	v_rcp_f32_e32 v16, v16
	v_rcp_f32_e32 v17, v17
	v_rcp_f32_e32 v12, v12
	v_mul_f32_e32 v6, 0xbfb8aa3b, v6
	v_mul_f32_e32 v8, 0xbfb8aa3b, v8
	v_mul_f32_e32 v9, 0xbfb8aa3b, v9
	v_mul_f32_e32 v2, 0xbfb8aa3b, v2
	v_mul_f32_e32 v3, 0xbfb8aa3b, v3
	v_mul_f32_e32 v4, 0xbfb8aa3b, v4
	v_mul_f32_e32 v5, 0xbfb8aa3b, v5
	v_exp_f32_e32 v15, v6
	v_exp_f32_e32 v8, v8
	v_exp_f32_e32 v9, v9
	v_exp_f32_e32 v2, v2
	v_exp_f32_e32 v3, v3
	v_exp_f32_e32 v4, v4
	v_exp_f32_e32 v5, v5
	v_fma_f32 v16, v178, v16, v138
	v_fmac_f32_e32 v139, v177, v17
	v_fmac_f32_e32 v135, v155, v12
	v_log_f32_e32 v16, v16
	v_log_f32_e32 v17, v139
	v_log_f32_e32 v20, v135
	v_add_f32_e32 v14, 1.0, v14
	v_add_f32_e32 v15, 1.0, v15
	v_add_f32_e32 v8, 1.0, v8
	v_add_f32_e32 v9, 1.0, v9
	v_add_f32_e32 v2, 1.0, v2
	v_add_f32_e32 v3, 1.0, v3
	v_add_f32_e32 v4, 1.0, v4
	v_add_f32_e32 v5, 1.0, v5
	s_mov_b64 s[14:15], 0xb0000
	v_rcp_f32_e32 v14, v14
	v_rcp_f32_e32 v15, v15
	v_rcp_f32_e32 v8, v8
	v_rcp_f32_e32 v9, v9
	v_rcp_f32_e32 v2, v2
	v_rcp_f32_e32 v3, v3
	v_rcp_f32_e32 v4, v4
	v_rcp_f32_e32 v5, v5
	v_lshl_add_u64 v[136:137], v[166:167], 0, s[14:15]
	s_mov_b32 s14, 0xb0000
	v_add_co_u32_e32 v6, vcc, s14, v166
	v_cvt_pk_f16_f32 v11, v16, v17
	v_cvt_pk_f16_f32 v12, v18, v13
	v_cvt_pk_f16_f32 v13, v19, v20
	v_addc_co_u32_e32 v7, vcc, 0, v167, vcc
	s_waitcnt lgkmcnt(0)
	global_store_dwordx4 v[236:237], v[232:235], off offset:64
	ds_bpermute_b32 v238, v244, v10
	ds_bpermute_b32 v239, v244, v11
	ds_bpermute_b32 v240, v244, v12
	ds_bpermute_b32 v241, v244, v13
	ds_bpermute_b32 v242, v244, v6
	ds_bpermute_b32 v243, v244, v7
	v_fma_f32 v6, v153, v14, v128
	v_fma_f32 v7, v168, v15, v129
	v_fma_f32 v8, v121, v8, v130
	v_fmac_f32_e32 v131, v122, v9
	v_fma_f32 v2, v123, v2, v124
	v_fma_f32 v3, v120, v3, v125
	v_fma_f32 v4, v118, v4, v126
	v_fmac_f32_e32 v127, v119, v5
	v_log_f32_e32 v6, v6
	v_log_f32_e32 v7, v7
	v_log_f32_e32 v8, v8
	v_log_f32_e32 v9, v131
	v_log_f32_e32 v2, v2
	v_log_f32_e32 v3, v3
	v_log_f32_e32 v4, v4
	v_log_f32_e32 v5, v127
	v_cvt_pk_f16_f32 v196, v181, v182
	v_cvt_pk_f16_f32 v132, v6, v7
	v_cvt_pk_f16_f32 v133, v8, v9
	v_cvt_pk_f16_f32 v134, v2, v3
	v_cvt_pk_f16_f32 v135, v4, v5
	s_waitcnt lgkmcnt(0)
	global_store_dwordx4 v[242:243], v[238:241], off
	ds_bpermute_b32 v232, v244, v194
	ds_bpermute_b32 v233, v244, v195
	ds_bpermute_b32 v234, v244, v196
	ds_bpermute_b32 v235, v244, v197
	ds_bpermute_b32 v236, v244, v166
	ds_bpermute_b32 v237, v244, v167
	s_andn2_b64 vcc, exec, s[38:39]
	s_mov_b64 s[28:29], -1
	s_waitcnt lgkmcnt(0)
	global_store_dwordx4 v[236:237], v[232:235], off offset:64
	ds_bpermute_b32 v238, v244, v132
	ds_bpermute_b32 v239, v244, v133
	ds_bpermute_b32 v240, v244, v134
	ds_bpermute_b32 v241, v244, v135
	ds_bpermute_b32 v242, v244, v136
	ds_bpermute_b32 v243, v244, v137
	s_waitcnt lgkmcnt(0)
	global_store_dwordx4 v[242:243], v[238:241], off offset:64
	s_cbranch_vccnz .LBB0_495

.LBB0_1082:
	v_mbcnt_lo_u32_b32 v244, -1, 0
	v_mbcnt_hi_u32_b32 v244, -1, v244
	v_lshrrev_b32_e32 v245, 2, v244
	v_and_b32_e32 v244, 3, v244
	v_lshl_add_u32 v244, v244, 4, v245
	v_lshlrev_b32_e32 v244, 2, v244
	v_pk_mul_f32 v[148:149], v[118:119], v[118:119]
	v_pk_mul_f32 v[150:151], v[126:127], v[126:127]
	v_pk_fma_f32 v[148:149], v[116:117], v[116:117], v[148:149]
	v_pk_fma_f32 v[150:151], v[124:125], v[124:125], v[150:151]
	v_lshl_add_u32 v144, s46, 8, v1
	v_pk_add_f32 v[152:153], v[148:149], v[150:151]
	v_cvt_pk_bf16_f32 v149, v118, v119
	v_cvt_pk_bf16_f32 v150, v124, v125
	v_pk_mul_f32 v[118:119], v[122:123], v[122:123]
	v_pk_mul_f32 v[124:125], v[130:131], v[130:131]
	v_pk_fma_f32 v[118:119], v[120:121], v[120:121], v[118:119]
	v_pk_fma_f32 v[124:125], v[128:129], v[128:129], v[124:125]
	s_lshl_b32 s16, s46, 5
	v_pk_add_f32 v[118:119], v[118:119], v[124:125]
	s_lshl_b32 s46, s48, 2
	v_pk_add_f32 v[124:125], v[152:153], v[118:119]
	s_or_b32 s17, s46, s12
	v_add_f32_e32 v124, v124, v125
	ds_swizzle_b32 v125, v124 offset:swizzle(SWAP,16)
	s_add_i32 s16, s17, s16
	s_ashr_i32 s17, s16, 31
	s_lshl_b64 s[16:17], s[16:17], 15
	v_cvt_pk_bf16_f32 v148, v116, v117
	v_lshl_add_u64 v[116:117], v[138:139], 0, s[16:17]
	v_cvt_pk_bf16_f32 v118, v120, v121
	v_cvt_pk_bf16_f32 v119, v122, v123
	v_cvt_pk_bf16_f32 v120, v128, v129
	v_cvt_pk_bf16_f32 v121, v130, v131
	ds_bpermute_b32 v232, v244, v118
	ds_bpermute_b32 v233, v244, v119
	ds_bpermute_b32 v234, v244, v120
	ds_bpermute_b32 v235, v244, v121
	ds_bpermute_b32 v236, v244, v116
	ds_bpermute_b32 v237, v244, v117
	s_ashr_i32 s47, s46, 31
	v_cvt_pk_bf16_f32 v151, v126, v127
	s_waitcnt lgkmcnt(0)
	global_store_dwordx4 v[236:237], v[232:235], off offset:64
	ds_bpermute_b32 v238, v244, v148
	ds_bpermute_b32 v239, v244, v149
	ds_bpermute_b32 v240, v244, v150
	ds_bpermute_b32 v241, v244, v151
	ds_bpermute_b32 v242, v244, v116
	ds_bpermute_b32 v243, v244, v117
	s_waitcnt lgkmcnt(0)
	v_add_f32_e32 v118, v124, v125
	v_mov_b32_e32 v119, v118
	s_nop 1
	v_permlane32_swap_b32_e32 v118, v119
	s_waitcnt lgkmcnt(0)
	global_store_dwordx4 v[242:243], v[238:241], off
	s_and_saveexec_b64 s[48:49], s[38:39]
	s_cbranch_execz .LBB0_1084
	v_ashrrev_i32_e32 v145, 31, v144
	v_add_f32_e32 v120, v118, v119
	v_lshlrev_b64 v[118:119], 7, v[144:145]
	v_lshl_add_u64 v[118:119], s[8:9], 0, v[118:119]
	v_lshl_add_u64 v[118:119], s[46:47], 2, v[118:119]
	s_lshl_b32 s24, s12, 2
	v_lshl_add_u64 v[118:119], v[118:119], 0, s[24:25]
	global_store_dword v[118:119], v120, off
.LBB0_1084:
	s_or_b64 exec, exec, s[48:49]
	v_pk_mul_f32 v[118:119], v[100:101], v[100:101]
	v_pk_mul_f32 v[120:121], v[104:105], v[104:105]
	v_pk_fma_f32 v[118:119], v[98:99], v[98:99], v[118:119]
	v_cvt_pk_bf16_f32 v98, v98, v99
	v_cvt_pk_bf16_f32 v99, v100, v101
	v_cvt_pk_bf16_f32 v100, v102, v103
	v_cvt_pk_bf16_f32 v101, v104, v105
	ds_bpermute_b32 v232, v244, v98
	ds_bpermute_b32 v233, v244, v99
	ds_bpermute_b32 v234, v244, v100
	ds_bpermute_b32 v235, v244, v101
	ds_bpermute_b32 v236, v244, v116
	ds_bpermute_b32 v237, v244, v117
	v_pk_fma_f32 v[120:121], v[102:103], v[102:103], v[120:121]
	s_nop 0
	v_pk_mul_f32 v[98:99], v[108:109], v[108:109]
	v_pk_mul_f32 v[100:101], v[112:113], v[112:113]
	v_pk_fma_f32 v[98:99], v[106:107], v[106:107], v[98:99]
	v_pk_fma_f32 v[100:101], v[110:111], v[110:111], v[100:101]
	v_pk_add_f32 v[118:119], v[118:119], v[120:121]
	v_pk_add_f32 v[98:99], v[98:99], v[100:101]
	s_nop 0
	v_pk_add_f32 v[100:101], v[118:119], v[98:99]
	v_cvt_pk_bf16_f32 v98, v106, v107
	v_cvt_pk_bf16_f32 v99, v108, v109
	s_nop 0
	v_add_f32_e32 v102, v100, v101
	ds_swizzle_b32 v103, v102 offset:swizzle(SWAP,16)
	v_cvt_pk_bf16_f32 v100, v110, v111
	v_cvt_pk_bf16_f32 v101, v112, v113
	s_waitcnt lgkmcnt(0)
	global_store_dwordx4 v[236:237], v[232:235], off offset:2048
	ds_bpermute_b32 v238, v244, v98
	ds_bpermute_b32 v239, v244, v99
	ds_bpermute_b32 v240, v244, v100
	ds_bpermute_b32 v241, v244, v101
	ds_bpermute_b32 v242, v244, v116
	ds_bpermute_b32 v243, v244, v117
	s_waitcnt lgkmcnt(0)
	s_nop 0
	v_add_f32_e32 v98, v102, v103
	v_mov_b32_e32 v99, v98
	s_nop 1
	v_permlane32_swap_b32_e32 v98, v99
	s_waitcnt lgkmcnt(0)
	global_store_dwordx4 v[242:243], v[238:241], off offset:2112
	s_and_saveexec_b64 s[48:49], s[38:39]
	s_cbranch_execz .LBB0_1086
	v_or_b32_e32 v100, 16, v144
	v_ashrrev_i32_e32 v101, 31, v100
	v_add_f32_e32 v102, v98, v99
	v_lshlrev_b64 v[98:99], 7, v[100:101]
	v_lshl_add_u64 v[98:99], s[8:9], 0, v[98:99]
	v_lshl_add_u64 v[98:99], s[46:47], 2, v[98:99]
	s_lshl_b32 s24, s12, 2
	v_lshl_add_u64 v[98:99], v[98:99], 0, s[24:25]
	global_store_dword v[98:99], v102, off
.LBB0_1086:
	s_or_b64 exec, exec, s[48:49]
	v_pk_mul_f32 v[98:99], v[84:85], v[84:85]
	v_pk_mul_f32 v[100:101], v[92:93], v[92:93]
	v_pk_fma_f32 v[98:99], v[82:83], v[82:83], v[98:99]
	v_pk_fma_f32 v[100:101], v[90:91], v[90:91], v[100:101]
	s_nop 0
	v_pk_add_f32 v[102:103], v[98:99], v[100:101]
	v_cvt_pk_bf16_f32 v99, v84, v85
	v_cvt_pk_bf16_f32 v100, v90, v91
	v_pk_mul_f32 v[84:85], v[88:89], v[88:89]
	v_pk_mul_f32 v[90:91], v[96:97], v[96:97]
	v_pk_fma_f32 v[84:85], v[86:87], v[86:87], v[84:85]
	v_pk_fma_f32 v[90:91], v[94:95], v[94:95], v[90:91]
	v_cvt_pk_bf16_f32 v98, v82, v83
	v_add_co_u32_e32 v82, vcc, s73, v116
	v_pk_add_f32 v[84:85], v[84:85], v[90:91]
	s_nop 0
	v_addc_co_u32_e32 v83, vcc, 0, v117, vcc
	v_pk_add_f32 v[90:91], v[102:103], v[84:85]
	v_cvt_pk_bf16_f32 v84, v86, v87
	v_cvt_pk_bf16_f32 v85, v88, v89
	v_cvt_pk_bf16_f32 v86, v94, v95
	v_cvt_pk_bf16_f32 v87, v96, v97
	ds_bpermute_b32 v232, v244, v84
	ds_bpermute_b32 v233, v244, v85
	ds_bpermute_b32 v234, v244, v86
	ds_bpermute_b32 v235, v244, v87
	ds_bpermute_b32 v236, v244, v82
	ds_bpermute_b32 v237, v244, v83
	v_add_f32_e32 v90, v90, v91
	ds_swizzle_b32 v91, v90 offset:swizzle(SWAP,16)
	v_cvt_pk_bf16_f32 v101, v92, v93
	s_waitcnt lgkmcnt(0)
	global_store_dwordx4 v[236:237], v[232:235], off offset:64
	ds_bpermute_b32 v238, v244, v98
	ds_bpermute_b32 v239, v244, v99
	ds_bpermute_b32 v240, v244, v100
	ds_bpermute_b32 v241, v244, v101
	ds_bpermute_b32 v242, v244, v82
	ds_bpermute_b32 v243, v244, v83
	s_waitcnt lgkmcnt(0)
	v_add_f32_e32 v84, v90, v91
	v_mov_b32_e32 v85, v84
	s_nop 1
	v_permlane32_swap_b32_e32 v84, v85
	s_waitcnt lgkmcnt(0)
	global_store_dwordx4 v[242:243], v[238:241], off
	s_and_saveexec_b64 s[48:49], s[38:39]
	s_cbranch_execz .LBB0_1088
	v_or_b32_e32 v86, 32, v144
	v_ashrrev_i32_e32 v87, 31, v86
	v_add_f32_e32 v88, v84, v85
	v_lshlrev_b64 v[84:85], 7, v[86:87]
	v_lshl_add_u64 v[84:85], s[8:9], 0, v[84:85]
	v_lshl_add_u64 v[84:85], s[46:47], 2, v[84:85]
	s_lshl_b32 s24, s12, 2
	v_lshl_add_u64 v[84:85], v[84:85], 0, s[24:25]
	global_store_dword v[84:85], v88, off
.LBB0_1088:
	s_or_b64 exec, exec, s[48:49]
	v_pk_mul_f32 v[84:85], v[60:61], v[60:61]
	v_pk_mul_f32 v[86:87], v[72:73], v[72:73]
	v_pk_fma_f32 v[84:85], v[58:59], v[58:59], v[84:85]
	v_cvt_pk_bf16_f32 v58, v58, v59
	v_cvt_pk_bf16_f32 v59, v60, v61
	v_cvt_pk_bf16_f32 v60, v70, v71
	v_cvt_pk_bf16_f32 v61, v72, v73
	ds_bpermute_b32 v232, v244, v58
	ds_bpermute_b32 v233, v244, v59
	ds_bpermute_b32 v234, v244, v60
	ds_bpermute_b32 v235, v244, v61
	ds_bpermute_b32 v236, v244, v82
	ds_bpermute_b32 v237, v244, v83
	v_pk_fma_f32 v[86:87], v[70:71], v[70:71], v[86:87]
	s_nop 0
	v_pk_mul_f32 v[58:59], v[76:77], v[76:77]
	v_pk_mul_f32 v[60:61], v[80:81], v[80:81]
	v_pk_fma_f32 v[58:59], v[74:75], v[74:75], v[58:59]
	v_pk_fma_f32 v[60:61], v[78:79], v[78:79], v[60:61]
	v_pk_add_f32 v[84:85], v[84:85], v[86:87]
	v_pk_add_f32 v[58:59], v[58:59], v[60:61]
	s_nop 0
	v_pk_add_f32 v[60:61], v[84:85], v[58:59]
	v_cvt_pk_bf16_f32 v58, v74, v75
	v_cvt_pk_bf16_f32 v59, v76, v77
	s_nop 0
	v_add_f32_e32 v70, v60, v61
	ds_swizzle_b32 v71, v70 offset:swizzle(SWAP,16)
	v_cvt_pk_bf16_f32 v60, v78, v79
	v_cvt_pk_bf16_f32 v61, v80, v81
	s_waitcnt lgkmcnt(0)
	global_store_dwordx4 v[236:237], v[232:235], off offset:2048
	ds_bpermute_b32 v238, v244, v58
	ds_bpermute_b32 v239, v244, v59
	ds_bpermute_b32 v240, v244, v60
	ds_bpermute_b32 v241, v244, v61
	ds_bpermute_b32 v242, v244, v82
	ds_bpermute_b32 v243, v244, v83
	s_waitcnt lgkmcnt(0)
	s_nop 0
	v_add_f32_e32 v58, v70, v71
	v_mov_b32_e32 v59, v58
	s_nop 1
	v_permlane32_swap_b32_e32 v58, v59
	s_waitcnt lgkmcnt(0)
	global_store_dwordx4 v[242:243], v[238:241], off offset:2112
	s_and_saveexec_b64 s[48:49], s[38:39]
	s_cbranch_execz .LBB0_1090
	v_or_b32_e32 v60, 48, v144
	v_ashrrev_i32_e32 v61, 31, v60
	v_add_f32_e32 v70, v58, v59
	v_lshlrev_b64 v[58:59], 7, v[60:61]
	v_lshl_add_u64 v[58:59], s[8:9], 0, v[58:59]
	v_lshl_add_u64 v[58:59], s[46:47], 2, v[58:59]
	s_lshl_b32 s24, s12, 2
	v_lshl_add_u64 v[58:59], v[58:59], 0, s[24:25]
	global_store_dword v[58:59], v70, off
.LBB0_1090:
	s_or_b64 exec, exec, s[48:49]
	v_pk_mul_f32 v[58:59], v[52:53], v[52:53]
	v_pk_mul_f32 v[60:61], v[64:65], v[64:65]
	v_pk_fma_f32 v[58:59], v[50:51], v[50:51], v[58:59]
	v_pk_fma_f32 v[60:61], v[62:63], v[62:63], v[60:61]
	s_nop 0
	v_pk_add_f32 v[70:71], v[58:59], v[60:61]
	v_cvt_pk_bf16_f32 v58, v50, v51
	v_add_co_u32_e32 v50, vcc, s72, v116
	v_cvt_pk_bf16_f32 v59, v52, v53
	v_cvt_pk_bf16_f32 v60, v62, v63
	v_cvt_pk_bf16_f32 v61, v64, v65
	v_pk_mul_f32 v[52:53], v[56:57], v[56:57]
	s_nop 0
	v_addc_co_u32_e32 v51, vcc, 0, v117, vcc
	ds_bpermute_b32 v232, v244, v58
	ds_bpermute_b32 v233, v244, v59
	ds_bpermute_b32 v234, v244, v60
	ds_bpermute_b32 v235, v244, v61
	ds_bpermute_b32 v236, v244, v50
	ds_bpermute_b32 v237, v244, v51
	v_pk_fma_f32 v[52:53], v[54:55], v[54:55], v[52:53]
	s_nop 0
	v_pk_mul_f32 v[58:59], v[68:69], v[68:69]
	s_nop 0
	v_pk_fma_f32 v[58:59], v[66:67], v[66:67], v[58:59]
	s_nop 0
	v_pk_add_f32 v[52:53], v[52:53], v[58:59]
	s_nop 0
	v_pk_add_f32 v[58:59], v[70:71], v[52:53]
	v_cvt_pk_bf16_f32 v52, v54, v55
	v_cvt_pk_bf16_f32 v53, v56, v57
	v_cvt_pk_bf16_f32 v54, v66, v67
	v_cvt_pk_bf16_f32 v55, v68, v69
	s_waitcnt lgkmcnt(0)
	global_store_dwordx4 v[236:237], v[232:235], off
	ds_bpermute_b32 v238, v244, v52
	ds_bpermute_b32 v239, v244, v53
	ds_bpermute_b32 v240, v244, v54
	ds_bpermute_b32 v241, v244, v55
	ds_bpermute_b32 v242, v244, v50
	ds_bpermute_b32 v243, v244, v51
	v_add_f32_e32 v58, v58, v59
	ds_swizzle_b32 v59, v58 offset:swizzle(SWAP,16)
	s_waitcnt lgkmcnt(0)
	v_add_f32_e32 v52, v58, v59
	v_mov_b32_e32 v53, v52
	s_nop 1
	v_permlane32_swap_b32_e32 v52, v53
	s_waitcnt lgkmcnt(0)
	global_store_dwordx4 v[242:243], v[238:241], off offset:64
	s_and_saveexec_b64 s[48:49], s[38:39]
	s_cbranch_execz .LBB0_1092
	v_ashrrev_i32_e32 v145, 31, v144
	v_add_f32_e32 v54, v52, v53
	v_lshlrev_b64 v[52:53], 7, v[144:145]
	v_lshl_add_u64 v[52:53], s[8:9], 0, v[52:53]
	v_lshl_add_u64 v[52:53], s[46:47], 2, v[52:53]
	s_lshl_b32 s24, s12, 2
	v_lshl_add_u64 v[52:53], v[52:53], 0, s[24:25]
	v_add_co_u32_e32 v52, vcc, 0x4000, v52
	s_nop 1
	v_addc_co_u32_e32 v53, vcc, 0, v53, vcc
	global_store_dword v[52:53], v54, off
.LBB0_1092:
	s_or_b64 exec, exec, s[48:49]
	v_pk_mul_f32 v[52:53], v[36:37], v[36:37]
	v_pk_mul_f32 v[54:55], v[40:41], v[40:41]
	v_pk_fma_f32 v[52:53], v[34:35], v[34:35], v[52:53]
	v_cvt_pk_bf16_f32 v34, v34, v35
	v_cvt_pk_bf16_f32 v35, v36, v37
	v_cvt_pk_bf16_f32 v36, v38, v39
	v_cvt_pk_bf16_f32 v37, v40, v41
	ds_bpermute_b32 v232, v244, v34
	ds_bpermute_b32 v233, v244, v35
	ds_bpermute_b32 v234, v244, v36
	ds_bpermute_b32 v235, v244, v37
	ds_bpermute_b32 v236, v244, v50
	ds_bpermute_b32 v237, v244, v51
	v_pk_fma_f32 v[54:55], v[38:39], v[38:39], v[54:55]
	s_nop 0
	v_pk_mul_f32 v[34:35], v[44:45], v[44:45]
	v_pk_mul_f32 v[36:37], v[48:49], v[48:49]
	v_pk_fma_f32 v[34:35], v[42:43], v[42:43], v[34:35]
	v_pk_fma_f32 v[36:37], v[46:47], v[46:47], v[36:37]
	v_pk_add_f32 v[52:53], v[52:53], v[54:55]
	v_pk_add_f32 v[34:35], v[34:35], v[36:37]
	s_nop 0
	v_pk_add_f32 v[36:37], v[52:53], v[34:35]
	v_cvt_pk_bf16_f32 v34, v42, v43
	v_cvt_pk_bf16_f32 v35, v44, v45
	s_nop 0
	v_add_f32_e32 v38, v36, v37
	ds_swizzle_b32 v39, v38 offset:swizzle(SWAP,16)
	v_cvt_pk_bf16_f32 v36, v46, v47
	v_cvt_pk_bf16_f32 v37, v48, v49
	s_waitcnt lgkmcnt(0)
	global_store_dwordx4 v[236:237], v[232:235], off offset:2048
	ds_bpermute_b32 v238, v244, v34
	ds_bpermute_b32 v239, v244, v35
	ds_bpermute_b32 v240, v244, v36
	ds_bpermute_b32 v241, v244, v37
	ds_bpermute_b32 v242, v244, v50
	ds_bpermute_b32 v243, v244, v51
	s_waitcnt lgkmcnt(0)
	s_nop 0
	v_add_f32_e32 v34, v38, v39
	v_mov_b32_e32 v35, v34
	s_nop 1
	v_permlane32_swap_b32_e32 v34, v35
	s_waitcnt lgkmcnt(0)
	global_store_dwordx4 v[242:243], v[238:241], off offset:2112
	s_and_saveexec_b64 s[48:49], s[38:39]
	s_cbranch_execz .LBB0_1094
	v_ashrrev_i32_e32 v145, 31, v144
	v_add_f32_e32 v36, v34, v35
	v_lshlrev_b64 v[34:35], 7, v[144:145]
	v_lshl_add_u64 v[34:35], s[8:9], 0, v[34:35]
	v_lshl_add_u64 v[34:35], s[46:47], 2, v[34:35]
	s_lshl_b32 s24, s12, 2
	v_lshl_add_u64 v[34:35], v[34:35], 0, s[24:25]
	v_add_co_u32_e32 v34, vcc, 0x4000, v34
	s_nop 1
	v_addc_co_u32_e32 v35, vcc, 0, v35, vcc
	global_store_dword v[34:35], v36, off offset:2048
.LBB0_1094:
	s_or_b64 exec, exec, s[48:49]
	v_pk_mul_f32 v[34:35], v[20:21], v[20:21]
	v_pk_mul_f32 v[36:37], v[28:29], v[28:29]
	v_pk_fma_f32 v[34:35], v[18:19], v[18:19], v[34:35]
	v_pk_fma_f32 v[36:37], v[26:27], v[26:27], v[36:37]
	s_nop 0
	v_pk_add_f32 v[38:39], v[34:35], v[36:37]
	v_cvt_pk_bf16_f32 v35, v20, v21
	v_cvt_pk_bf16_f32 v36, v26, v27
	v_pk_mul_f32 v[20:21], v[24:25], v[24:25]
	v_pk_mul_f32 v[26:27], v[32:33], v[32:33]
	v_pk_fma_f32 v[20:21], v[22:23], v[22:23], v[20:21]
	v_pk_fma_f32 v[26:27], v[30:31], v[30:31], v[26:27]
	v_cvt_pk_bf16_f32 v34, v18, v19
	v_add_co_u32_e32 v18, vcc, s31, v116
	v_pk_add_f32 v[20:21], v[20:21], v[26:27]
	s_nop 0
	v_addc_co_u32_e32 v19, vcc, 0, v117, vcc
	v_pk_add_f32 v[26:27], v[38:39], v[20:21]
	v_cvt_pk_bf16_f32 v20, v22, v23
	v_cvt_pk_bf16_f32 v21, v24, v25
	v_cvt_pk_bf16_f32 v22, v30, v31
	v_cvt_pk_bf16_f32 v23, v32, v33
	ds_bpermute_b32 v232, v244, v20
	ds_bpermute_b32 v233, v244, v21
	ds_bpermute_b32 v234, v244, v22
	ds_bpermute_b32 v235, v244, v23
	ds_bpermute_b32 v236, v244, v18
	ds_bpermute_b32 v237, v244, v19
	v_add_f32_e32 v26, v26, v27
	ds_swizzle_b32 v27, v26 offset:swizzle(SWAP,16)
	v_cvt_pk_bf16_f32 v37, v28, v29
	s_waitcnt lgkmcnt(0)
	global_store_dwordx4 v[236:237], v[232:235], off offset:64
	ds_bpermute_b32 v238, v244, v34
	ds_bpermute_b32 v239, v244, v35
	ds_bpermute_b32 v240, v244, v36
	ds_bpermute_b32 v241, v244, v37
	ds_bpermute_b32 v242, v244, v18
	ds_bpermute_b32 v243, v244, v19
	s_waitcnt lgkmcnt(0)
	v_add_f32_e32 v20, v26, v27
	v_mov_b32_e32 v21, v20
	s_nop 1
	v_permlane32_swap_b32_e32 v20, v21
	s_waitcnt lgkmcnt(0)
	global_store_dwordx4 v[242:243], v[238:241], off
	s_and_saveexec_b64 s[48:49], s[38:39]
	s_cbranch_execz .LBB0_1096
	v_ashrrev_i32_e32 v145, 31, v144
	v_add_f32_e32 v22, v20, v21
	v_lshlrev_b64 v[20:21], 7, v[144:145]
	v_lshl_add_u64 v[20:21], s[8:9], 0, v[20:21]
	v_lshl_add_u64 v[20:21], s[46:47], 2, v[20:21]
	s_lshl_b32 s24, s12, 2
	v_lshl_add_u64 v[20:21], v[20:21], 0, s[24:25]
	v_add_co_u32_e32 v20, vcc, 0x5000, v20
	s_nop 1
	v_addc_co_u32_e32 v21, vcc, 0, v21, vcc
	global_store_dword v[20:21], v22, off
.LBB0_1096:
	s_or_b64 exec, exec, s[48:49]
	v_pk_mul_f32 v[20:21], v[4:5], v[4:5]
	v_pk_mul_f32 v[22:23], v[8:9], v[8:9]
	v_pk_fma_f32 v[20:21], v[2:3], v[2:3], v[20:21]
	v_cvt_pk_bf16_f32 v2, v2, v3
	v_cvt_pk_bf16_f32 v3, v4, v5
	v_cvt_pk_bf16_f32 v4, v6, v7
	v_cvt_pk_bf16_f32 v5, v8, v9
	ds_bpermute_b32 v232, v244, v2
	ds_bpermute_b32 v233, v244, v3
	ds_bpermute_b32 v234, v244, v4
	ds_bpermute_b32 v235, v244, v5
	ds_bpermute_b32 v236, v244, v18
	ds_bpermute_b32 v237, v244, v19
	v_pk_fma_f32 v[22:23], v[6:7], v[6:7], v[22:23]
	s_nop 0
	v_pk_mul_f32 v[2:3], v[12:13], v[12:13]
	v_pk_mul_f32 v[4:5], v[16:17], v[16:17]
	v_pk_fma_f32 v[2:3], v[10:11], v[10:11], v[2:3]
	v_pk_fma_f32 v[4:5], v[14:15], v[14:15], v[4:5]
	v_pk_add_f32 v[20:21], v[20:21], v[22:23]
	v_pk_add_f32 v[2:3], v[2:3], v[4:5]
	s_nop 0
	v_pk_add_f32 v[4:5], v[20:21], v[2:3]
	v_cvt_pk_bf16_f32 v2, v10, v11
	v_cvt_pk_bf16_f32 v3, v12, v13
	s_nop 0
	v_add_f32_e32 v6, v4, v5
	ds_swizzle_b32 v7, v6 offset:swizzle(SWAP,16)
	v_cvt_pk_bf16_f32 v4, v14, v15
	v_cvt_pk_bf16_f32 v5, v16, v17
	s_waitcnt lgkmcnt(0)
	global_store_dwordx4 v[236:237], v[232:235], off offset:2048
	ds_bpermute_b32 v238, v244, v2
	ds_bpermute_b32 v239, v244, v3
	ds_bpermute_b32 v240, v244, v4
	ds_bpermute_b32 v241, v244, v5
	ds_bpermute_b32 v242, v244, v18
	ds_bpermute_b32 v243, v244, v19
	s_waitcnt lgkmcnt(0)
	s_nop 0
	v_add_f32_e32 v2, v6, v7
	v_mov_b32_e32 v3, v2
	s_nop 1
	v_permlane32_swap_b32_e32 v2, v3
	s_waitcnt lgkmcnt(0)
	global_store_dwordx4 v[242:243], v[238:241], off offset:2112
	s_and_saveexec_b64 s[48:49], s[38:39]
	s_cbranch_execz .LBB0_1098
	v_ashrrev_i32_e32 v145, 31, v144
	v_add_f32_e32 v4, v2, v3
	v_lshlrev_b64 v[2:3], 7, v[144:145]
	v_lshl_add_u64 v[2:3], s[8:9], 0, v[2:3]
	v_lshl_add_u64 v[2:3], s[46:47], 2, v[2:3]
	s_lshl_b32 s24, s12, 2
	v_lshl_add_u64 v[2:3], v[2:3], 0, s[24:25]
	v_add_co_u32_e32 v2, vcc, 0x5000, v2
	s_nop 1
	v_addc_co_u32_e32 v3, vcc, 0, v3, vcc
	global_store_dword v[2:3], v4, off offset:2048

.LBB0_1233:
	v_mbcnt_lo_u32_b32 v244, -1, 0
	v_mbcnt_hi_u32_b32 v244, -1, v244
	v_lshrrev_b32_e32 v245, 2, v244
	v_and_b32_e32 v244, 3, v244
	v_lshl_add_u32 v244, v244, 4, v245
	v_lshlrev_b32_e32 v244, 2, v244
	v_lshl_add_u32 v148, s59, 10, v146
	ds_read2_b32 v[150:151], v148 offset1:16
	s_lshl_b32 s17, s58, 2
	v_med3_f32 v124, v124, 0, v193
	v_med3_f32 v125, v125, 0, v193
	s_lshl_b32 s16, s44, 7
	s_or_b32 s17, s17, s45
	s_waitcnt lgkmcnt(0)
	v_mul_f32_e32 v150, v150, v150
	v_pk_mul_f32 v[124:125], v[124:125], v[124:125]
	s_add_i32 s16, s17, s16
	v_pk_mul_f32 v[152:153], v[124:125], v[150:151] op_sel_hi:[1,0]
	v_med3_f32 v124, v130, 0, v193
	v_med3_f32 v125, v131, 0, v193
	s_ashr_i32 s17, s16, 31
	v_med3_f32 v128, v128, 0, v193
	v_med3_f32 v129, v129, 0, v193
	v_med3_f32 v126, v126, 0, v193
	v_med3_f32 v127, v127, 0, v193
	v_pk_mul_f32 v[124:125], v[124:125], v[124:125]
	s_lshl_b64 s[16:17], s[16:17], 15
	v_pk_mul_f32 v[128:129], v[128:129], v[128:129]
	v_pk_mul_f32 v[130:131], v[124:125], v[150:151] op_sel_hi:[1,0]
	v_pk_mul_f32 v[124:125], v[126:127], v[126:127]
	v_med3_f32 v116, v116, 0, v193
	v_med3_f32 v117, v117, 0, v193
	v_lshl_add_u64 v[144:145], v[138:139], 0, s[16:17]
	v_pk_mul_f32 v[128:129], v[128:129], v[150:151] op_sel_hi:[1,0]
	v_pk_mul_f32 v[154:155], v[124:125], v[150:151] op_sel_hi:[1,0]
	v_cvt_pk_bf16_f32 v124, v128, v129
	v_cvt_pk_bf16_f32 v125, v130, v131
	v_pk_mul_f32 v[116:117], v[116:117], v[116:117]
	v_cvt_pk_bf16_f32 v126, v152, v153
	v_cvt_pk_bf16_f32 v127, v154, v155
	ds_bpermute_b32 v232, v244, v124
	ds_bpermute_b32 v233, v244, v125
	ds_bpermute_b32 v234, v244, v126
	ds_bpermute_b32 v235, v244, v127
	ds_bpermute_b32 v236, v244, v144
	ds_bpermute_b32 v237, v244, v145
	v_med3_f32 v120, v120, 0, v193
	v_med3_f32 v121, v121, 0, v193
	v_pk_mul_f32 v[124:125], v[116:117], v[150:151] op_sel_hi:[1,0]
	v_med3_f32 v116, v122, 0, v193
	v_med3_f32 v117, v123, 0, v193
	v_med3_f32 v118, v118, 0, v193
	v_med3_f32 v119, v119, 0, v193
	v_pk_mul_f32 v[116:117], v[116:117], v[116:117]
	v_pk_mul_f32 v[120:121], v[120:121], v[120:121]
	v_pk_mul_f32 v[122:123], v[116:117], v[150:151] op_sel_hi:[1,0]
	v_pk_mul_f32 v[116:117], v[118:119], v[118:119]
	v_pk_mul_f32 v[120:121], v[120:121], v[150:151] op_sel_hi:[1,0]
	v_pk_mul_f32 v[126:127], v[116:117], v[150:151] op_sel_hi:[1,0]
	v_cvt_pk_bf16_f32 v116, v120, v121
	v_med3_f32 v106, v106, 0, v193
	v_med3_f32 v107, v107, 0, v193
	v_cvt_pk_bf16_f32 v117, v122, v123
	v_cvt_pk_bf16_f32 v118, v124, v125
	v_cvt_pk_bf16_f32 v119, v126, v127
	s_waitcnt lgkmcnt(0)
	global_store_dwordx4 v[236:237], v[232:235], off
	ds_bpermute_b32 v238, v244, v116
	ds_bpermute_b32 v239, v244, v117
	ds_bpermute_b32 v240, v244, v118
	ds_bpermute_b32 v241, v244, v119
	ds_bpermute_b32 v242, v244, v144
	ds_bpermute_b32 v243, v244, v145
	v_pk_mul_f32 v[106:107], v[106:107], v[106:107]
	v_med3_f32 v110, v110, 0, v193
	v_mul_f32_e32 v116, v151, v151
	v_pk_mul_f32 v[118:119], v[106:107], v[116:117] op_sel_hi:[1,0]
	v_med3_f32 v106, v112, 0, v193
	v_med3_f32 v107, v113, 0, v193
	v_med3_f32 v111, v111, 0, v193
	v_med3_f32 v108, v108, 0, v193
	v_med3_f32 v109, v109, 0, v193
	v_pk_mul_f32 v[106:107], v[106:107], v[106:107]
	v_pk_mul_f32 v[110:111], v[110:111], v[110:111]
	v_pk_mul_f32 v[112:113], v[106:107], v[116:117] op_sel_hi:[1,0]
	v_pk_mul_f32 v[106:107], v[108:109], v[108:109]
	v_med3_f32 v98, v98, 0, v193
	v_med3_f32 v99, v99, 0, v193
	v_pk_mul_f32 v[110:111], v[110:111], v[116:117] op_sel_hi:[1,0]
	v_pk_mul_f32 v[120:121], v[106:107], v[116:117] op_sel_hi:[1,0]
	v_cvt_pk_bf16_f32 v106, v110, v111
	v_cvt_pk_bf16_f32 v107, v112, v113
	v_pk_mul_f32 v[98:99], v[98:99], v[98:99]
	v_cvt_pk_bf16_f32 v108, v118, v119
	v_cvt_pk_bf16_f32 v109, v120, v121
	s_waitcnt lgkmcnt(0)
	global_store_dwordx4 v[242:243], v[238:241], off offset:64
	ds_bpermute_b32 v232, v244, v106
	ds_bpermute_b32 v233, v244, v107
	ds_bpermute_b32 v234, v244, v108
	ds_bpermute_b32 v235, v244, v109
	ds_bpermute_b32 v236, v244, v144
	ds_bpermute_b32 v237, v244, v145
	v_med3_f32 v102, v102, 0, v193
	v_med3_f32 v103, v103, 0, v193
	v_pk_mul_f32 v[106:107], v[98:99], v[116:117] op_sel_hi:[1,0]
	v_med3_f32 v98, v104, 0, v193
	v_med3_f32 v99, v105, 0, v193
	v_pk_mul_f32 v[102:103], v[102:103], v[102:103]
	v_med3_f32 v100, v100, 0, v193
	v_med3_f32 v101, v101, 0, v193
	v_pk_mul_f32 v[98:99], v[98:99], v[98:99]
	v_pk_mul_f32 v[102:103], v[102:103], v[116:117] op_sel_hi:[1,0]
	v_pk_mul_f32 v[104:105], v[98:99], v[116:117] op_sel_hi:[1,0]
	v_pk_mul_f32 v[98:99], v[100:101], v[100:101]
	v_med3_f32 v90, v90, 0, v193
	v_pk_mul_f32 v[108:109], v[98:99], v[116:117] op_sel_hi:[1,0]
	v_cvt_pk_bf16_f32 v98, v102, v103
	ds_read2_b32 v[102:103], v148 offset0:32 offset1:48
	v_med3_f32 v91, v91, 0, v193
	v_cvt_pk_bf16_f32 v99, v104, v105
	v_cvt_pk_bf16_f32 v100, v106, v107
	v_cvt_pk_bf16_f32 v101, v108, v109
	s_waitcnt lgkmcnt(0)
	global_store_dwordx4 v[236:237], v[232:235], off offset:2048
	ds_bpermute_b32 v238, v244, v98
	ds_bpermute_b32 v239, v244, v99
	ds_bpermute_b32 v240, v244, v100
	ds_bpermute_b32 v241, v244, v101
	ds_bpermute_b32 v242, v244, v144
	ds_bpermute_b32 v243, v244, v145
	v_pk_mul_f32 v[90:91], v[90:91], v[90:91]
	v_med3_f32 v94, v94, 0, v193
	s_waitcnt lgkmcnt(0)
	v_mul_f32_e32 v98, v102, v102
	v_med3_f32 v95, v95, 0, v193
	v_pk_mul_f32 v[100:101], v[90:91], v[98:99] op_sel_hi:[1,0]
	v_med3_f32 v90, v96, 0, v193
	v_med3_f32 v91, v97, 0, v193
	v_pk_mul_f32 v[94:95], v[94:95], v[94:95]
	v_med3_f32 v92, v92, 0, v193
	v_med3_f32 v93, v93, 0, v193
	v_pk_mul_f32 v[90:91], v[90:91], v[90:91]
	v_pk_mul_f32 v[94:95], v[94:95], v[98:99] op_sel_hi:[1,0]
	v_pk_mul_f32 v[96:97], v[90:91], v[98:99] op_sel_hi:[1,0]
	v_pk_mul_f32 v[90:91], v[92:93], v[92:93]
	v_med3_f32 v82, v82, 0, v193
	v_pk_mul_f32 v[104:105], v[90:91], v[98:99] op_sel_hi:[1,0]
	v_cvt_pk_bf16_f32 v90, v94, v95
	v_add_co_u32_e32 v94, vcc, s73, v144
	v_med3_f32 v83, v83, 0, v193
	v_cvt_pk_bf16_f32 v91, v96, v97
	s_nop 0
	v_addc_co_u32_e32 v95, vcc, 0, v145, vcc
	v_pk_mul_f32 v[82:83], v[82:83], v[82:83]
	v_cvt_pk_bf16_f32 v92, v100, v101
	v_cvt_pk_bf16_f32 v93, v104, v105
	s_waitcnt lgkmcnt(0)
	global_store_dwordx4 v[242:243], v[238:241], off offset:2112
	ds_bpermute_b32 v232, v244, v90
	ds_bpermute_b32 v233, v244, v91
	ds_bpermute_b32 v234, v244, v92
	ds_bpermute_b32 v235, v244, v93
	ds_bpermute_b32 v236, v244, v94
	ds_bpermute_b32 v237, v244, v95
	v_med3_f32 v86, v86, 0, v193
	v_med3_f32 v87, v87, 0, v193
	v_pk_mul_f32 v[90:91], v[82:83], v[98:99] op_sel_hi:[1,0]
	v_med3_f32 v82, v88, 0, v193
	v_med3_f32 v83, v89, 0, v193
	v_med3_f32 v84, v84, 0, v193
	v_med3_f32 v85, v85, 0, v193
	v_pk_mul_f32 v[82:83], v[82:83], v[82:83]
	v_pk_mul_f32 v[86:87], v[86:87], v[86:87]
	v_pk_mul_f32 v[88:89], v[82:83], v[98:99] op_sel_hi:[1,0]
	v_pk_mul_f32 v[82:83], v[84:85], v[84:85]
	v_pk_mul_f32 v[86:87], v[86:87], v[98:99] op_sel_hi:[1,0]
	v_pk_mul_f32 v[92:93], v[82:83], v[98:99] op_sel_hi:[1,0]
	v_cvt_pk_bf16_f32 v82, v86, v87
	v_med3_f32 v74, v74, 0, v193
	v_med3_f32 v75, v75, 0, v193
	v_cvt_pk_bf16_f32 v83, v88, v89
	v_cvt_pk_bf16_f32 v84, v90, v91
	v_cvt_pk_bf16_f32 v85, v92, v93
	s_waitcnt lgkmcnt(0)
	global_store_dwordx4 v[236:237], v[232:235], off
	ds_bpermute_b32 v238, v244, v82
	ds_bpermute_b32 v239, v244, v83
	ds_bpermute_b32 v240, v244, v84
	ds_bpermute_b32 v241, v244, v85
	ds_bpermute_b32 v242, v244, v94
	ds_bpermute_b32 v243, v244, v95
	v_pk_mul_f32 v[74:75], v[74:75], v[74:75]
	v_med3_f32 v78, v78, 0, v193
	v_mul_f32_e32 v82, v103, v103
	v_pk_mul_f32 v[84:85], v[74:75], v[82:83] op_sel_hi:[1,0]
	v_med3_f32 v74, v80, 0, v193
	v_med3_f32 v75, v81, 0, v193
	v_med3_f32 v79, v79, 0, v193
	v_med3_f32 v76, v76, 0, v193
	v_med3_f32 v77, v77, 0, v193
	v_pk_mul_f32 v[74:75], v[74:75], v[74:75]
	v_pk_mul_f32 v[78:79], v[78:79], v[78:79]
	v_pk_mul_f32 v[80:81], v[74:75], v[82:83] op_sel_hi:[1,0]
	v_pk_mul_f32 v[74:75], v[76:77], v[76:77]
	v_med3_f32 v66, v66, 0, v193
	v_med3_f32 v67, v67, 0, v193
	v_pk_mul_f32 v[78:79], v[78:79], v[82:83] op_sel_hi:[1,0]
	v_pk_mul_f32 v[86:87], v[74:75], v[82:83] op_sel_hi:[1,0]
	v_cvt_pk_bf16_f32 v74, v78, v79
	v_cvt_pk_bf16_f32 v75, v80, v81
	v_pk_mul_f32 v[66:67], v[66:67], v[66:67]
	v_cvt_pk_bf16_f32 v76, v84, v85
	v_cvt_pk_bf16_f32 v77, v86, v87
	s_waitcnt lgkmcnt(0)
	global_store_dwordx4 v[242:243], v[238:241], off offset:64
	ds_bpermute_b32 v232, v244, v74
	ds_bpermute_b32 v233, v244, v75
	ds_bpermute_b32 v234, v244, v76
	ds_bpermute_b32 v235, v244, v77
	ds_bpermute_b32 v236, v244, v94
	ds_bpermute_b32 v237, v244, v95
	v_med3_f32 v70, v70, 0, v193
	v_med3_f32 v71, v71, 0, v193
	v_pk_mul_f32 v[74:75], v[66:67], v[82:83] op_sel_hi:[1,0]
	v_med3_f32 v66, v72, 0, v193
	v_med3_f32 v67, v73, 0, v193
	v_pk_mul_f32 v[70:71], v[70:71], v[70:71]
	v_med3_f32 v68, v68, 0, v193
	v_med3_f32 v69, v69, 0, v193
	v_pk_mul_f32 v[66:67], v[66:67], v[66:67]
	v_pk_mul_f32 v[70:71], v[70:71], v[82:83] op_sel_hi:[1,0]
	v_pk_mul_f32 v[72:73], v[66:67], v[82:83] op_sel_hi:[1,0]
	v_pk_mul_f32 v[66:67], v[68:69], v[68:69]
	v_med3_f32 v64, v64, 0, v193
	v_pk_mul_f32 v[76:77], v[66:67], v[82:83] op_sel_hi:[1,0]
	v_cvt_pk_bf16_f32 v66, v70, v71
	ds_read2_b32 v[70:71], v148 offset0:128 offset1:144
	v_med3_f32 v65, v65, 0, v193
	v_cvt_pk_bf16_f32 v67, v72, v73
	v_cvt_pk_bf16_f32 v68, v74, v75
	v_cvt_pk_bf16_f32 v69, v76, v77
	s_waitcnt lgkmcnt(0)
	global_store_dwordx4 v[236:237], v[232:235], off offset:2048
	ds_bpermute_b32 v238, v244, v66
	ds_bpermute_b32 v239, v244, v67
	ds_bpermute_b32 v240, v244, v68
	ds_bpermute_b32 v241, v244, v69
	ds_bpermute_b32 v242, v244, v94
	ds_bpermute_b32 v243, v244, v95
	v_med3_f32 v60, v60, 0, v193
	v_med3_f32 v61, v61, 0, v193
	s_waitcnt lgkmcnt(0)
	v_mul_f32_e32 v66, v70, v70
	v_pk_mul_f32 v[64:65], v[64:65], v[64:65]
	v_med3_f32 v62, v62, 0, v193
	v_med3_f32 v63, v63, 0, v193
	v_med3_f32 v58, v58, 0, v193
	v_med3_f32 v59, v59, 0, v193
	v_pk_mul_f32 v[64:65], v[64:65], v[66:67] op_sel_hi:[1,0]
	v_pk_mul_f32 v[60:61], v[60:61], v[60:61]
	v_pk_mul_f32 v[62:63], v[62:63], v[62:63]
	v_pk_mul_f32 v[58:59], v[58:59], v[58:59]
	v_pk_mul_f32 v[68:69], v[60:61], v[66:67] op_sel_hi:[1,0]
	v_cvt_pk_bf16_f32 v61, v64, v65
	v_add_co_u32_e32 v64, vcc, s72, v144
	v_pk_mul_f32 v[62:63], v[62:63], v[66:67] op_sel_hi:[1,0]
	v_pk_mul_f32 v[58:59], v[58:59], v[66:67] op_sel_hi:[1,0]
	v_addc_co_u32_e32 v65, vcc, 0, v145, vcc
	v_cvt_pk_bf16_f32 v60, v62, v63
	v_cvt_pk_bf16_f32 v62, v58, v59
	v_add_co_u32_e32 v58, vcc, s31, v144
	v_med3_f32 v50, v50, 0, v193
	v_med3_f32 v51, v51, 0, v193
	v_addc_co_u32_e32 v59, vcc, 0, v145, vcc
	v_pk_mul_f32 v[50:51], v[50:51], v[50:51]
	v_cvt_pk_bf16_f32 v63, v68, v69
	s_waitcnt lgkmcnt(0)
	global_store_dwordx4 v[242:243], v[238:241], off offset:2112
	ds_bpermute_b32 v232, v244, v60
	ds_bpermute_b32 v233, v244, v61
	ds_bpermute_b32 v234, v244, v62
	ds_bpermute_b32 v235, v244, v63
	ds_bpermute_b32 v236, v244, v58
	ds_bpermute_b32 v237, v244, v59
	v_med3_f32 v54, v54, 0, v193
	v_med3_f32 v55, v55, 0, v193
	v_pk_mul_f32 v[60:61], v[50:51], v[66:67] op_sel_hi:[1,0]
	v_med3_f32 v50, v56, 0, v193
	v_med3_f32 v51, v57, 0, v193
	v_med3_f32 v52, v52, 0, v193
	v_med3_f32 v53, v53, 0, v193
	v_pk_mul_f32 v[50:51], v[50:51], v[50:51]
	v_pk_mul_f32 v[54:55], v[54:55], v[54:55]
	v_pk_mul_f32 v[56:57], v[50:51], v[66:67] op_sel_hi:[1,0]
	v_pk_mul_f32 v[50:51], v[52:53], v[52:53]
	v_pk_mul_f32 v[54:55], v[54:55], v[66:67] op_sel_hi:[1,0]
	v_pk_mul_f32 v[62:63], v[50:51], v[66:67] op_sel_hi:[1,0]
	v_cvt_pk_bf16_f32 v50, v54, v55
	v_med3_f32 v42, v42, 0, v193
	v_med3_f32 v43, v43, 0, v193
	v_cvt_pk_bf16_f32 v51, v56, v57
	v_cvt_pk_bf16_f32 v52, v60, v61
	v_cvt_pk_bf16_f32 v53, v62, v63
	s_waitcnt lgkmcnt(0)
	global_store_dwordx4 v[236:237], v[232:235], off offset:-4096
	ds_bpermute_b32 v238, v244, v50
	ds_bpermute_b32 v239, v244, v51
	ds_bpermute_b32 v240, v244, v52
	ds_bpermute_b32 v241, v244, v53
	ds_bpermute_b32 v242, v244, v64
	ds_bpermute_b32 v243, v244, v65
	v_pk_mul_f32 v[42:43], v[42:43], v[42:43]
	v_med3_f32 v46, v46, 0, v193
	v_mul_f32_e32 v50, v71, v71
	v_pk_mul_f32 v[52:53], v[42:43], v[50:51] op_sel_hi:[1,0]
	v_med3_f32 v42, v48, 0, v193
	v_med3_f32 v43, v49, 0, v193
	v_med3_f32 v47, v47, 0, v193
	v_med3_f32 v44, v44, 0, v193
	v_med3_f32 v45, v45, 0, v193
	v_pk_mul_f32 v[42:43], v[42:43], v[42:43]
	v_pk_mul_f32 v[46:47], v[46:47], v[46:47]
	v_pk_mul_f32 v[48:49], v[42:43], v[50:51] op_sel_hi:[1,0]
	v_pk_mul_f32 v[42:43], v[44:45], v[44:45]
	v_med3_f32 v34, v34, 0, v193
	v_med3_f32 v35, v35, 0, v193
	v_pk_mul_f32 v[46:47], v[46:47], v[50:51] op_sel_hi:[1,0]
	v_pk_mul_f32 v[54:55], v[42:43], v[50:51] op_sel_hi:[1,0]
	v_cvt_pk_bf16_f32 v42, v46, v47
	v_cvt_pk_bf16_f32 v43, v48, v49
	v_pk_mul_f32 v[34:35], v[34:35], v[34:35]
	v_cvt_pk_bf16_f32 v44, v52, v53
	v_cvt_pk_bf16_f32 v45, v54, v55
	s_waitcnt lgkmcnt(0)
	global_store_dwordx4 v[242:243], v[238:241], off offset:64
	ds_bpermute_b32 v232, v244, v42
	ds_bpermute_b32 v233, v244, v43
	ds_bpermute_b32 v234, v244, v44
	ds_bpermute_b32 v235, v244, v45
	ds_bpermute_b32 v236, v244, v64
	ds_bpermute_b32 v237, v244, v65
	v_med3_f32 v38, v38, 0, v193
	v_med3_f32 v39, v39, 0, v193
	v_pk_mul_f32 v[42:43], v[34:35], v[50:51] op_sel_hi:[1,0]
	v_med3_f32 v34, v40, 0, v193
	v_med3_f32 v35, v41, 0, v193
	v_pk_mul_f32 v[38:39], v[38:39], v[38:39]
	v_med3_f32 v36, v36, 0, v193
	v_med3_f32 v37, v37, 0, v193
	v_pk_mul_f32 v[34:35], v[34:35], v[34:35]
	v_pk_mul_f32 v[38:39], v[38:39], v[50:51] op_sel_hi:[1,0]
	v_pk_mul_f32 v[40:41], v[34:35], v[50:51] op_sel_hi:[1,0]
	v_pk_mul_f32 v[34:35], v[36:37], v[36:37]
	v_med3_f32 v26, v26, 0, v193
	v_pk_mul_f32 v[44:45], v[34:35], v[50:51] op_sel_hi:[1,0]
	v_cvt_pk_bf16_f32 v34, v38, v39
	ds_read2_b32 v[38:39], v148 offset0:160 offset1:176
	v_med3_f32 v27, v27, 0, v193
	v_cvt_pk_bf16_f32 v35, v40, v41
	v_cvt_pk_bf16_f32 v36, v42, v43
	v_cvt_pk_bf16_f32 v37, v44, v45
	s_waitcnt lgkmcnt(0)
	global_store_dwordx4 v[236:237], v[232:235], off offset:2048
	ds_bpermute_b32 v238, v244, v34
	ds_bpermute_b32 v239, v244, v35
	ds_bpermute_b32 v240, v244, v36
	ds_bpermute_b32 v241, v244, v37
	ds_bpermute_b32 v242, v244, v64
	ds_bpermute_b32 v243, v244, v65
	v_pk_mul_f32 v[26:27], v[26:27], v[26:27]
	v_med3_f32 v30, v30, 0, v193
	s_waitcnt lgkmcnt(0)
	v_mul_f32_e32 v34, v38, v38
	v_pk_mul_f32 v[36:37], v[26:27], v[34:35] op_sel_hi:[1,0]
	v_med3_f32 v26, v32, 0, v193
	v_med3_f32 v27, v33, 0, v193
	v_med3_f32 v31, v31, 0, v193
	v_med3_f32 v28, v28, 0, v193
	v_med3_f32 v29, v29, 0, v193
	v_pk_mul_f32 v[26:27], v[26:27], v[26:27]
	v_pk_mul_f32 v[30:31], v[30:31], v[30:31]
	v_pk_mul_f32 v[32:33], v[26:27], v[34:35] op_sel_hi:[1,0]
	v_pk_mul_f32 v[26:27], v[28:29], v[28:29]
	v_med3_f32 v18, v18, 0, v193
	v_med3_f32 v19, v19, 0, v193
	v_pk_mul_f32 v[30:31], v[30:31], v[34:35] op_sel_hi:[1,0]
	v_pk_mul_f32 v[40:41], v[26:27], v[34:35] op_sel_hi:[1,0]
	v_cvt_pk_bf16_f32 v26, v30, v31
	v_cvt_pk_bf16_f32 v27, v32, v33
	v_pk_mul_f32 v[18:19], v[18:19], v[18:19]
	v_cvt_pk_bf16_f32 v28, v36, v37
	v_cvt_pk_bf16_f32 v29, v40, v41
	s_waitcnt lgkmcnt(0)
	global_store_dwordx4 v[242:243], v[238:241], off offset:2112
	ds_bpermute_b32 v232, v244, v26
	ds_bpermute_b32 v233, v244, v27
	ds_bpermute_b32 v234, v244, v28
	ds_bpermute_b32 v235, v244, v29
	ds_bpermute_b32 v236, v244, v58
	ds_bpermute_b32 v237, v244, v59
	v_med3_f32 v22, v22, 0, v193
	v_med3_f32 v23, v23, 0, v193
	v_pk_mul_f32 v[26:27], v[18:19], v[34:35] op_sel_hi:[1,0]
	v_med3_f32 v18, v24, 0, v193
	v_med3_f32 v19, v25, 0, v193
	v_med3_f32 v20, v20, 0, v193
	v_med3_f32 v21, v21, 0, v193
	v_pk_mul_f32 v[18:19], v[18:19], v[18:19]
	v_pk_mul_f32 v[22:23], v[22:23], v[22:23]
	v_pk_mul_f32 v[24:25], v[18:19], v[34:35] op_sel_hi:[1,0]
	v_pk_mul_f32 v[18:19], v[20:21], v[20:21]
	v_pk_mul_f32 v[22:23], v[22:23], v[34:35] op_sel_hi:[1,0]
	v_pk_mul_f32 v[28:29], v[18:19], v[34:35] op_sel_hi:[1,0]
	v_cvt_pk_bf16_f32 v18, v22, v23
	v_med3_f32 v10, v10, 0, v193
	v_med3_f32 v11, v11, 0, v193
	v_cvt_pk_bf16_f32 v19, v24, v25
	v_cvt_pk_bf16_f32 v20, v26, v27
	v_cvt_pk_bf16_f32 v21, v28, v29
	s_waitcnt lgkmcnt(0)
	global_store_dwordx4 v[236:237], v[232:235], off
	ds_bpermute_b32 v238, v244, v18
	ds_bpermute_b32 v239, v244, v19
	ds_bpermute_b32 v240, v244, v20
	ds_bpermute_b32 v241, v244, v21
	ds_bpermute_b32 v242, v244, v58
	ds_bpermute_b32 v243, v244, v59
	v_pk_mul_f32 v[10:11], v[10:11], v[10:11]
	v_med3_f32 v14, v14, 0, v193
	v_mul_f32_e32 v18, v39, v39
	v_pk_mul_f32 v[20:21], v[10:11], v[18:19] op_sel_hi:[1,0]
	v_med3_f32 v10, v16, 0, v193
	v_med3_f32 v11, v17, 0, v193
	v_med3_f32 v15, v15, 0, v193
	v_med3_f32 v12, v12, 0, v193
	v_med3_f32 v13, v13, 0, v193
	v_pk_mul_f32 v[10:11], v[10:11], v[10:11]
	v_pk_mul_f32 v[14:15], v[14:15], v[14:15]
	v_pk_mul_f32 v[16:17], v[10:11], v[18:19] op_sel_hi:[1,0]
	v_pk_mul_f32 v[10:11], v[12:13], v[12:13]
	v_med3_f32 v2, v2, 0, v193
	v_med3_f32 v3, v3, 0, v193
	v_pk_mul_f32 v[14:15], v[14:15], v[18:19] op_sel_hi:[1,0]
	v_pk_mul_f32 v[22:23], v[10:11], v[18:19] op_sel_hi:[1,0]
	v_cvt_pk_bf16_f32 v10, v14, v15
	v_cvt_pk_bf16_f32 v11, v16, v17
	v_pk_mul_f32 v[2:3], v[2:3], v[2:3]
	v_cvt_pk_bf16_f32 v12, v20, v21
	v_cvt_pk_bf16_f32 v13, v22, v23
	s_waitcnt lgkmcnt(0)
	global_store_dwordx4 v[242:243], v[238:241], off offset:64
	ds_bpermute_b32 v232, v244, v10
	ds_bpermute_b32 v233, v244, v11
	ds_bpermute_b32 v234, v244, v12
	ds_bpermute_b32 v235, v244, v13
	ds_bpermute_b32 v236, v244, v58
	ds_bpermute_b32 v237, v244, v59
	v_med3_f32 v6, v6, 0, v193
	v_med3_f32 v7, v7, 0, v193
	v_pk_mul_f32 v[10:11], v[2:3], v[18:19] op_sel_hi:[1,0]
	v_med3_f32 v2, v8, 0, v193
	v_med3_f32 v3, v9, 0, v193
	v_med3_f32 v4, v4, 0, v193
	v_med3_f32 v5, v5, 0, v193
	v_pk_mul_f32 v[2:3], v[2:3], v[2:3]
	v_pk_mul_f32 v[6:7], v[6:7], v[6:7]
	v_pk_mul_f32 v[8:9], v[2:3], v[18:19] op_sel_hi:[1,0]
	v_pk_mul_f32 v[2:3], v[4:5], v[4:5]
	s_andn2_b64 vcc, exec, s[38:39]
	s_mov_b64 s[38:39], -1
	v_pk_mul_f32 v[6:7], v[6:7], v[18:19] op_sel_hi:[1,0]
	v_pk_mul_f32 v[12:13], v[2:3], v[18:19] op_sel_hi:[1,0]
	v_cvt_pk_bf16_f32 v2, v6, v7
	v_cvt_pk_bf16_f32 v3, v8, v9
	v_cvt_pk_bf16_f32 v4, v10, v11
	s_nop 0
	v_cvt_pk_bf16_f32 v5, v12, v13
	s_waitcnt lgkmcnt(0)
	global_store_dwordx4 v[236:237], v[232:235], off offset:2048
	ds_bpermute_b32 v238, v244, v2
	ds_bpermute_b32 v239, v244, v3
	ds_bpermute_b32 v240, v244, v4
	ds_bpermute_b32 v241, v244, v5
	ds_bpermute_b32 v242, v244, v58
	ds_bpermute_b32 v243, v244, v59
	s_waitcnt lgkmcnt(0)
	global_store_dwordx4 v[242:243], v[238:241], off offset:2112
	s_cbranch_vccnz .LBB0_1222
	s_andn2_b64 vcc, exec, s[0:1]
	s_cbranch_vccnz .LBB0_1221
	s_barrier
	s_branch .LBB0_1221

.LBB0_1337:
	v_mbcnt_lo_u32_b32 v244, -1, 0
	v_mbcnt_hi_u32_b32 v244, -1, v244
	v_lshrrev_b32_e32 v245, 2, v244
	v_and_b32_e32 v244, 3, v244
	v_lshl_add_u32 v244, v244, 4, v245
	v_lshlrev_b32_e32 v244, 2, v244
	v_pk_mul_f32 v[148:149], v[118:119], v[118:119]
	v_pk_mul_f32 v[150:151], v[126:127], v[126:127]
	v_pk_fma_f32 v[148:149], v[116:117], v[116:117], v[148:149]
	v_pk_fma_f32 v[150:151], v[124:125], v[124:125], v[150:151]
	v_lshl_add_u32 v144, s46, 8, v1
	v_pk_add_f32 v[152:153], v[148:149], v[150:151]
	v_cvt_pk_bf16_f32 v149, v118, v119
	v_cvt_pk_bf16_f32 v150, v124, v125
	v_pk_mul_f32 v[118:119], v[122:123], v[122:123]
	v_pk_mul_f32 v[124:125], v[130:131], v[130:131]
	v_pk_fma_f32 v[118:119], v[120:121], v[120:121], v[118:119]
	v_pk_fma_f32 v[124:125], v[128:129], v[128:129], v[124:125]
	s_lshl_b32 s16, s46, 5
	v_pk_add_f32 v[118:119], v[118:119], v[124:125]
	s_lshl_b32 s46, s48, 2
	v_pk_add_f32 v[124:125], v[152:153], v[118:119]
	s_or_b32 s17, s46, s14
	v_add_f32_e32 v124, v124, v125
	ds_swizzle_b32 v125, v124 offset:swizzle(SWAP,16)
	s_add_i32 s16, s17, s16
	s_ashr_i32 s17, s16, 31
	s_lshl_b64 s[16:17], s[16:17], 15
	v_cvt_pk_bf16_f32 v148, v116, v117
	v_lshl_add_u64 v[116:117], v[138:139], 0, s[16:17]
	v_cvt_pk_bf16_f32 v118, v120, v121
	v_cvt_pk_bf16_f32 v119, v122, v123
	v_cvt_pk_bf16_f32 v120, v128, v129
	v_cvt_pk_bf16_f32 v121, v130, v131
	ds_bpermute_b32 v232, v244, v118
	ds_bpermute_b32 v233, v244, v119
	ds_bpermute_b32 v234, v244, v120
	ds_bpermute_b32 v235, v244, v121
	ds_bpermute_b32 v236, v244, v116
	ds_bpermute_b32 v237, v244, v117
	s_ashr_i32 s47, s46, 31
	v_cvt_pk_bf16_f32 v151, v126, v127
	s_waitcnt lgkmcnt(0)
	global_store_dwordx4 v[236:237], v[232:235], off offset:64
	ds_bpermute_b32 v238, v244, v148
	ds_bpermute_b32 v239, v244, v149
	ds_bpermute_b32 v240, v244, v150
	ds_bpermute_b32 v241, v244, v151
	ds_bpermute_b32 v242, v244, v116
	ds_bpermute_b32 v243, v244, v117
	s_waitcnt lgkmcnt(0)
	v_add_f32_e32 v118, v124, v125
	v_mov_b32_e32 v119, v118
	s_nop 1
	v_permlane32_swap_b32_e32 v118, v119
	s_waitcnt lgkmcnt(0)
	global_store_dwordx4 v[242:243], v[238:241], off
	s_and_saveexec_b64 s[48:49], s[38:39]
	s_cbranch_execz .LBB0_1339
	v_ashrrev_i32_e32 v145, 31, v144
	v_add_f32_e32 v120, v118, v119
	v_lshlrev_b64 v[118:119], 7, v[144:145]
	v_lshl_add_u64 v[118:119], s[8:9], 0, v[118:119]
	v_lshl_add_u64 v[118:119], s[46:47], 2, v[118:119]
	s_lshl_b32 s24, s14, 2
	v_lshl_add_u64 v[118:119], v[118:119], 0, s[24:25]
	global_store_dword v[118:119], v120, off
.LBB0_1339:
	s_or_b64 exec, exec, s[48:49]
	v_pk_mul_f32 v[118:119], v[100:101], v[100:101]
	v_pk_mul_f32 v[120:121], v[104:105], v[104:105]
	v_pk_fma_f32 v[118:119], v[98:99], v[98:99], v[118:119]
	v_cvt_pk_bf16_f32 v98, v98, v99
	v_cvt_pk_bf16_f32 v99, v100, v101
	v_cvt_pk_bf16_f32 v100, v102, v103
	v_cvt_pk_bf16_f32 v101, v104, v105
	ds_bpermute_b32 v232, v244, v98
	ds_bpermute_b32 v233, v244, v99
	ds_bpermute_b32 v234, v244, v100
	ds_bpermute_b32 v235, v244, v101
	ds_bpermute_b32 v236, v244, v116
	ds_bpermute_b32 v237, v244, v117
	v_pk_fma_f32 v[120:121], v[102:103], v[102:103], v[120:121]
	s_nop 0
	v_pk_mul_f32 v[98:99], v[108:109], v[108:109]
	v_pk_mul_f32 v[100:101], v[112:113], v[112:113]
	v_pk_fma_f32 v[98:99], v[106:107], v[106:107], v[98:99]
	v_pk_fma_f32 v[100:101], v[110:111], v[110:111], v[100:101]
	v_pk_add_f32 v[118:119], v[118:119], v[120:121]
	v_pk_add_f32 v[98:99], v[98:99], v[100:101]
	s_nop 0
	v_pk_add_f32 v[100:101], v[118:119], v[98:99]
	v_cvt_pk_bf16_f32 v98, v106, v107
	v_cvt_pk_bf16_f32 v99, v108, v109
	s_nop 0
	v_add_f32_e32 v102, v100, v101
	ds_swizzle_b32 v103, v102 offset:swizzle(SWAP,16)
	v_cvt_pk_bf16_f32 v100, v110, v111
	v_cvt_pk_bf16_f32 v101, v112, v113
	s_waitcnt lgkmcnt(0)
	global_store_dwordx4 v[236:237], v[232:235], off offset:2048
	ds_bpermute_b32 v238, v244, v98
	ds_bpermute_b32 v239, v244, v99
	ds_bpermute_b32 v240, v244, v100
	ds_bpermute_b32 v241, v244, v101
	ds_bpermute_b32 v242, v244, v116
	ds_bpermute_b32 v243, v244, v117
	s_waitcnt lgkmcnt(0)
	s_nop 0
	v_add_f32_e32 v98, v102, v103
	v_mov_b32_e32 v99, v98
	s_nop 1
	v_permlane32_swap_b32_e32 v98, v99
	s_waitcnt lgkmcnt(0)
	global_store_dwordx4 v[242:243], v[238:241], off offset:2112
	s_and_saveexec_b64 s[48:49], s[38:39]
	s_cbranch_execz .LBB0_1341
	v_or_b32_e32 v100, 16, v144
	v_ashrrev_i32_e32 v101, 31, v100
	v_add_f32_e32 v102, v98, v99
	v_lshlrev_b64 v[98:99], 7, v[100:101]
	v_lshl_add_u64 v[98:99], s[8:9], 0, v[98:99]
	v_lshl_add_u64 v[98:99], s[46:47], 2, v[98:99]
	s_lshl_b32 s24, s14, 2
	v_lshl_add_u64 v[98:99], v[98:99], 0, s[24:25]
	global_store_dword v[98:99], v102, off
.LBB0_1341:
	s_or_b64 exec, exec, s[48:49]
	v_pk_mul_f32 v[98:99], v[84:85], v[84:85]
	v_pk_mul_f32 v[100:101], v[92:93], v[92:93]
	v_pk_fma_f32 v[98:99], v[82:83], v[82:83], v[98:99]
	v_pk_fma_f32 v[100:101], v[90:91], v[90:91], v[100:101]
	s_nop 0
	v_pk_add_f32 v[102:103], v[98:99], v[100:101]
	v_cvt_pk_bf16_f32 v99, v84, v85
	v_cvt_pk_bf16_f32 v100, v90, v91
	v_pk_mul_f32 v[84:85], v[88:89], v[88:89]
	v_pk_mul_f32 v[90:91], v[96:97], v[96:97]
	v_pk_fma_f32 v[84:85], v[86:87], v[86:87], v[84:85]
	v_pk_fma_f32 v[90:91], v[94:95], v[94:95], v[90:91]
	v_cvt_pk_bf16_f32 v98, v82, v83
	v_add_co_u32_e32 v82, vcc, s73, v116
	v_pk_add_f32 v[84:85], v[84:85], v[90:91]
	s_nop 0
	v_addc_co_u32_e32 v83, vcc, 0, v117, vcc
	v_pk_add_f32 v[90:91], v[102:103], v[84:85]
	v_cvt_pk_bf16_f32 v84, v86, v87
	v_cvt_pk_bf16_f32 v85, v88, v89
	v_cvt_pk_bf16_f32 v86, v94, v95
	v_cvt_pk_bf16_f32 v87, v96, v97
	ds_bpermute_b32 v232, v244, v84
	ds_bpermute_b32 v233, v244, v85
	ds_bpermute_b32 v234, v244, v86
	ds_bpermute_b32 v235, v244, v87
	ds_bpermute_b32 v236, v244, v82
	ds_bpermute_b32 v237, v244, v83
	v_add_f32_e32 v90, v90, v91
	ds_swizzle_b32 v91, v90 offset:swizzle(SWAP,16)
	v_cvt_pk_bf16_f32 v101, v92, v93
	s_waitcnt lgkmcnt(0)
	global_store_dwordx4 v[236:237], v[232:235], off offset:64
	ds_bpermute_b32 v238, v244, v98
	ds_bpermute_b32 v239, v244, v99
	ds_bpermute_b32 v240, v244, v100
	ds_bpermute_b32 v241, v244, v101
	ds_bpermute_b32 v242, v244, v82
	ds_bpermute_b32 v243, v244, v83
	s_waitcnt lgkmcnt(0)
	v_add_f32_e32 v84, v90, v91
	v_mov_b32_e32 v85, v84
	s_nop 1
	v_permlane32_swap_b32_e32 v84, v85
	s_waitcnt lgkmcnt(0)
	global_store_dwordx4 v[242:243], v[238:241], off
	s_and_saveexec_b64 s[48:49], s[38:39]
	s_cbranch_execz .LBB0_1343
	v_or_b32_e32 v86, 32, v144
	v_ashrrev_i32_e32 v87, 31, v86
	v_add_f32_e32 v88, v84, v85
	v_lshlrev_b64 v[84:85], 7, v[86:87]
	v_lshl_add_u64 v[84:85], s[8:9], 0, v[84:85]
	v_lshl_add_u64 v[84:85], s[46:47], 2, v[84:85]
	s_lshl_b32 s24, s14, 2
	v_lshl_add_u64 v[84:85], v[84:85], 0, s[24:25]
	global_store_dword v[84:85], v88, off
.LBB0_1343:
	s_or_b64 exec, exec, s[48:49]
	v_pk_mul_f32 v[84:85], v[60:61], v[60:61]
	v_pk_mul_f32 v[86:87], v[72:73], v[72:73]
	v_pk_fma_f32 v[84:85], v[58:59], v[58:59], v[84:85]
	v_cvt_pk_bf16_f32 v58, v58, v59
	v_cvt_pk_bf16_f32 v59, v60, v61
	v_cvt_pk_bf16_f32 v60, v70, v71
	v_cvt_pk_bf16_f32 v61, v72, v73
	ds_bpermute_b32 v232, v244, v58
	ds_bpermute_b32 v233, v244, v59
	ds_bpermute_b32 v234, v244, v60
	ds_bpermute_b32 v235, v244, v61
	ds_bpermute_b32 v236, v244, v82
	ds_bpermute_b32 v237, v244, v83
	v_pk_fma_f32 v[86:87], v[70:71], v[70:71], v[86:87]
	s_nop 0
	v_pk_mul_f32 v[58:59], v[76:77], v[76:77]
	v_pk_mul_f32 v[60:61], v[80:81], v[80:81]
	v_pk_fma_f32 v[58:59], v[74:75], v[74:75], v[58:59]
	v_pk_fma_f32 v[60:61], v[78:79], v[78:79], v[60:61]
	v_pk_add_f32 v[84:85], v[84:85], v[86:87]
	v_pk_add_f32 v[58:59], v[58:59], v[60:61]
	s_nop 0
	v_pk_add_f32 v[60:61], v[84:85], v[58:59]
	v_cvt_pk_bf16_f32 v58, v74, v75
	v_cvt_pk_bf16_f32 v59, v76, v77
	s_nop 0
	v_add_f32_e32 v70, v60, v61
	ds_swizzle_b32 v71, v70 offset:swizzle(SWAP,16)
	v_cvt_pk_bf16_f32 v60, v78, v79
	v_cvt_pk_bf16_f32 v61, v80, v81
	s_waitcnt lgkmcnt(0)
	global_store_dwordx4 v[236:237], v[232:235], off offset:2048
	ds_bpermute_b32 v238, v244, v58
	ds_bpermute_b32 v239, v244, v59
	ds_bpermute_b32 v240, v244, v60
	ds_bpermute_b32 v241, v244, v61
	ds_bpermute_b32 v242, v244, v82
	ds_bpermute_b32 v243, v244, v83
	s_waitcnt lgkmcnt(0)
	s_nop 0
	v_add_f32_e32 v58, v70, v71
	v_mov_b32_e32 v59, v58
	s_nop 1
	v_permlane32_swap_b32_e32 v58, v59
	s_waitcnt lgkmcnt(0)
	global_store_dwordx4 v[242:243], v[238:241], off offset:2112
	s_and_saveexec_b64 s[48:49], s[38:39]
	s_cbranch_execz .LBB0_1345
	v_or_b32_e32 v60, 48, v144
	v_ashrrev_i32_e32 v61, 31, v60
	v_add_f32_e32 v70, v58, v59
	v_lshlrev_b64 v[58:59], 7, v[60:61]
	v_lshl_add_u64 v[58:59], s[8:9], 0, v[58:59]
	v_lshl_add_u64 v[58:59], s[46:47], 2, v[58:59]
	s_lshl_b32 s24, s14, 2
	v_lshl_add_u64 v[58:59], v[58:59], 0, s[24:25]
	global_store_dword v[58:59], v70, off
.LBB0_1345:
	s_or_b64 exec, exec, s[48:49]
	v_pk_mul_f32 v[58:59], v[52:53], v[52:53]
	v_pk_mul_f32 v[60:61], v[64:65], v[64:65]
	v_pk_fma_f32 v[58:59], v[50:51], v[50:51], v[58:59]
	v_pk_fma_f32 v[60:61], v[62:63], v[62:63], v[60:61]
	s_nop 0
	v_pk_add_f32 v[70:71], v[58:59], v[60:61]
	v_cvt_pk_bf16_f32 v58, v50, v51
	v_add_co_u32_e32 v50, vcc, s72, v116
	v_cvt_pk_bf16_f32 v59, v52, v53
	v_cvt_pk_bf16_f32 v60, v62, v63
	v_cvt_pk_bf16_f32 v61, v64, v65
	v_pk_mul_f32 v[52:53], v[56:57], v[56:57]
	s_nop 0
	v_addc_co_u32_e32 v51, vcc, 0, v117, vcc
	ds_bpermute_b32 v232, v244, v58
	ds_bpermute_b32 v233, v244, v59
	ds_bpermute_b32 v234, v244, v60
	ds_bpermute_b32 v235, v244, v61
	ds_bpermute_b32 v236, v244, v50
	ds_bpermute_b32 v237, v244, v51
	v_pk_fma_f32 v[52:53], v[54:55], v[54:55], v[52:53]
	s_nop 0
	v_pk_mul_f32 v[58:59], v[68:69], v[68:69]
	s_nop 0
	v_pk_fma_f32 v[58:59], v[66:67], v[66:67], v[58:59]
	s_nop 0
	v_pk_add_f32 v[52:53], v[52:53], v[58:59]
	s_nop 0
	v_pk_add_f32 v[58:59], v[70:71], v[52:53]
	v_cvt_pk_bf16_f32 v52, v54, v55
	v_cvt_pk_bf16_f32 v53, v56, v57
	v_cvt_pk_bf16_f32 v54, v66, v67
	v_cvt_pk_bf16_f32 v55, v68, v69
	s_waitcnt lgkmcnt(0)
	global_store_dwordx4 v[236:237], v[232:235], off
	ds_bpermute_b32 v238, v244, v52
	ds_bpermute_b32 v239, v244, v53
	ds_bpermute_b32 v240, v244, v54
	ds_bpermute_b32 v241, v244, v55
	ds_bpermute_b32 v242, v244, v50
	ds_bpermute_b32 v243, v244, v51
	v_add_f32_e32 v58, v58, v59
	ds_swizzle_b32 v59, v58 offset:swizzle(SWAP,16)
	s_waitcnt lgkmcnt(0)
	v_add_f32_e32 v52, v58, v59
	v_mov_b32_e32 v53, v52
	s_nop 1
	v_permlane32_swap_b32_e32 v52, v53
	s_waitcnt lgkmcnt(0)
	global_store_dwordx4 v[242:243], v[238:241], off offset:64
	s_and_saveexec_b64 s[48:49], s[38:39]
	s_cbranch_execz .LBB0_1347
	v_ashrrev_i32_e32 v145, 31, v144
	v_add_f32_e32 v54, v52, v53
	v_lshlrev_b64 v[52:53], 7, v[144:145]
	v_lshl_add_u64 v[52:53], s[8:9], 0, v[52:53]
	v_lshl_add_u64 v[52:53], s[46:47], 2, v[52:53]
	s_lshl_b32 s24, s14, 2
	v_lshl_add_u64 v[52:53], v[52:53], 0, s[24:25]
	v_add_co_u32_e32 v52, vcc, 0x4000, v52
	s_nop 1
	v_addc_co_u32_e32 v53, vcc, 0, v53, vcc
	global_store_dword v[52:53], v54, off
.LBB0_1347:
	s_or_b64 exec, exec, s[48:49]
	v_pk_mul_f32 v[52:53], v[36:37], v[36:37]
	v_pk_mul_f32 v[54:55], v[40:41], v[40:41]
	v_pk_fma_f32 v[52:53], v[34:35], v[34:35], v[52:53]
	v_cvt_pk_bf16_f32 v34, v34, v35
	v_cvt_pk_bf16_f32 v35, v36, v37
	v_cvt_pk_bf16_f32 v36, v38, v39
	v_cvt_pk_bf16_f32 v37, v40, v41
	ds_bpermute_b32 v232, v244, v34
	ds_bpermute_b32 v233, v244, v35
	ds_bpermute_b32 v234, v244, v36
	ds_bpermute_b32 v235, v244, v37
	ds_bpermute_b32 v236, v244, v50
	ds_bpermute_b32 v237, v244, v51
	v_pk_fma_f32 v[54:55], v[38:39], v[38:39], v[54:55]
	s_nop 0
	v_pk_mul_f32 v[34:35], v[44:45], v[44:45]
	v_pk_mul_f32 v[36:37], v[48:49], v[48:49]
	v_pk_fma_f32 v[34:35], v[42:43], v[42:43], v[34:35]
	v_pk_fma_f32 v[36:37], v[46:47], v[46:47], v[36:37]
	v_pk_add_f32 v[52:53], v[52:53], v[54:55]
	v_pk_add_f32 v[34:35], v[34:35], v[36:37]
	s_nop 0
	v_pk_add_f32 v[36:37], v[52:53], v[34:35]
	v_cvt_pk_bf16_f32 v34, v42, v43
	v_cvt_pk_bf16_f32 v35, v44, v45
	s_nop 0
	v_add_f32_e32 v38, v36, v37
	ds_swizzle_b32 v39, v38 offset:swizzle(SWAP,16)
	v_cvt_pk_bf16_f32 v36, v46, v47
	v_cvt_pk_bf16_f32 v37, v48, v49
	s_waitcnt lgkmcnt(0)
	global_store_dwordx4 v[236:237], v[232:235], off offset:2048
	ds_bpermute_b32 v238, v244, v34
	ds_bpermute_b32 v239, v244, v35
	ds_bpermute_b32 v240, v244, v36
	ds_bpermute_b32 v241, v244, v37
	ds_bpermute_b32 v242, v244, v50
	ds_bpermute_b32 v243, v244, v51
	s_waitcnt lgkmcnt(0)
	s_nop 0
	v_add_f32_e32 v34, v38, v39
	v_mov_b32_e32 v35, v34
	s_nop 1
	v_permlane32_swap_b32_e32 v34, v35
	s_waitcnt lgkmcnt(0)
	global_store_dwordx4 v[242:243], v[238:241], off offset:2112
	s_and_saveexec_b64 s[48:49], s[38:39]
	s_cbranch_execz .LBB0_1349
	v_ashrrev_i32_e32 v145, 31, v144
	v_add_f32_e32 v36, v34, v35
	v_lshlrev_b64 v[34:35], 7, v[144:145]
	v_lshl_add_u64 v[34:35], s[8:9], 0, v[34:35]
	v_lshl_add_u64 v[34:35], s[46:47], 2, v[34:35]
	s_lshl_b32 s24, s14, 2
	v_lshl_add_u64 v[34:35], v[34:35], 0, s[24:25]
	v_add_co_u32_e32 v34, vcc, 0x4000, v34
	s_nop 1
	v_addc_co_u32_e32 v35, vcc, 0, v35, vcc
	global_store_dword v[34:35], v36, off offset:2048
.LBB0_1349:
	s_or_b64 exec, exec, s[48:49]
	v_pk_mul_f32 v[34:35], v[20:21], v[20:21]
	v_pk_mul_f32 v[36:37], v[28:29], v[28:29]
	v_pk_fma_f32 v[34:35], v[18:19], v[18:19], v[34:35]
	v_pk_fma_f32 v[36:37], v[26:27], v[26:27], v[36:37]
	s_nop 0
	v_pk_add_f32 v[38:39], v[34:35], v[36:37]
	v_cvt_pk_bf16_f32 v35, v20, v21
	v_cvt_pk_bf16_f32 v36, v26, v27
	v_pk_mul_f32 v[20:21], v[24:25], v[24:25]
	v_pk_mul_f32 v[26:27], v[32:33], v[32:33]
	v_pk_fma_f32 v[20:21], v[22:23], v[22:23], v[20:21]
	v_pk_fma_f32 v[26:27], v[30:31], v[30:31], v[26:27]
	v_cvt_pk_bf16_f32 v34, v18, v19
	v_add_co_u32_e32 v18, vcc, s31, v116
	v_pk_add_f32 v[20:21], v[20:21], v[26:27]
	s_nop 0
	v_addc_co_u32_e32 v19, vcc, 0, v117, vcc
	v_pk_add_f32 v[26:27], v[38:39], v[20:21]
	v_cvt_pk_bf16_f32 v20, v22, v23
	v_cvt_pk_bf16_f32 v21, v24, v25
	v_cvt_pk_bf16_f32 v22, v30, v31
	v_cvt_pk_bf16_f32 v23, v32, v33
	ds_bpermute_b32 v232, v244, v20
	ds_bpermute_b32 v233, v244, v21
	ds_bpermute_b32 v234, v244, v22
	ds_bpermute_b32 v235, v244, v23
	ds_bpermute_b32 v236, v244, v18
	ds_bpermute_b32 v237, v244, v19
	v_add_f32_e32 v26, v26, v27
	ds_swizzle_b32 v27, v26 offset:swizzle(SWAP,16)
	v_cvt_pk_bf16_f32 v37, v28, v29
	s_waitcnt lgkmcnt(0)
	global_store_dwordx4 v[236:237], v[232:235], off offset:64
	ds_bpermute_b32 v238, v244, v34
	ds_bpermute_b32 v239, v244, v35
	ds_bpermute_b32 v240, v244, v36
	ds_bpermute_b32 v241, v244, v37
	ds_bpermute_b32 v242, v244, v18
	ds_bpermute_b32 v243, v244, v19
	s_waitcnt lgkmcnt(0)
	v_add_f32_e32 v20, v26, v27
	v_mov_b32_e32 v21, v20
	s_nop 1
	v_permlane32_swap_b32_e32 v20, v21
	s_waitcnt lgkmcnt(0)
	global_store_dwordx4 v[242:243], v[238:241], off
	s_and_saveexec_b64 s[48:49], s[38:39]
	s_cbranch_execz .LBB0_1351
	v_ashrrev_i32_e32 v145, 31, v144
	v_add_f32_e32 v22, v20, v21
	v_lshlrev_b64 v[20:21], 7, v[144:145]
	v_lshl_add_u64 v[20:21], s[8:9], 0, v[20:21]
	v_lshl_add_u64 v[20:21], s[46:47], 2, v[20:21]
	s_lshl_b32 s24, s14, 2
	v_lshl_add_u64 v[20:21], v[20:21], 0, s[24:25]
	v_add_co_u32_e32 v20, vcc, 0x5000, v20
	s_nop 1
	v_addc_co_u32_e32 v21, vcc, 0, v21, vcc
	global_store_dword v[20:21], v22, off
.LBB0_1351:
	s_or_b64 exec, exec, s[48:49]
	v_pk_mul_f32 v[20:21], v[4:5], v[4:5]
	v_pk_mul_f32 v[22:23], v[8:9], v[8:9]
	v_pk_fma_f32 v[20:21], v[2:3], v[2:3], v[20:21]
	v_cvt_pk_bf16_f32 v2, v2, v3
	v_cvt_pk_bf16_f32 v3, v4, v5
	v_cvt_pk_bf16_f32 v4, v6, v7
	v_cvt_pk_bf16_f32 v5, v8, v9
	ds_bpermute_b32 v232, v244, v2
	ds_bpermute_b32 v233, v244, v3
	ds_bpermute_b32 v234, v244, v4
	ds_bpermute_b32 v235, v244, v5
	ds_bpermute_b32 v236, v244, v18
	ds_bpermute_b32 v237, v244, v19
	v_pk_fma_f32 v[22:23], v[6:7], v[6:7], v[22:23]
	s_nop 0
	v_pk_mul_f32 v[2:3], v[12:13], v[12:13]
	v_pk_mul_f32 v[4:5], v[16:17], v[16:17]
	v_pk_fma_f32 v[2:3], v[10:11], v[10:11], v[2:3]
	v_pk_fma_f32 v[4:5], v[14:15], v[14:15], v[4:5]
	v_pk_add_f32 v[20:21], v[20:21], v[22:23]
	v_pk_add_f32 v[2:3], v[2:3], v[4:5]
	s_nop 0
	v_pk_add_f32 v[4:5], v[20:21], v[2:3]
	v_cvt_pk_bf16_f32 v2, v10, v11
	v_cvt_pk_bf16_f32 v3, v12, v13
	s_nop 0
	v_add_f32_e32 v6, v4, v5
	ds_swizzle_b32 v7, v6 offset:swizzle(SWAP,16)
	v_cvt_pk_bf16_f32 v4, v14, v15
	v_cvt_pk_bf16_f32 v5, v16, v17
	s_waitcnt lgkmcnt(0)
	global_store_dwordx4 v[236:237], v[232:235], off offset:2048
	ds_bpermute_b32 v238, v244, v2
	ds_bpermute_b32 v239, v244, v3
	ds_bpermute_b32 v240, v244, v4
	ds_bpermute_b32 v241, v244, v5
	ds_bpermute_b32 v242, v244, v18
	ds_bpermute_b32 v243, v244, v19
	s_waitcnt lgkmcnt(0)
	s_nop 0
	v_add_f32_e32 v2, v6, v7
	v_mov_b32_e32 v3, v2
	s_nop 1
	v_permlane32_swap_b32_e32 v2, v3
	s_waitcnt lgkmcnt(0)
	global_store_dwordx4 v[242:243], v[238:241], off offset:2112
	s_and_saveexec_b64 s[48:49], s[38:39]
	s_cbranch_execz .LBB0_1353
	v_ashrrev_i32_e32 v145, 31, v144
	v_add_f32_e32 v4, v2, v3
	v_lshlrev_b64 v[2:3], 7, v[144:145]
	v_lshl_add_u64 v[2:3], s[8:9], 0, v[2:3]
	v_lshl_add_u64 v[2:3], s[46:47], 2, v[2:3]
	s_lshl_b32 s24, s14, 2
	v_lshl_add_u64 v[2:3], v[2:3], 0, s[24:25]
	v_add_co_u32_e32 v2, vcc, 0x5000, v2
	s_nop 1
	v_addc_co_u32_e32 v3, vcc, 0, v3, vcc
	global_store_dword v[2:3], v4, off offset:2048
